# GEMM tiles: first K-loop iteration peeled so the first MFMA of every accumulator takes C=0 - the 128 accumulator-zeroing v_mov per tile are gone; on top of v024
# speedup vs baseline: 1.0136x; 1.0136x over previous
.LBB0_260:
	s_ashr_i32 s69, s68, 31
	s_lshl_b64 s[26:27], s[68:69], 20
	v_readlane_b32 s8, v254, 56
	v_readlane_b32 s9, v254, 57
	s_add_u32 s70, s8, s26
	s_addc_u32 s71, s9, s27
	s_and_b64 s[26:27], s[0:1], exec
	s_cselect_b32 s69, s71, s83
	s_cselect_b32 s75, s70, s82
	s_ashr_i32 s57, s56, 31
	s_lshl_b64 s[26:27], s[56:57], 20
	s_add_u32 s72, s84, s26
	s_addc_u32 s73, s85, s27
	s_and_b64 s[26:27], s[0:1], exec
	s_cselect_b32 s57, s73, s81
	s_cselect_b32 s96, s72, s80
	s_add_u32 s97, s80, 0x10000
	s_addc_u32 vcc_lo, s81, 0
	s_add_u32 s80, s82, 0x80080
	s_addc_u32 s81, s83, 0
	s_mov_b32 vcc_hi, -2
	ds_read_b128 v[144:147], v170
	ds_read_b128 v[148:151], v170 offset:1024
	ds_read_b128 v[174:177], v170 offset:2048
	ds_read_b128 v[178:181], v170 offset:3072
	ds_read_b128 v[182:185], v171
	ds_read_b128 v[186:189], v171 offset:1024
	ds_read_b128 v[190:193], v171 offset:2048
	ds_read_b128 v[194:197], v171 offset:3072
	s_add_u32 s26, s80, 0xfff80080
	s_addc_u32 s27, s81, -1
	s_cmp_eq_u32 vcc_hi, 28
	s_cselect_b32 s83, s69, s27
	s_cselect_b32 s82, s75, s26
	s_cselect_b32 s27, s57, vcc_lo
	s_cselect_b32 s26, s96, s97
	v_lshl_add_u64 v[152:153], s[80:81], 0, v[134:135]
	s_add_i32 m0, s87, 0xc000
	ds_read_b128 v[198:201], v172
	ds_read_b128 v[202:205], v172 offset:1024
	ds_read_b128 v[206:209], v172 offset:2048
	ds_read_b128 v[210:213], v172 offset:3072
	ds_read_b128 v[214:217], v172 offset:4096
	ds_read_b128 v[220:223], v172 offset:5120
	ds_read_b128 v[224:227], v172 offset:6144
	ds_read_b128 v[228:231], v172 offset:7168
	global_load_lds_dwordx4 v[152:153], off
	v_lshl_add_u64 v[152:153], s[80:81], 0, v[138:139]
	s_add_i32 m0, s87, 0xe000
	s_nop 0
	global_load_lds_dwordx4 v[152:153], off
	s_waitcnt vmcnt(8)
	s_waitcnt lgkmcnt(0)
	s_barrier
	s_waitcnt lgkmcnt(0)
	v_mfma_f32_16x16x32_bf16 v[122:125], v[144:147], v[198:201], 0
	v_mfma_f32_16x16x32_bf16 v[118:121], v[174:177], v[198:201], 0
	v_mfma_f32_16x16x32_bf16 v[106:109], v[144:147], v[206:209], 0
	v_mfma_f32_16x16x32_bf16 v[102:105], v[174:177], v[206:209], 0
	v_mfma_f32_16x16x32_bf16 v[90:93], v[144:147], v[214:217], 0
	v_mfma_f32_16x16x32_bf16 v[86:89], v[174:177], v[214:217], 0
	v_mfma_f32_16x16x32_bf16 v[74:77], v[144:147], v[224:227], 0
	v_mfma_f32_16x16x32_bf16 v[70:73], v[174:177], v[224:227], 0
	v_mfma_f32_16x16x32_bf16 v[122:125], v[148:151], v[202:205], v[122:125]
	v_mfma_f32_16x16x32_bf16 v[118:121], v[178:181], v[202:205], v[118:121]
	v_mfma_f32_16x16x32_bf16 v[106:109], v[148:151], v[210:213], v[106:109]
	v_mfma_f32_16x16x32_bf16 v[102:105], v[178:181], v[210:213], v[102:105]
	v_mfma_f32_16x16x32_bf16 v[90:93], v[148:151], v[220:223], v[90:93]
	v_mfma_f32_16x16x32_bf16 v[86:89], v[178:181], v[220:223], v[86:89]
	v_mfma_f32_16x16x32_bf16 v[74:77], v[148:151], v[228:231], v[74:77]
	v_mfma_f32_16x16x32_bf16 v[70:73], v[178:181], v[228:231], v[70:73]
	v_mfma_f32_16x16x32_bf16 v[126:129], v[182:185], v[198:201], 0
	v_mfma_f32_16x16x32_bf16 v[114:117], v[190:193], v[198:201], 0
	v_mfma_f32_16x16x32_bf16 v[110:113], v[182:185], v[206:209], 0
	v_mfma_f32_16x16x32_bf16 v[98:101], v[190:193], v[206:209], 0
	v_mfma_f32_16x16x32_bf16 v[94:97], v[182:185], v[214:217], 0
	v_mfma_f32_16x16x32_bf16 v[82:85], v[190:193], v[214:217], 0
	v_mfma_f32_16x16x32_bf16 v[78:81], v[182:185], v[224:227], 0
	v_mfma_f32_16x16x32_bf16 v[66:69], v[190:193], v[224:227], 0
	v_mfma_f32_16x16x32_bf16 v[126:129], v[186:189], v[202:205], v[126:129]
	v_mfma_f32_16x16x32_bf16 v[114:117], v[194:197], v[202:205], v[114:117]
	v_mfma_f32_16x16x32_bf16 v[110:113], v[186:189], v[210:213], v[110:113]
	v_mfma_f32_16x16x32_bf16 v[98:101], v[194:197], v[210:213], v[98:101]
	v_mfma_f32_16x16x32_bf16 v[94:97], v[186:189], v[220:223], v[94:97]
	v_mfma_f32_16x16x32_bf16 v[82:85], v[194:197], v[220:223], v[82:85]
	v_mfma_f32_16x16x32_bf16 v[78:81], v[186:189], v[228:231], v[78:81]
	v_mfma_f32_16x16x32_bf16 v[66:69], v[194:197], v[228:231], v[66:69]
	s_barrier
	v_lshl_add_u64 v[152:153], s[26:27], 0, v[162:163]
	s_add_i32 s26, s94, s86
	s_mov_b32 m0, s26
	ds_read_b128 v[198:201], v172 offset:16384
	ds_read_b128 v[202:205], v172 offset:17408
	ds_read_b128 v[206:209], v172 offset:18432
	ds_read_b128 v[210:213], v172 offset:19456
	ds_read_b128 v[214:217], v172 offset:20480
	ds_read_b128 v[220:223], v172 offset:21504
	ds_read_b128 v[224:227], v172 offset:22528
	ds_read_b128 v[228:231], v172 offset:23552
	global_load_lds_dwordx4 v[152:153], off
	v_lshl_add_u64 v[232:233], v[152:153], 0, s[10:11]
	s_add_i32 m0, s26, 0x2000
	s_add_i32 s26, s95, s86
	global_load_lds_dwordx4 v[232:233], off
	v_lshl_add_u64 v[232:233], v[152:153], 0, s[12:13]
	s_mov_b32 m0, s26
	v_lshl_add_u64 v[234:235], s[82:83], 0, v[132:133]
	global_load_lds_dwordx4 v[232:233], off
	v_lshl_add_u64 v[232:233], v[152:153], 0, s[14:15]
	s_add_i32 m0, s26, 0x2000
	s_nop 0
	global_load_lds_dwordx4 v[232:233], off
	v_lshl_add_u64 v[232:233], s[82:83], 0, v[130:131]
	s_mov_b32 m0, s87
	s_nop 0
	global_load_lds_dwordx4 v[232:233], off
	s_mov_b32 m0, s88
	s_nop 0
	global_load_lds_dwordx4 v[234:235], off
	s_waitcnt vmcnt(8)
	s_waitcnt lgkmcnt(0)
	s_barrier
	s_waitcnt lgkmcnt(0)
	v_mfma_f32_16x16x32_bf16 v[58:61], v[144:147], v[198:201], 0
	v_mfma_f32_16x16x32_bf16 v[54:57], v[174:177], v[198:201], 0
	v_mfma_f32_16x16x32_bf16 v[42:45], v[144:147], v[206:209], 0
	v_mfma_f32_16x16x32_bf16 v[38:41], v[174:177], v[206:209], 0
	v_mfma_f32_16x16x32_bf16 v[26:29], v[144:147], v[214:217], 0
	v_mfma_f32_16x16x32_bf16 v[22:25], v[174:177], v[214:217], 0
	v_mfma_f32_16x16x32_bf16 v[10:13], v[144:147], v[224:227], 0
	v_mfma_f32_16x16x32_bf16 v[6:9], v[174:177], v[224:227], 0
	v_mfma_f32_16x16x32_bf16 v[58:61], v[148:151], v[202:205], v[58:61]
	v_mfma_f32_16x16x32_bf16 v[54:57], v[178:181], v[202:205], v[54:57]
	v_mfma_f32_16x16x32_bf16 v[42:45], v[148:151], v[210:213], v[42:45]
	v_mfma_f32_16x16x32_bf16 v[38:41], v[178:181], v[210:213], v[38:41]
	v_mfma_f32_16x16x32_bf16 v[26:29], v[148:151], v[220:223], v[26:29]
	v_mfma_f32_16x16x32_bf16 v[22:25], v[178:181], v[220:223], v[22:25]
	v_mfma_f32_16x16x32_bf16 v[10:13], v[148:151], v[228:231], v[10:13]
	v_mfma_f32_16x16x32_bf16 v[6:9], v[178:181], v[228:231], v[6:9]
	v_mfma_f32_16x16x32_bf16 v[62:65], v[182:185], v[198:201], 0
	v_mfma_f32_16x16x32_bf16 v[50:53], v[190:193], v[198:201], 0
	v_mfma_f32_16x16x32_bf16 v[46:49], v[182:185], v[206:209], 0
	v_mfma_f32_16x16x32_bf16 v[34:37], v[190:193], v[206:209], 0
	v_mfma_f32_16x16x32_bf16 v[30:33], v[182:185], v[214:217], 0
	v_mfma_f32_16x16x32_bf16 v[18:21], v[190:193], v[214:217], 0
	v_mfma_f32_16x16x32_bf16 v[14:17], v[182:185], v[224:227], 0
	v_mfma_f32_16x16x32_bf16 v[2:5], v[190:193], v[224:227], 0
	v_mfma_f32_16x16x32_bf16 v[62:65], v[186:189], v[202:205], v[62:65]
	v_mfma_f32_16x16x32_bf16 v[50:53], v[194:197], v[202:205], v[50:53]
	v_mfma_f32_16x16x32_bf16 v[46:49], v[186:189], v[210:213], v[46:49]
	v_mfma_f32_16x16x32_bf16 v[34:37], v[194:197], v[210:213], v[34:37]
	v_mfma_f32_16x16x32_bf16 v[30:33], v[186:189], v[220:223], v[30:33]
	v_mfma_f32_16x16x32_bf16 v[18:21], v[194:197], v[220:223], v[18:21]
	v_mfma_f32_16x16x32_bf16 v[14:17], v[186:189], v[228:231], v[14:17]
	v_mfma_f32_16x16x32_bf16 v[2:5], v[194:197], v[228:231], v[2:5]
	s_barrier
	s_add_i32 s33, 0, 0x18000
	v_add_u32_e32 v136, s33, v167
	s_add_i32 s8, 0, 0x1c000
	ds_read_b128 v[144:147], v136
	ds_read_b128 v[148:151], v136 offset:1024
	ds_read_b128 v[174:177], v136 offset:2048
	ds_read_b128 v[178:181], v136 offset:3072
	v_add_u32_e32 v136, s8, v167
	ds_read_b128 v[182:185], v136
	ds_read_b128 v[186:189], v136 offset:1024
	ds_read_b128 v[190:193], v136 offset:2048
	ds_read_b128 v[194:197], v136 offset:3072
	s_add_u32 s26, s82, 0x80000
	s_addc_u32 s27, s83, 0
	s_mov_b32 m0, s89
	v_lshl_add_u64 v[236:237], s[26:27], 0, v[130:131]
	ds_read_b128 v[198:201], v172 offset:32768
	ds_read_b128 v[202:205], v172 offset:33792
	ds_read_b128 v[206:209], v172 offset:34816
	ds_read_b128 v[210:213], v172 offset:35840
	ds_read_b128 v[214:217], v172 offset:36864
	ds_read_b128 v[220:223], v172 offset:37888
	ds_read_b128 v[224:227], v172 offset:38912
	ds_read_b128 v[228:231], v172 offset:39936
	global_load_lds_dwordx4 v[236:237], off
	v_lshl_add_u64 v[236:237], s[26:27], 0, v[132:133]
	s_mov_b32 m0, s90
	s_nop 0
	global_load_lds_dwordx4 v[236:237], off
	s_waitcnt vmcnt(8)
	s_waitcnt lgkmcnt(0)
	s_barrier
	s_waitcnt lgkmcnt(0)
	v_mfma_f32_16x16x32_bf16 v[122:125], v[144:147], v[198:201], v[122:125]
	v_mfma_f32_16x16x32_bf16 v[118:121], v[174:177], v[198:201], v[118:121]
	v_mfma_f32_16x16x32_bf16 v[106:109], v[144:147], v[206:209], v[106:109]
	v_mfma_f32_16x16x32_bf16 v[102:105], v[174:177], v[206:209], v[102:105]
	v_mfma_f32_16x16x32_bf16 v[90:93], v[144:147], v[214:217], v[90:93]
	v_mfma_f32_16x16x32_bf16 v[86:89], v[174:177], v[214:217], v[86:89]
	v_mfma_f32_16x16x32_bf16 v[74:77], v[144:147], v[224:227], v[74:77]
	v_mfma_f32_16x16x32_bf16 v[70:73], v[174:177], v[224:227], v[70:73]
	v_mfma_f32_16x16x32_bf16 v[122:125], v[148:151], v[202:205], v[122:125]
	v_mfma_f32_16x16x32_bf16 v[118:121], v[178:181], v[202:205], v[118:121]
	v_mfma_f32_16x16x32_bf16 v[106:109], v[148:151], v[210:213], v[106:109]
	v_mfma_f32_16x16x32_bf16 v[102:105], v[178:181], v[210:213], v[102:105]
	v_mfma_f32_16x16x32_bf16 v[90:93], v[148:151], v[220:223], v[90:93]
	v_mfma_f32_16x16x32_bf16 v[86:89], v[178:181], v[220:223], v[86:89]
	v_mfma_f32_16x16x32_bf16 v[74:77], v[148:151], v[228:231], v[74:77]
	v_mfma_f32_16x16x32_bf16 v[70:73], v[178:181], v[228:231], v[70:73]
	v_mfma_f32_16x16x32_bf16 v[126:129], v[182:185], v[198:201], v[126:129]
	v_mfma_f32_16x16x32_bf16 v[114:117], v[190:193], v[198:201], v[114:117]
	v_mfma_f32_16x16x32_bf16 v[110:113], v[182:185], v[206:209], v[110:113]
	v_mfma_f32_16x16x32_bf16 v[98:101], v[190:193], v[206:209], v[98:101]
	v_mfma_f32_16x16x32_bf16 v[94:97], v[182:185], v[214:217], v[94:97]
	v_mfma_f32_16x16x32_bf16 v[82:85], v[190:193], v[214:217], v[82:85]
	v_mfma_f32_16x16x32_bf16 v[78:81], v[182:185], v[224:227], v[78:81]
	v_mfma_f32_16x16x32_bf16 v[66:69], v[190:193], v[224:227], v[66:69]
	v_mfma_f32_16x16x32_bf16 v[126:129], v[186:189], v[202:205], v[126:129]
	v_mfma_f32_16x16x32_bf16 v[114:117], v[194:197], v[202:205], v[114:117]
	v_mfma_f32_16x16x32_bf16 v[110:113], v[186:189], v[210:213], v[110:113]
	v_mfma_f32_16x16x32_bf16 v[98:101], v[194:197], v[210:213], v[98:101]
	v_mfma_f32_16x16x32_bf16 v[94:97], v[186:189], v[220:223], v[94:97]
	v_mfma_f32_16x16x32_bf16 v[82:85], v[194:197], v[220:223], v[82:85]
	v_mfma_f32_16x16x32_bf16 v[78:81], v[186:189], v[228:231], v[78:81]
	v_mfma_f32_16x16x32_bf16 v[66:69], v[194:197], v[228:231], v[66:69]
	s_barrier
	s_add_i32 s9, s33, s86
	v_lshl_add_u64 v[236:237], v[152:153], 0, s[20:21]
	s_mov_b32 m0, s9
	ds_read_b128 v[198:201], v172 offset:49152
	ds_read_b128 v[202:205], v172 offset:50176
	ds_read_b128 v[206:209], v172 offset:51200
	ds_read_b128 v[210:213], v172 offset:52224
	ds_read_b128 v[214:217], v172 offset:53248
	ds_read_b128 v[220:223], v172 offset:54272
	ds_read_b128 v[224:227], v172 offset:55296
	ds_read_b128 v[228:231], v172 offset:56320
	global_load_lds_dwordx4 v[236:237], off
	v_lshl_add_u64 v[236:237], v[152:153], 0, s[22:23]
	s_add_i32 m0, s9, 0x2000
	s_add_i32 s8, s8, s86
	global_load_lds_dwordx4 v[236:237], off
	v_lshl_add_u64 v[236:237], v[152:153], 0, s[40:41]
	s_mov_b32 m0, s8
	v_lshl_add_u64 v[152:153], v[152:153], 0, s[44:45]
	global_load_lds_dwordx4 v[236:237], off
	s_add_i32 m0, s8, 0x2000
	s_nop 0
	global_load_lds_dwordx4 v[152:153], off
	v_lshl_add_u64 v[152:153], v[232:233], 0, s[24:25]
	s_mov_b32 m0, s91
	s_nop 0
	global_load_lds_dwordx4 v[152:153], off
	v_lshl_add_u64 v[152:153], v[234:235], 0, s[24:25]
	s_mov_b32 m0, s92
	s_nop 0
	global_load_lds_dwordx4 v[152:153], off
	s_waitcnt vmcnt(8)
	s_waitcnt lgkmcnt(0)
	s_barrier
	s_waitcnt lgkmcnt(0)
	v_mfma_f32_16x16x32_bf16 v[58:61], v[144:147], v[198:201], v[58:61]
	v_mfma_f32_16x16x32_bf16 v[54:57], v[174:177], v[198:201], v[54:57]
	v_mfma_f32_16x16x32_bf16 v[42:45], v[144:147], v[206:209], v[42:45]
	v_mfma_f32_16x16x32_bf16 v[38:41], v[174:177], v[206:209], v[38:41]
	v_mfma_f32_16x16x32_bf16 v[26:29], v[144:147], v[214:217], v[26:29]
	v_mfma_f32_16x16x32_bf16 v[22:25], v[174:177], v[214:217], v[22:25]
	v_mfma_f32_16x16x32_bf16 v[10:13], v[144:147], v[224:227], v[10:13]
	v_mfma_f32_16x16x32_bf16 v[6:9], v[174:177], v[224:227], v[6:9]
	v_mfma_f32_16x16x32_bf16 v[58:61], v[148:151], v[202:205], v[58:61]
	v_mfma_f32_16x16x32_bf16 v[54:57], v[178:181], v[202:205], v[54:57]
	v_mfma_f32_16x16x32_bf16 v[42:45], v[148:151], v[210:213], v[42:45]
	v_mfma_f32_16x16x32_bf16 v[38:41], v[178:181], v[210:213], v[38:41]
	v_mfma_f32_16x16x32_bf16 v[26:29], v[148:151], v[220:223], v[26:29]
	v_mfma_f32_16x16x32_bf16 v[22:25], v[178:181], v[220:223], v[22:25]
	v_mfma_f32_16x16x32_bf16 v[10:13], v[148:151], v[228:231], v[10:13]
	v_mfma_f32_16x16x32_bf16 v[6:9], v[178:181], v[228:231], v[6:9]
	v_mfma_f32_16x16x32_bf16 v[62:65], v[182:185], v[198:201], v[62:65]
	v_mfma_f32_16x16x32_bf16 v[50:53], v[190:193], v[198:201], v[50:53]
	v_mfma_f32_16x16x32_bf16 v[46:49], v[182:185], v[206:209], v[46:49]
	v_mfma_f32_16x16x32_bf16 v[34:37], v[190:193], v[206:209], v[34:37]
	v_mfma_f32_16x16x32_bf16 v[30:33], v[182:185], v[214:217], v[30:33]
	v_mfma_f32_16x16x32_bf16 v[18:21], v[190:193], v[214:217], v[18:21]
	v_mfma_f32_16x16x32_bf16 v[14:17], v[182:185], v[224:227], v[14:17]
	v_mfma_f32_16x16x32_bf16 v[2:5], v[190:193], v[224:227], v[2:5]
	v_mfma_f32_16x16x32_bf16 v[62:65], v[186:189], v[202:205], v[62:65]
	v_mfma_f32_16x16x32_bf16 v[50:53], v[194:197], v[202:205], v[50:53]
	v_mfma_f32_16x16x32_bf16 v[46:49], v[186:189], v[210:213], v[46:49]
	v_mfma_f32_16x16x32_bf16 v[34:37], v[194:197], v[210:213], v[34:37]
	v_mfma_f32_16x16x32_bf16 v[30:33], v[186:189], v[220:223], v[30:33]
	v_mfma_f32_16x16x32_bf16 v[18:21], v[194:197], v[220:223], v[18:21]
	v_mfma_f32_16x16x32_bf16 v[14:17], v[186:189], v[228:231], v[14:17]
	v_mfma_f32_16x16x32_bf16 v[2:5], v[194:197], v[228:231], v[2:5]
	s_barrier
	s_add_i32 vcc_hi, vcc_hi, 2
	s_add_u32 s97, s97, 0x10000
	s_addc_u32 vcc_lo, vcc_lo, 0
	s_add_u32 s80, s80, 0x100
	s_addc_u32 s81, s81, 0
	s_cmp_gt_u32 vcc_hi, 29

.LBB0_284:
	s_ashr_i32 s51, s50, 31
	s_lshl_b64 s[26:27], s[50:51], 19
	v_readlane_b32 s54, v254, 58
	v_readlane_b32 s55, v254, 59
	s_add_u32 s54, s54, s26
	s_addc_u32 s55, s55, s27
	s_and_b64 s[26:27], s[0:1], exec
	s_cselect_b32 s51, s55, s73
	s_cselect_b32 s90, s54, s72
	s_ashr_i32 s45, s44, 31
	s_lshl_b64 s[26:27], s[44:45], 19
	s_add_u32 s56, s81, s26
	s_addc_u32 s57, s82, s27
	s_and_b64 s[26:27], s[0:1], exec
	s_cselect_b32 s45, s57, s71
	s_cselect_b32 s91, s56, s70
	s_add_u32 s92, s70, 0x10000
	s_addc_u32 s93, s71, 0
	s_add_u32 s70, s72, 0x40080
	s_addc_u32 s71, s73, 0
	s_mov_b32 s94, -2
	ds_read_b128 v[26:29], v1
	ds_read_b128 v[30:33], v1 offset:1024
	ds_read_b128 v[18:21], v1 offset:2048
	ds_read_b128 v[22:25], v1 offset:3072
	ds_read_b128 v[10:13], v185
	ds_read_b128 v[14:17], v185 offset:1024
	ds_read_b128 v[2:5], v185 offset:2048
	ds_read_b128 v[6:9], v185 offset:3072
	s_add_u32 s26, s70, 0xfffc0080
	s_addc_u32 s27, s71, -1
	s_cmp_eq_u32 s94, 12
	s_cselect_b32 s73, s51, s27
	s_cselect_b32 s72, s90, s26
	s_cselect_b32 s75, s45, s93
	s_cselect_b32 s74, s91, s92
	v_lshl_add_u64 v[176:177], s[70:71], 0, v[168:169]
	s_add_i32 m0, s33, 0xc000
	ds_read_b128 v[190:193], v186
	ds_read_b128 v[194:197], v186 offset:1024
	ds_read_b128 v[198:201], v186 offset:2048
	ds_read_b128 v[202:205], v186 offset:3072
	ds_read_b128 v[206:209], v186 offset:4096
	ds_read_b128 v[210:213], v186 offset:5120
	ds_read_b128 v[220:223], v186 offset:6144
	ds_read_b128 v[224:227], v186 offset:7168
	global_load_lds_dwordx4 v[176:177], off
	v_lshl_add_u64 v[176:177], s[70:71], 0, v[170:171]
	s_add_i32 m0, s33, 0xe000
	s_nop 0
	global_load_lds_dwordx4 v[176:177], off
	s_waitcnt vmcnt(8)
	s_waitcnt lgkmcnt(0)
	s_barrier
	s_waitcnt lgkmcnt(0)
	v_mfma_scale_f32_16x16x128_f8f6f4 v[158:161], v[26:33], v[190:197], 0, v187, v188 op_sel_hi:[0,0,0]
	v_mfma_scale_f32_16x16x128_f8f6f4 v[154:157], v[18:25], v[190:197], 0, v187, v188 op_sel_hi:[0,0,0]
	v_mfma_scale_f32_16x16x128_f8f6f4 v[150:153], v[26:33], v[198:205], 0, v187, v188 op_sel_hi:[0,0,0]
	v_mfma_scale_f32_16x16x128_f8f6f4 v[142:145], v[18:25], v[198:205], 0, v187, v188 op_sel_hi:[0,0,0]
	v_mfma_scale_f32_16x16x128_f8f6f4 v[134:137], v[26:33], v[206:213], 0, v187, v188 op_sel_hi:[0,0,0]
	v_mfma_scale_f32_16x16x128_f8f6f4 v[126:129], v[18:25], v[206:213], 0, v187, v188 op_sel_hi:[0,0,0]
	v_mfma_scale_f32_16x16x128_f8f6f4 v[118:121], v[26:33], v[220:227], 0, v187, v188 op_sel_hi:[0,0,0]
	v_mfma_scale_f32_16x16x128_f8f6f4 v[110:113], v[18:25], v[220:227], 0, v187, v188 op_sel_hi:[0,0,0]
	v_mfma_scale_f32_16x16x128_f8f6f4 v[146:149], v[10:17], v[190:197], 0, v187, v188 op_sel_hi:[0,0,0]
	v_mfma_scale_f32_16x16x128_f8f6f4 v[138:141], v[2:9], v[190:197], 0, v187, v188 op_sel_hi:[0,0,0]
	v_mfma_scale_f32_16x16x128_f8f6f4 v[130:133], v[10:17], v[198:205], 0, v187, v188 op_sel_hi:[0,0,0]
	v_mfma_scale_f32_16x16x128_f8f6f4 v[122:125], v[2:9], v[198:205], 0, v187, v188 op_sel_hi:[0,0,0]
	v_mfma_scale_f32_16x16x128_f8f6f4 v[114:117], v[10:17], v[206:213], 0, v187, v188 op_sel_hi:[0,0,0]
	v_mfma_scale_f32_16x16x128_f8f6f4 v[106:109], v[2:9], v[206:213], 0, v187, v188 op_sel_hi:[0,0,0]
	v_mfma_scale_f32_16x16x128_f8f6f4 v[102:105], v[10:17], v[220:227], 0, v187, v188 op_sel_hi:[0,0,0]
	v_mfma_scale_f32_16x16x128_f8f6f4 v[98:101], v[2:9], v[220:227], 0, v187, v188 op_sel_hi:[0,0,0]
	s_barrier
	s_add_i32 s26, s88, s80
	v_lshl_add_u64 v[176:177], s[74:75], 0, v[162:163]
	s_mov_b32 m0, s26
	ds_read_b128 v[190:193], v186 offset:16384
	ds_read_b128 v[194:197], v186 offset:17408
	ds_read_b128 v[198:201], v186 offset:18432
	ds_read_b128 v[202:205], v186 offset:19456
	ds_read_b128 v[206:209], v186 offset:20480
	ds_read_b128 v[210:213], v186 offset:21504
	ds_read_b128 v[220:223], v186 offset:22528
	ds_read_b128 v[224:227], v186 offset:23552
	global_load_lds_dwordx4 v[176:177], off
	v_lshl_add_u64 v[178:179], v[176:177], 0, s[8:9]
	s_add_i32 m0, s26, 0x2000
	s_add_i32 s26, s89, s80
	global_load_lds_dwordx4 v[178:179], off
	v_lshl_add_u64 v[178:179], v[176:177], 0, s[10:11]
	s_mov_b32 m0, s26
	v_lshl_add_u64 v[180:181], s[72:73], 0, v[166:167]
	global_load_lds_dwordx4 v[178:179], off
	v_lshl_add_u64 v[178:179], v[176:177], 0, s[12:13]
	s_add_i32 m0, s26, 0x2000
	s_nop 0
	global_load_lds_dwordx4 v[178:179], off
	v_lshl_add_u64 v[178:179], s[72:73], 0, v[164:165]
	s_mov_b32 m0, s33
	s_nop 0
	global_load_lds_dwordx4 v[178:179], off
	s_mov_b32 m0, s69
	s_nop 0
	global_load_lds_dwordx4 v[180:181], off
	s_waitcnt vmcnt(8)
	s_waitcnt lgkmcnt(0)
	s_barrier
	s_waitcnt lgkmcnt(0)
	v_mfma_scale_f32_16x16x128_f8f6f4 v[94:97], v[26:33], v[190:197], 0, v187, v188 op_sel_hi:[0,0,0]
	v_mfma_scale_f32_16x16x128_f8f6f4 v[90:93], v[18:25], v[190:197], 0, v187, v188 op_sel_hi:[0,0,0]
	v_mfma_scale_f32_16x16x128_f8f6f4 v[86:89], v[26:33], v[198:205], 0, v187, v188 op_sel_hi:[0,0,0]
	v_mfma_scale_f32_16x16x128_f8f6f4 v[78:81], v[18:25], v[198:205], 0, v187, v188 op_sel_hi:[0,0,0]
	v_mfma_scale_f32_16x16x128_f8f6f4 v[70:73], v[26:33], v[206:213], 0, v187, v188 op_sel_hi:[0,0,0]
	v_mfma_scale_f32_16x16x128_f8f6f4 v[62:65], v[18:25], v[206:213], 0, v187, v188 op_sel_hi:[0,0,0]
	v_mfma_scale_f32_16x16x128_f8f6f4 v[54:57], v[26:33], v[220:227], 0, v187, v188 op_sel_hi:[0,0,0]
	v_mfma_scale_f32_16x16x128_f8f6f4 v[46:49], v[18:25], v[220:227], 0, v187, v188 op_sel_hi:[0,0,0]
	v_mfma_scale_f32_16x16x128_f8f6f4 v[82:85], v[10:17], v[190:197], 0, v187, v188 op_sel_hi:[0,0,0]
	v_mfma_scale_f32_16x16x128_f8f6f4 v[74:77], v[2:9], v[190:197], 0, v187, v188 op_sel_hi:[0,0,0]
	v_mfma_scale_f32_16x16x128_f8f6f4 v[66:69], v[10:17], v[198:205], 0, v187, v188 op_sel_hi:[0,0,0]
	v_mfma_scale_f32_16x16x128_f8f6f4 v[58:61], v[2:9], v[198:205], 0, v187, v188 op_sel_hi:[0,0,0]
	v_mfma_scale_f32_16x16x128_f8f6f4 v[50:53], v[10:17], v[206:213], 0, v187, v188 op_sel_hi:[0,0,0]
	v_mfma_scale_f32_16x16x128_f8f6f4 v[42:45], v[2:9], v[206:213], 0, v187, v188 op_sel_hi:[0,0,0]
	v_mfma_scale_f32_16x16x128_f8f6f4 v[38:41], v[10:17], v[220:227], 0, v187, v188 op_sel_hi:[0,0,0]
	v_mfma_scale_f32_16x16x128_f8f6f4 v[34:37], v[2:9], v[220:227], 0, v187, v188 op_sel_hi:[0,0,0]
	s_barrier
	s_add_i32 s74, 0, 0x18000
	s_add_i32 s75, 0, 0x1c000
	v_add_u32_e32 v14, s74, v183
	v_add_u32_e32 v30, s75, v183
	ds_read_b128 v[2:5], v14
	ds_read_b128 v[6:9], v14 offset:1024
	ds_read_b128 v[10:13], v14 offset:2048
	ds_read_b128 v[14:17], v14 offset:3072
	ds_read_b128 v[18:21], v30
	ds_read_b128 v[22:25], v30 offset:1024
	ds_read_b128 v[26:29], v30 offset:2048
	ds_read_b128 v[30:33], v30 offset:3072
	s_add_u32 s26, s72, 0x40000
	s_addc_u32 s27, s73, 0
	s_mov_b32 m0, s83
	v_lshl_add_u64 v[214:215], s[26:27], 0, v[164:165]
	ds_read_b128 v[190:193], v186 offset:32768
	ds_read_b128 v[194:197], v186 offset:33792
	ds_read_b128 v[198:201], v186 offset:34816
	ds_read_b128 v[202:205], v186 offset:35840
	ds_read_b128 v[206:209], v186 offset:36864
	ds_read_b128 v[210:213], v186 offset:37888
	ds_read_b128 v[220:223], v186 offset:38912
	ds_read_b128 v[224:227], v186 offset:39936
	global_load_lds_dwordx4 v[214:215], off
	v_lshl_add_u64 v[214:215], s[26:27], 0, v[166:167]
	s_mov_b32 m0, s84
	s_nop 0
	global_load_lds_dwordx4 v[214:215], off
	s_waitcnt vmcnt(8)
	s_waitcnt lgkmcnt(0)
	s_barrier
	s_waitcnt lgkmcnt(0)
	v_mfma_scale_f32_16x16x128_f8f6f4 v[158:161], v[2:9], v[190:197], v[158:161], v187, v188 op_sel_hi:[0,0,0]
	v_mfma_scale_f32_16x16x128_f8f6f4 v[154:157], v[10:17], v[190:197], v[154:157], v187, v188 op_sel_hi:[0,0,0]
	v_mfma_scale_f32_16x16x128_f8f6f4 v[150:153], v[2:9], v[198:205], v[150:153], v187, v188 op_sel_hi:[0,0,0]
	v_mfma_scale_f32_16x16x128_f8f6f4 v[142:145], v[10:17], v[198:205], v[142:145], v187, v188 op_sel_hi:[0,0,0]
	v_mfma_scale_f32_16x16x128_f8f6f4 v[134:137], v[2:9], v[206:213], v[134:137], v187, v188 op_sel_hi:[0,0,0]
	v_mfma_scale_f32_16x16x128_f8f6f4 v[126:129], v[10:17], v[206:213], v[126:129], v187, v188 op_sel_hi:[0,0,0]
	v_mfma_scale_f32_16x16x128_f8f6f4 v[118:121], v[2:9], v[220:227], v[118:121], v187, v188 op_sel_hi:[0,0,0]
	v_mfma_scale_f32_16x16x128_f8f6f4 v[110:113], v[10:17], v[220:227], v[110:113], v187, v188 op_sel_hi:[0,0,0]
	v_mfma_scale_f32_16x16x128_f8f6f4 v[146:149], v[18:25], v[190:197], v[146:149], v187, v188 op_sel_hi:[0,0,0]
	v_mfma_scale_f32_16x16x128_f8f6f4 v[138:141], v[26:33], v[190:197], v[138:141], v187, v188 op_sel_hi:[0,0,0]
	v_mfma_scale_f32_16x16x128_f8f6f4 v[130:133], v[18:25], v[198:205], v[130:133], v187, v188 op_sel_hi:[0,0,0]
	v_mfma_scale_f32_16x16x128_f8f6f4 v[122:125], v[26:33], v[198:205], v[122:125], v187, v188 op_sel_hi:[0,0,0]
	v_mfma_scale_f32_16x16x128_f8f6f4 v[114:117], v[18:25], v[206:213], v[114:117], v187, v188 op_sel_hi:[0,0,0]
	v_mfma_scale_f32_16x16x128_f8f6f4 v[106:109], v[26:33], v[206:213], v[106:109], v187, v188 op_sel_hi:[0,0,0]
	v_mfma_scale_f32_16x16x128_f8f6f4 v[102:105], v[18:25], v[220:227], v[102:105], v187, v188 op_sel_hi:[0,0,0]
	v_mfma_scale_f32_16x16x128_f8f6f4 v[98:101], v[26:33], v[220:227], v[98:101], v187, v188 op_sel_hi:[0,0,0]
	s_barrier
	s_add_i32 s26, s74, s80
	v_lshl_add_u64 v[214:215], v[176:177], 0, s[16:17]
	s_mov_b32 m0, s26
	ds_read_b128 v[190:193], v186 offset:49152
	ds_read_b128 v[194:197], v186 offset:50176
	ds_read_b128 v[198:201], v186 offset:51200
	ds_read_b128 v[202:205], v186 offset:52224
	ds_read_b128 v[206:209], v186 offset:53248
	ds_read_b128 v[210:213], v186 offset:54272
	ds_read_b128 v[220:223], v186 offset:55296
	ds_read_b128 v[224:227], v186 offset:56320
	global_load_lds_dwordx4 v[214:215], off
	v_lshl_add_u64 v[214:215], v[176:177], 0, s[18:19]
	s_add_i32 m0, s26, 0x2000
	s_add_i32 s26, s75, s80
	global_load_lds_dwordx4 v[214:215], off
	v_lshl_add_u64 v[214:215], v[176:177], 0, s[22:23]
	s_mov_b32 m0, s26
	v_lshl_add_u64 v[176:177], v[176:177], 0, s[24:25]
	global_load_lds_dwordx4 v[214:215], off
	s_add_i32 m0, s26, 0x2000
	s_nop 0
	global_load_lds_dwordx4 v[176:177], off
	v_lshl_add_u64 v[176:177], v[178:179], 0, s[20:21]
	s_mov_b32 m0, s86
	s_nop 0
	global_load_lds_dwordx4 v[176:177], off
	v_lshl_add_u64 v[176:177], v[180:181], 0, s[20:21]
	s_mov_b32 m0, s87
	s_nop 0
	global_load_lds_dwordx4 v[176:177], off
	s_waitcnt vmcnt(8)
	s_waitcnt lgkmcnt(0)
	s_barrier
	s_waitcnt lgkmcnt(0)
	v_mfma_scale_f32_16x16x128_f8f6f4 v[94:97], v[2:9], v[190:197], v[94:97], v187, v188 op_sel_hi:[0,0,0]
	v_mfma_scale_f32_16x16x128_f8f6f4 v[90:93], v[10:17], v[190:197], v[90:93], v187, v188 op_sel_hi:[0,0,0]
	v_mfma_scale_f32_16x16x128_f8f6f4 v[86:89], v[2:9], v[198:205], v[86:89], v187, v188 op_sel_hi:[0,0,0]
	v_mfma_scale_f32_16x16x128_f8f6f4 v[78:81], v[10:17], v[198:205], v[78:81], v187, v188 op_sel_hi:[0,0,0]
	v_mfma_scale_f32_16x16x128_f8f6f4 v[70:73], v[2:9], v[206:213], v[70:73], v187, v188 op_sel_hi:[0,0,0]
	v_mfma_scale_f32_16x16x128_f8f6f4 v[62:65], v[10:17], v[206:213], v[62:65], v187, v188 op_sel_hi:[0,0,0]
	v_mfma_scale_f32_16x16x128_f8f6f4 v[54:57], v[2:9], v[220:227], v[54:57], v187, v188 op_sel_hi:[0,0,0]
	v_mfma_scale_f32_16x16x128_f8f6f4 v[46:49], v[10:17], v[220:227], v[46:49], v187, v188 op_sel_hi:[0,0,0]
	v_mfma_scale_f32_16x16x128_f8f6f4 v[82:85], v[18:25], v[190:197], v[82:85], v187, v188 op_sel_hi:[0,0,0]
	v_mfma_scale_f32_16x16x128_f8f6f4 v[74:77], v[26:33], v[190:197], v[74:77], v187, v188 op_sel_hi:[0,0,0]
	v_mfma_scale_f32_16x16x128_f8f6f4 v[66:69], v[18:25], v[198:205], v[66:69], v187, v188 op_sel_hi:[0,0,0]
	v_mfma_scale_f32_16x16x128_f8f6f4 v[58:61], v[26:33], v[198:205], v[58:61], v187, v188 op_sel_hi:[0,0,0]
	v_mfma_scale_f32_16x16x128_f8f6f4 v[50:53], v[18:25], v[206:213], v[50:53], v187, v188 op_sel_hi:[0,0,0]
	v_mfma_scale_f32_16x16x128_f8f6f4 v[42:45], v[26:33], v[206:213], v[42:45], v187, v188 op_sel_hi:[0,0,0]
	v_mfma_scale_f32_16x16x128_f8f6f4 v[38:41], v[18:25], v[220:227], v[38:41], v187, v188 op_sel_hi:[0,0,0]
	v_mfma_scale_f32_16x16x128_f8f6f4 v[34:37], v[26:33], v[220:227], v[34:37], v187, v188 op_sel_hi:[0,0,0]
	s_barrier
	s_add_i32 s94, s94, 2
	s_add_u32 s92, s92, 0x10000
	s_addc_u32 s93, s93, 0
	s_add_u32 s70, s70, 0x100
	s_addc_u32 s71, s71, 0
	s_cmp_gt_u32 s94, 13

.LBB0_659:
	s_ashr_i32 s45, s44, 31
	s_lshl_b64 s[26:27], s[44:45], 20
	v_readlane_b32 s50, v254, 58
	v_readlane_b32 s51, v254, 59
	s_add_u32 s50, s50, s26
	s_addc_u32 s51, s51, s27
	s_and_b64 s[26:27], s[0:1], exec
	s_cselect_b32 s45, s51, s61
	s_cselect_b32 s72, s50, s60
	s_ashr_i32 s41, s40, 31
	s_lshl_b64 s[26:27], s[40:41], 20
	s_add_u32 s54, s3, s26
	s_addc_u32 s55, s33, s27
	s_and_b64 s[26:27], s[0:1], exec
	s_cselect_b32 s41, s55, s59
	s_cselect_b32 s73, s54, s58
	s_add_u32 s74, s58, 0x10000
	s_addc_u32 s75, s59, 0
	s_add_u32 s58, s60, 0x80080
	s_addc_u32 s59, s61, 0
	s_mov_b32 s80, -2
	ds_read_b128 v[130:133], v222
	ds_read_b128 v[134:137], v222 offset:1024
	ds_read_b128 v[138:141], v222 offset:2048
	ds_read_b128 v[142:145], v222 offset:3072
	ds_read_b128 v[146:149], v223
	ds_read_b128 v[150:153], v223 offset:1024
	ds_read_b128 v[154:157], v223 offset:2048
	ds_read_b128 v[158:161], v223 offset:3072
	s_add_u32 s26, s58, 0xfff80080
	s_addc_u32 s27, s59, -1
	s_cmp_eq_u32 s80, 28
	s_cselect_b32 s61, s45, s27
	s_cselect_b32 s60, s72, s26
	s_cselect_b32 s27, s41, s75
	s_cselect_b32 s26, s73, s74
	v_lshl_add_u64 v[208:209], s[58:59], 0, v[200:201]
	s_add_i32 m0, s57, 0xc000
	ds_read_b128 v[162:165], v224
	ds_read_b128 v[166:169], v224 offset:1024
	ds_read_b128 v[170:173], v224 offset:2048
	ds_read_b128 v[174:177], v224 offset:3072
	ds_read_b128 v[178:181], v224 offset:4096
	ds_read_b128 v[182:185], v224 offset:5120
	ds_read_b128 v[186:189], v224 offset:6144
	ds_read_b128 v[190:193], v224 offset:7168
	global_load_lds_dwordx4 v[208:209], off
	v_lshl_add_u64 v[208:209], s[58:59], 0, v[202:203]
	s_add_i32 m0, s57, 0xe000
	s_nop 0
	global_load_lds_dwordx4 v[208:209], off
	s_waitcnt vmcnt(8)
	s_waitcnt lgkmcnt(0)
	s_barrier
	s_waitcnt lgkmcnt(0)
	v_mfma_f32_16x16x32_bf16 v[126:129], v[130:133], v[162:165], 0
	v_mfma_f32_16x16x32_bf16 v[122:125], v[138:141], v[162:165], 0
	v_mfma_f32_16x16x32_bf16 v[118:121], v[130:133], v[170:173], 0
	v_mfma_f32_16x16x32_bf16 v[114:117], v[138:141], v[170:173], 0
	v_mfma_f32_16x16x32_bf16 v[110:113], v[130:133], v[178:181], 0
	v_mfma_f32_16x16x32_bf16 v[102:105], v[138:141], v[178:181], 0
	v_mfma_f32_16x16x32_bf16 v[94:97], v[130:133], v[186:189], 0
	v_mfma_f32_16x16x32_bf16 v[74:77], v[138:141], v[186:189], 0
	v_mfma_f32_16x16x32_bf16 v[126:129], v[134:137], v[166:169], v[126:129]
	v_mfma_f32_16x16x32_bf16 v[122:125], v[142:145], v[166:169], v[122:125]
	v_mfma_f32_16x16x32_bf16 v[118:121], v[134:137], v[174:177], v[118:121]
	v_mfma_f32_16x16x32_bf16 v[114:117], v[142:145], v[174:177], v[114:117]
	v_mfma_f32_16x16x32_bf16 v[110:113], v[134:137], v[182:185], v[110:113]
	v_mfma_f32_16x16x32_bf16 v[102:105], v[142:145], v[182:185], v[102:105]
	v_mfma_f32_16x16x32_bf16 v[94:97], v[134:137], v[190:193], v[94:97]
	v_mfma_f32_16x16x32_bf16 v[74:77], v[142:145], v[190:193], v[74:77]
	v_mfma_f32_16x16x32_bf16 v[106:109], v[146:149], v[162:165], 0
	v_mfma_f32_16x16x32_bf16 v[98:101], v[154:157], v[162:165], 0
	v_mfma_f32_16x16x32_bf16 v[90:93], v[146:149], v[170:173], 0
	v_mfma_f32_16x16x32_bf16 v[86:89], v[154:157], v[170:173], 0
	v_mfma_f32_16x16x32_bf16 v[82:85], v[146:149], v[178:181], 0
	v_mfma_f32_16x16x32_bf16 v[78:81], v[154:157], v[178:181], 0
	v_mfma_f32_16x16x32_bf16 v[70:73], v[146:149], v[186:189], 0
	v_mfma_f32_16x16x32_bf16 v[66:69], v[154:157], v[186:189], 0
	v_mfma_f32_16x16x32_bf16 v[106:109], v[150:153], v[166:169], v[106:109]
	v_mfma_f32_16x16x32_bf16 v[98:101], v[158:161], v[166:169], v[98:101]
	v_mfma_f32_16x16x32_bf16 v[90:93], v[150:153], v[174:177], v[90:93]
	v_mfma_f32_16x16x32_bf16 v[86:89], v[158:161], v[174:177], v[86:89]
	v_mfma_f32_16x16x32_bf16 v[82:85], v[150:153], v[182:185], v[82:85]
	v_mfma_f32_16x16x32_bf16 v[78:81], v[158:161], v[182:185], v[78:81]
	v_mfma_f32_16x16x32_bf16 v[70:73], v[150:153], v[190:193], v[70:73]
	v_mfma_f32_16x16x32_bf16 v[66:69], v[158:161], v[190:193], v[66:69]
	s_barrier
	v_lshl_add_u64 v[208:209], s[26:27], 0, v[194:195]
	s_add_i32 s26, s70, s35
	s_mov_b32 m0, s26
	ds_read_b128 v[162:165], v224 offset:16384
	ds_read_b128 v[166:169], v224 offset:17408
	ds_read_b128 v[170:173], v224 offset:18432
	ds_read_b128 v[174:177], v224 offset:19456
	ds_read_b128 v[178:181], v224 offset:20480
	ds_read_b128 v[182:185], v224 offset:21504
	ds_read_b128 v[186:189], v224 offset:22528
	ds_read_b128 v[190:193], v224 offset:23552
	global_load_lds_dwordx4 v[208:209], off
	v_lshl_add_u64 v[210:211], v[208:209], 0, s[6:7]
	s_add_i32 m0, s26, 0x2000
	s_add_i32 s26, s71, s35
	global_load_lds_dwordx4 v[210:211], off
	v_lshl_add_u64 v[210:211], v[208:209], 0, s[8:9]
	s_mov_b32 m0, s26
	v_lshl_add_u64 v[212:213], s[60:61], 0, v[198:199]
	global_load_lds_dwordx4 v[210:211], off
	v_lshl_add_u64 v[210:211], v[208:209], 0, s[10:11]
	s_add_i32 m0, s26, 0x2000
	s_nop 0
	global_load_lds_dwordx4 v[210:211], off
	v_lshl_add_u64 v[210:211], s[60:61], 0, v[196:197]
	s_mov_b32 m0, s57
	s_nop 0
	global_load_lds_dwordx4 v[210:211], off
	s_mov_b32 m0, s63
	s_nop 0
	global_load_lds_dwordx4 v[212:213], off
	s_waitcnt vmcnt(8)
	s_waitcnt lgkmcnt(0)
	s_barrier
	s_waitcnt lgkmcnt(0)
	v_mfma_f32_16x16x32_bf16 v[62:65], v[130:133], v[162:165], 0
	v_mfma_f32_16x16x32_bf16 v[58:61], v[138:141], v[162:165], 0
	v_mfma_f32_16x16x32_bf16 v[54:57], v[130:133], v[170:173], 0
	v_mfma_f32_16x16x32_bf16 v[50:53], v[138:141], v[170:173], 0
	v_mfma_f32_16x16x32_bf16 v[46:49], v[130:133], v[178:181], 0
	v_mfma_f32_16x16x32_bf16 v[38:41], v[138:141], v[178:181], 0
	v_mfma_f32_16x16x32_bf16 v[30:33], v[130:133], v[186:189], 0
	v_mfma_f32_16x16x32_bf16 v[10:13], v[138:141], v[186:189], 0
	v_mfma_f32_16x16x32_bf16 v[62:65], v[134:137], v[166:169], v[62:65]
	v_mfma_f32_16x16x32_bf16 v[58:61], v[142:145], v[166:169], v[58:61]
	v_mfma_f32_16x16x32_bf16 v[54:57], v[134:137], v[174:177], v[54:57]
	v_mfma_f32_16x16x32_bf16 v[50:53], v[142:145], v[174:177], v[50:53]
	v_mfma_f32_16x16x32_bf16 v[46:49], v[134:137], v[182:185], v[46:49]
	v_mfma_f32_16x16x32_bf16 v[38:41], v[142:145], v[182:185], v[38:41]
	v_mfma_f32_16x16x32_bf16 v[30:33], v[134:137], v[190:193], v[30:33]
	v_mfma_f32_16x16x32_bf16 v[10:13], v[142:145], v[190:193], v[10:13]
	v_mfma_f32_16x16x32_bf16 v[42:45], v[146:149], v[162:165], 0
	v_mfma_f32_16x16x32_bf16 v[34:37], v[154:157], v[162:165], 0
	v_mfma_f32_16x16x32_bf16 v[26:29], v[146:149], v[170:173], 0
	v_mfma_f32_16x16x32_bf16 v[22:25], v[154:157], v[170:173], 0
	v_mfma_f32_16x16x32_bf16 v[18:21], v[146:149], v[178:181], 0
	v_mfma_f32_16x16x32_bf16 v[14:17], v[154:157], v[178:181], 0
	v_mfma_f32_16x16x32_bf16 v[6:9], v[146:149], v[186:189], 0
	v_mfma_f32_16x16x32_bf16 v[2:5], v[154:157], v[186:189], 0
	v_mfma_f32_16x16x32_bf16 v[42:45], v[150:153], v[166:169], v[42:45]
	v_mfma_f32_16x16x32_bf16 v[34:37], v[158:161], v[166:169], v[34:37]
	v_mfma_f32_16x16x32_bf16 v[26:29], v[150:153], v[174:177], v[26:29]
	v_mfma_f32_16x16x32_bf16 v[22:25], v[158:161], v[174:177], v[22:25]
	v_mfma_f32_16x16x32_bf16 v[18:21], v[150:153], v[182:185], v[18:21]
	v_mfma_f32_16x16x32_bf16 v[14:17], v[158:161], v[182:185], v[14:17]
	v_mfma_f32_16x16x32_bf16 v[6:9], v[150:153], v[190:193], v[6:9]
	v_mfma_f32_16x16x32_bf16 v[2:5], v[158:161], v[190:193], v[2:5]
	s_barrier
	s_add_i32 s81, 0, 0x18000
	s_add_i32 s82, 0, 0x1c000
	v_add_u32_e32 v142, s81, v220
	v_add_u32_e32 v158, s82, v220
	ds_read_b128 v[130:133], v142
	ds_read_b128 v[134:137], v142 offset:1024
	ds_read_b128 v[138:141], v142 offset:2048
	ds_read_b128 v[142:145], v142 offset:3072
	ds_read_b128 v[146:149], v158
	ds_read_b128 v[150:153], v158 offset:1024
	ds_read_b128 v[154:157], v158 offset:2048
	ds_read_b128 v[158:161], v158 offset:3072
	s_add_u32 s26, s60, 0x80000
	s_addc_u32 s27, s61, 0
	s_mov_b32 m0, s64
	v_lshl_add_u64 v[214:215], s[26:27], 0, v[196:197]
	ds_read_b128 v[162:165], v224 offset:32768
	ds_read_b128 v[166:169], v224 offset:33792
	ds_read_b128 v[170:173], v224 offset:34816
	ds_read_b128 v[174:177], v224 offset:35840
	ds_read_b128 v[178:181], v224 offset:36864
	ds_read_b128 v[182:185], v224 offset:37888
	ds_read_b128 v[186:189], v224 offset:38912
	ds_read_b128 v[190:193], v224 offset:39936
	global_load_lds_dwordx4 v[214:215], off
	v_lshl_add_u64 v[214:215], s[26:27], 0, v[198:199]
	s_mov_b32 m0, s65
	s_nop 0
	global_load_lds_dwordx4 v[214:215], off
	s_waitcnt vmcnt(8)
	s_waitcnt lgkmcnt(0)
	s_barrier
	s_waitcnt lgkmcnt(0)
	v_mfma_f32_16x16x32_bf16 v[126:129], v[130:133], v[162:165], v[126:129]
	v_mfma_f32_16x16x32_bf16 v[122:125], v[138:141], v[162:165], v[122:125]
	v_mfma_f32_16x16x32_bf16 v[118:121], v[130:133], v[170:173], v[118:121]
	v_mfma_f32_16x16x32_bf16 v[114:117], v[138:141], v[170:173], v[114:117]
	v_mfma_f32_16x16x32_bf16 v[110:113], v[130:133], v[178:181], v[110:113]
	v_mfma_f32_16x16x32_bf16 v[102:105], v[138:141], v[178:181], v[102:105]
	v_mfma_f32_16x16x32_bf16 v[94:97], v[130:133], v[186:189], v[94:97]
	v_mfma_f32_16x16x32_bf16 v[74:77], v[138:141], v[186:189], v[74:77]
	v_mfma_f32_16x16x32_bf16 v[126:129], v[134:137], v[166:169], v[126:129]
	v_mfma_f32_16x16x32_bf16 v[122:125], v[142:145], v[166:169], v[122:125]
	v_mfma_f32_16x16x32_bf16 v[118:121], v[134:137], v[174:177], v[118:121]
	v_mfma_f32_16x16x32_bf16 v[114:117], v[142:145], v[174:177], v[114:117]
	v_mfma_f32_16x16x32_bf16 v[110:113], v[134:137], v[182:185], v[110:113]
	v_mfma_f32_16x16x32_bf16 v[102:105], v[142:145], v[182:185], v[102:105]
	v_mfma_f32_16x16x32_bf16 v[94:97], v[134:137], v[190:193], v[94:97]
	v_mfma_f32_16x16x32_bf16 v[74:77], v[142:145], v[190:193], v[74:77]
	v_mfma_f32_16x16x32_bf16 v[106:109], v[146:149], v[162:165], v[106:109]
	v_mfma_f32_16x16x32_bf16 v[98:101], v[154:157], v[162:165], v[98:101]
	v_mfma_f32_16x16x32_bf16 v[90:93], v[146:149], v[170:173], v[90:93]
	v_mfma_f32_16x16x32_bf16 v[86:89], v[154:157], v[170:173], v[86:89]
	v_mfma_f32_16x16x32_bf16 v[82:85], v[146:149], v[178:181], v[82:85]
	v_mfma_f32_16x16x32_bf16 v[78:81], v[154:157], v[178:181], v[78:81]
	v_mfma_f32_16x16x32_bf16 v[70:73], v[146:149], v[186:189], v[70:73]
	v_mfma_f32_16x16x32_bf16 v[66:69], v[154:157], v[186:189], v[66:69]
	v_mfma_f32_16x16x32_bf16 v[106:109], v[150:153], v[166:169], v[106:109]
	v_mfma_f32_16x16x32_bf16 v[98:101], v[158:161], v[166:169], v[98:101]
	v_mfma_f32_16x16x32_bf16 v[90:93], v[150:153], v[174:177], v[90:93]
	v_mfma_f32_16x16x32_bf16 v[86:89], v[158:161], v[174:177], v[86:89]
	v_mfma_f32_16x16x32_bf16 v[82:85], v[150:153], v[182:185], v[82:85]
	v_mfma_f32_16x16x32_bf16 v[78:81], v[158:161], v[182:185], v[78:81]
	v_mfma_f32_16x16x32_bf16 v[70:73], v[150:153], v[190:193], v[70:73]
	v_mfma_f32_16x16x32_bf16 v[66:69], v[158:161], v[190:193], v[66:69]
	s_barrier
	s_add_i32 s26, s81, s35
	v_lshl_add_u64 v[214:215], v[208:209], 0, s[14:15]
	s_mov_b32 m0, s26
	ds_read_b128 v[162:165], v224 offset:49152
	ds_read_b128 v[166:169], v224 offset:50176
	ds_read_b128 v[170:173], v224 offset:51200
	ds_read_b128 v[174:177], v224 offset:52224
	ds_read_b128 v[178:181], v224 offset:53248
	ds_read_b128 v[182:185], v224 offset:54272
	ds_read_b128 v[186:189], v224 offset:55296
	ds_read_b128 v[190:193], v224 offset:56320
	global_load_lds_dwordx4 v[214:215], off
	v_lshl_add_u64 v[214:215], v[208:209], 0, s[16:17]
	s_add_i32 m0, s26, 0x2000
	s_add_i32 s26, s82, s35
	global_load_lds_dwordx4 v[214:215], off
	v_lshl_add_u64 v[214:215], v[208:209], 0, s[20:21]
	s_mov_b32 m0, s26
	v_lshl_add_u64 v[208:209], v[208:209], 0, s[22:23]
	global_load_lds_dwordx4 v[214:215], off
	s_add_i32 m0, s26, 0x2000
	s_nop 0
	global_load_lds_dwordx4 v[208:209], off
	v_lshl_add_u64 v[208:209], v[210:211], 0, s[18:19]
	s_mov_b32 m0, s67
	s_nop 0
	global_load_lds_dwordx4 v[208:209], off
	v_lshl_add_u64 v[208:209], v[212:213], 0, s[18:19]
	s_mov_b32 m0, s68
	s_nop 0
	global_load_lds_dwordx4 v[208:209], off
	s_waitcnt vmcnt(8)
	s_waitcnt lgkmcnt(0)
	s_barrier
	s_waitcnt lgkmcnt(0)
	v_mfma_f32_16x16x32_bf16 v[62:65], v[130:133], v[162:165], v[62:65]
	v_mfma_f32_16x16x32_bf16 v[58:61], v[138:141], v[162:165], v[58:61]
	v_mfma_f32_16x16x32_bf16 v[54:57], v[130:133], v[170:173], v[54:57]
	v_mfma_f32_16x16x32_bf16 v[50:53], v[138:141], v[170:173], v[50:53]
	v_mfma_f32_16x16x32_bf16 v[46:49], v[130:133], v[178:181], v[46:49]
	v_mfma_f32_16x16x32_bf16 v[38:41], v[138:141], v[178:181], v[38:41]
	v_mfma_f32_16x16x32_bf16 v[30:33], v[130:133], v[186:189], v[30:33]
	v_mfma_f32_16x16x32_bf16 v[10:13], v[138:141], v[186:189], v[10:13]
	v_mfma_f32_16x16x32_bf16 v[62:65], v[134:137], v[166:169], v[62:65]
	v_mfma_f32_16x16x32_bf16 v[58:61], v[142:145], v[166:169], v[58:61]
	v_mfma_f32_16x16x32_bf16 v[54:57], v[134:137], v[174:177], v[54:57]
	v_mfma_f32_16x16x32_bf16 v[50:53], v[142:145], v[174:177], v[50:53]
	v_mfma_f32_16x16x32_bf16 v[46:49], v[134:137], v[182:185], v[46:49]
	v_mfma_f32_16x16x32_bf16 v[38:41], v[142:145], v[182:185], v[38:41]
	v_mfma_f32_16x16x32_bf16 v[30:33], v[134:137], v[190:193], v[30:33]
	v_mfma_f32_16x16x32_bf16 v[10:13], v[142:145], v[190:193], v[10:13]
	v_mfma_f32_16x16x32_bf16 v[42:45], v[146:149], v[162:165], v[42:45]
	v_mfma_f32_16x16x32_bf16 v[34:37], v[154:157], v[162:165], v[34:37]
	v_mfma_f32_16x16x32_bf16 v[26:29], v[146:149], v[170:173], v[26:29]
	v_mfma_f32_16x16x32_bf16 v[22:25], v[154:157], v[170:173], v[22:25]
	v_mfma_f32_16x16x32_bf16 v[18:21], v[146:149], v[178:181], v[18:21]
	v_mfma_f32_16x16x32_bf16 v[14:17], v[154:157], v[178:181], v[14:17]
	v_mfma_f32_16x16x32_bf16 v[6:9], v[146:149], v[186:189], v[6:9]
	v_mfma_f32_16x16x32_bf16 v[2:5], v[154:157], v[186:189], v[2:5]
	v_mfma_f32_16x16x32_bf16 v[42:45], v[150:153], v[166:169], v[42:45]
	v_mfma_f32_16x16x32_bf16 v[34:37], v[158:161], v[166:169], v[34:37]
	v_mfma_f32_16x16x32_bf16 v[26:29], v[150:153], v[174:177], v[26:29]
	v_mfma_f32_16x16x32_bf16 v[22:25], v[158:161], v[174:177], v[22:25]
	v_mfma_f32_16x16x32_bf16 v[18:21], v[150:153], v[182:185], v[18:21]
	v_mfma_f32_16x16x32_bf16 v[14:17], v[158:161], v[182:185], v[14:17]
	v_mfma_f32_16x16x32_bf16 v[6:9], v[150:153], v[190:193], v[6:9]
	v_mfma_f32_16x16x32_bf16 v[2:5], v[158:161], v[190:193], v[2:5]
	s_barrier
	s_add_i32 s80, s80, 2
	s_add_u32 s74, s74, 0x10000
	s_addc_u32 s75, s75, 0
	s_add_u32 s58, s58, 0x100
	s_addc_u32 s59, s59, 0
	s_cmp_gt_u32 s80, 29

.LBB0_782:
	s_ashr_i32 s55, s54, 31
	s_lshl_b64 s[26:27], s[54:55], 20
	v_readlane_b32 s56, v254, 56
	v_readlane_b32 s57, v254, 57
	s_add_u32 s56, s56, s26
	s_addc_u32 s57, s57, s27
	s_and_b64 s[26:27], s[0:1], exec
	s_cselect_b32 s55, s57, s65
	s_cselect_b32 s81, s56, s64
	s_ashr_i32 s53, s52, 31
	s_lshl_b64 s[26:27], s[52:53], 20
	s_add_u32 s58, s3, s26
	s_addc_u32 s59, s33, s27
	s_and_b64 s[26:27], s[0:1], exec
	s_cselect_b32 s53, s59, s63
	s_cselect_b32 s82, s58, s62
	s_add_u32 s83, s62, 0x10000
	s_addc_u32 s84, s63, 0
	s_add_u32 s62, s64, 0x80080
	s_addc_u32 s63, s65, 0
	s_mov_b32 s85, -2
	ds_read_b128 v[144:147], v151
	ds_read_b128 v[156:159], v151 offset:1024
	ds_read_b128 v[160:163], v151 offset:2048
	ds_read_b128 v[164:167], v151 offset:3072
	ds_read_b128 v[168:171], v152
	ds_read_b128 v[172:175], v152 offset:1024
	ds_read_b128 v[176:179], v152 offset:2048
	ds_read_b128 v[180:183], v152 offset:3072
	s_add_u32 s26, s62, 0xfff80080
	s_addc_u32 s27, s63, -1
	s_cmp_eq_u32 s85, 28
	s_cselect_b32 s65, s55, s27
	s_cselect_b32 s64, s81, s26
	s_cselect_b32 s27, s53, s84
	s_cselect_b32 s26, s82, s83
	v_lshl_add_u64 v[216:217], s[62:63], 0, v[136:137]
	s_add_i32 m0, s61, 0xc000
	ds_read_b128 v[184:187], v153
	ds_read_b128 v[188:191], v153 offset:1024
	ds_read_b128 v[192:195], v153 offset:2048
	ds_read_b128 v[196:199], v153 offset:3072
	ds_read_b128 v[200:203], v153 offset:4096
	ds_read_b128 v[204:207], v153 offset:5120
	ds_read_b128 v[208:211], v153 offset:6144
	ds_read_b128 v[212:215], v153 offset:7168
	global_load_lds_dwordx4 v[216:217], off
	v_lshl_add_u64 v[216:217], s[62:63], 0, v[138:139]
	s_add_i32 m0, s61, 0xe000
	s_nop 0
	global_load_lds_dwordx4 v[216:217], off
	s_waitcnt vmcnt(8)
	s_waitcnt lgkmcnt(0)
	s_barrier
	s_waitcnt lgkmcnt(0)
	v_mfma_f32_16x16x32_bf16 v[126:129], v[144:147], v[184:187], 0
	v_mfma_f32_16x16x32_bf16 v[118:121], v[160:163], v[184:187], 0
	v_mfma_f32_16x16x32_bf16 v[110:113], v[144:147], v[192:195], 0
	v_mfma_f32_16x16x32_bf16 v[102:105], v[160:163], v[192:195], 0
	v_mfma_f32_16x16x32_bf16 v[94:97], v[144:147], v[200:203], 0
	v_mfma_f32_16x16x32_bf16 v[86:89], v[160:163], v[200:203], 0
	v_mfma_f32_16x16x32_bf16 v[78:81], v[144:147], v[208:211], 0
	v_mfma_f32_16x16x32_bf16 v[70:73], v[160:163], v[208:211], 0
	v_mfma_f32_16x16x32_bf16 v[126:129], v[156:159], v[188:191], v[126:129]
	v_mfma_f32_16x16x32_bf16 v[118:121], v[164:167], v[188:191], v[118:121]
	v_mfma_f32_16x16x32_bf16 v[110:113], v[156:159], v[196:199], v[110:113]
	v_mfma_f32_16x16x32_bf16 v[102:105], v[164:167], v[196:199], v[102:105]
	v_mfma_f32_16x16x32_bf16 v[94:97], v[156:159], v[204:207], v[94:97]
	v_mfma_f32_16x16x32_bf16 v[86:89], v[164:167], v[204:207], v[86:89]
	v_mfma_f32_16x16x32_bf16 v[78:81], v[156:159], v[212:215], v[78:81]
	v_mfma_f32_16x16x32_bf16 v[70:73], v[164:167], v[212:215], v[70:73]
	v_mfma_f32_16x16x32_bf16 v[122:125], v[168:171], v[184:187], 0
	v_mfma_f32_16x16x32_bf16 v[114:117], v[176:179], v[184:187], 0
	v_mfma_f32_16x16x32_bf16 v[106:109], v[168:171], v[192:195], 0
	v_mfma_f32_16x16x32_bf16 v[98:101], v[176:179], v[192:195], 0
	v_mfma_f32_16x16x32_bf16 v[90:93], v[168:171], v[200:203], 0
	v_mfma_f32_16x16x32_bf16 v[82:85], v[176:179], v[200:203], 0
	v_mfma_f32_16x16x32_bf16 v[74:77], v[168:171], v[208:211], 0
	v_mfma_f32_16x16x32_bf16 v[66:69], v[176:179], v[208:211], 0
	v_mfma_f32_16x16x32_bf16 v[122:125], v[172:175], v[188:191], v[122:125]
	v_mfma_f32_16x16x32_bf16 v[114:117], v[180:183], v[188:191], v[114:117]
	v_mfma_f32_16x16x32_bf16 v[106:109], v[172:175], v[196:199], v[106:109]
	v_mfma_f32_16x16x32_bf16 v[98:101], v[180:183], v[196:199], v[98:101]
	v_mfma_f32_16x16x32_bf16 v[90:93], v[172:175], v[204:207], v[90:93]
	v_mfma_f32_16x16x32_bf16 v[82:85], v[180:183], v[204:207], v[82:85]
	v_mfma_f32_16x16x32_bf16 v[74:77], v[172:175], v[212:215], v[74:77]
	v_mfma_f32_16x16x32_bf16 v[66:69], v[180:183], v[212:215], v[66:69]
	s_barrier
	v_lshl_add_u64 v[216:217], s[26:27], 0, v[130:131]
	s_add_i32 s26, s73, s35
	s_mov_b32 m0, s26
	ds_read_b128 v[184:187], v153 offset:16384
	ds_read_b128 v[188:191], v153 offset:17408
	ds_read_b128 v[192:195], v153 offset:18432
	ds_read_b128 v[196:199], v153 offset:19456
	ds_read_b128 v[200:203], v153 offset:20480
	ds_read_b128 v[204:207], v153 offset:21504
	ds_read_b128 v[208:211], v153 offset:22528
	ds_read_b128 v[212:215], v153 offset:23552
	global_load_lds_dwordx4 v[216:217], off
	v_lshl_add_u64 v[220:221], v[216:217], 0, s[6:7]
	s_add_i32 m0, s26, 0x2000
	s_add_i32 s26, s74, s35
	global_load_lds_dwordx4 v[220:221], off
	v_lshl_add_u64 v[220:221], v[216:217], 0, s[8:9]
	s_mov_b32 m0, s26
	v_lshl_add_u64 v[222:223], s[64:65], 0, v[134:135]
	global_load_lds_dwordx4 v[220:221], off
	v_lshl_add_u64 v[220:221], v[216:217], 0, s[10:11]
	s_add_i32 m0, s26, 0x2000
	s_nop 0
	global_load_lds_dwordx4 v[220:221], off
	v_lshl_add_u64 v[220:221], s[64:65], 0, v[132:133]
	s_mov_b32 m0, s61
	s_nop 0
	global_load_lds_dwordx4 v[220:221], off
	s_mov_b32 m0, s66
	s_nop 0
	global_load_lds_dwordx4 v[222:223], off
	s_waitcnt vmcnt(8)
	s_waitcnt lgkmcnt(0)
	s_barrier
	s_waitcnt lgkmcnt(0)
	v_mfma_f32_16x16x32_bf16 v[62:65], v[144:147], v[184:187], 0
	v_mfma_f32_16x16x32_bf16 v[54:57], v[160:163], v[184:187], 0
	v_mfma_f32_16x16x32_bf16 v[46:49], v[144:147], v[192:195], 0
	v_mfma_f32_16x16x32_bf16 v[38:41], v[160:163], v[192:195], 0
	v_mfma_f32_16x16x32_bf16 v[30:33], v[144:147], v[200:203], 0
	v_mfma_f32_16x16x32_bf16 v[22:25], v[160:163], v[200:203], 0
	v_mfma_f32_16x16x32_bf16 v[14:17], v[144:147], v[208:211], 0
	v_mfma_f32_16x16x32_bf16 v[6:9], v[160:163], v[208:211], 0
	v_mfma_f32_16x16x32_bf16 v[62:65], v[156:159], v[188:191], v[62:65]
	v_mfma_f32_16x16x32_bf16 v[54:57], v[164:167], v[188:191], v[54:57]
	v_mfma_f32_16x16x32_bf16 v[46:49], v[156:159], v[196:199], v[46:49]
	v_mfma_f32_16x16x32_bf16 v[38:41], v[164:167], v[196:199], v[38:41]
	v_mfma_f32_16x16x32_bf16 v[30:33], v[156:159], v[204:207], v[30:33]
	v_mfma_f32_16x16x32_bf16 v[22:25], v[164:167], v[204:207], v[22:25]
	v_mfma_f32_16x16x32_bf16 v[14:17], v[156:159], v[212:215], v[14:17]
	v_mfma_f32_16x16x32_bf16 v[6:9], v[164:167], v[212:215], v[6:9]
	v_mfma_f32_16x16x32_bf16 v[58:61], v[168:171], v[184:187], 0
	v_mfma_f32_16x16x32_bf16 v[50:53], v[176:179], v[184:187], 0
	v_mfma_f32_16x16x32_bf16 v[42:45], v[168:171], v[192:195], 0
	v_mfma_f32_16x16x32_bf16 v[34:37], v[176:179], v[192:195], 0
	v_mfma_f32_16x16x32_bf16 v[26:29], v[168:171], v[200:203], 0
	v_mfma_f32_16x16x32_bf16 v[18:21], v[176:179], v[200:203], 0
	v_mfma_f32_16x16x32_bf16 v[10:13], v[168:171], v[208:211], 0
	v_mfma_f32_16x16x32_bf16 v[2:5], v[176:179], v[208:211], 0
	v_mfma_f32_16x16x32_bf16 v[58:61], v[172:175], v[188:191], v[58:61]
	v_mfma_f32_16x16x32_bf16 v[50:53], v[180:183], v[188:191], v[50:53]
	v_mfma_f32_16x16x32_bf16 v[42:45], v[172:175], v[196:199], v[42:45]
	v_mfma_f32_16x16x32_bf16 v[34:37], v[180:183], v[196:199], v[34:37]
	v_mfma_f32_16x16x32_bf16 v[26:29], v[172:175], v[204:207], v[26:29]
	v_mfma_f32_16x16x32_bf16 v[18:21], v[180:183], v[204:207], v[18:21]
	v_mfma_f32_16x16x32_bf16 v[10:13], v[172:175], v[212:215], v[10:13]
	v_mfma_f32_16x16x32_bf16 v[2:5], v[180:183], v[212:215], v[2:5]
	s_barrier
	s_add_i32 s86, 0, 0x18000
	v_add_u32_e32 v155, s86, v149
	s_add_i32 s87, 0, 0x1c000
	ds_read_b128 v[144:147], v155
	ds_read_b128 v[156:159], v155 offset:1024
	ds_read_b128 v[160:163], v155 offset:2048
	ds_read_b128 v[164:167], v155 offset:3072
	v_add_u32_e32 v155, s87, v149
	ds_read_b128 v[168:171], v155
	ds_read_b128 v[172:175], v155 offset:1024
	ds_read_b128 v[176:179], v155 offset:2048
	ds_read_b128 v[180:183], v155 offset:3072
	s_add_u32 s26, s64, 0x80000
	s_addc_u32 s27, s65, 0
	s_mov_b32 m0, s67
	v_lshl_add_u64 v[224:225], s[26:27], 0, v[132:133]
	ds_read_b128 v[184:187], v153 offset:32768
	ds_read_b128 v[188:191], v153 offset:33792
	ds_read_b128 v[192:195], v153 offset:34816
	ds_read_b128 v[196:199], v153 offset:35840
	ds_read_b128 v[200:203], v153 offset:36864
	ds_read_b128 v[204:207], v153 offset:37888
	ds_read_b128 v[208:211], v153 offset:38912
	ds_read_b128 v[212:215], v153 offset:39936
	global_load_lds_dwordx4 v[224:225], off
	v_lshl_add_u64 v[224:225], s[26:27], 0, v[134:135]
	s_mov_b32 m0, s68
	s_nop 0
	global_load_lds_dwordx4 v[224:225], off
	s_waitcnt vmcnt(8)
	s_waitcnt lgkmcnt(0)
	s_barrier
	s_waitcnt lgkmcnt(0)
	v_mfma_f32_16x16x32_bf16 v[126:129], v[144:147], v[184:187], v[126:129]
	v_mfma_f32_16x16x32_bf16 v[118:121], v[160:163], v[184:187], v[118:121]
	v_mfma_f32_16x16x32_bf16 v[110:113], v[144:147], v[192:195], v[110:113]
	v_mfma_f32_16x16x32_bf16 v[102:105], v[160:163], v[192:195], v[102:105]
	v_mfma_f32_16x16x32_bf16 v[94:97], v[144:147], v[200:203], v[94:97]
	v_mfma_f32_16x16x32_bf16 v[86:89], v[160:163], v[200:203], v[86:89]
	v_mfma_f32_16x16x32_bf16 v[78:81], v[144:147], v[208:211], v[78:81]
	v_mfma_f32_16x16x32_bf16 v[70:73], v[160:163], v[208:211], v[70:73]
	v_mfma_f32_16x16x32_bf16 v[126:129], v[156:159], v[188:191], v[126:129]
	v_mfma_f32_16x16x32_bf16 v[118:121], v[164:167], v[188:191], v[118:121]
	v_mfma_f32_16x16x32_bf16 v[110:113], v[156:159], v[196:199], v[110:113]
	v_mfma_f32_16x16x32_bf16 v[102:105], v[164:167], v[196:199], v[102:105]
	v_mfma_f32_16x16x32_bf16 v[94:97], v[156:159], v[204:207], v[94:97]
	v_mfma_f32_16x16x32_bf16 v[86:89], v[164:167], v[204:207], v[86:89]
	v_mfma_f32_16x16x32_bf16 v[78:81], v[156:159], v[212:215], v[78:81]
	v_mfma_f32_16x16x32_bf16 v[70:73], v[164:167], v[212:215], v[70:73]
	v_mfma_f32_16x16x32_bf16 v[122:125], v[168:171], v[184:187], v[122:125]
	v_mfma_f32_16x16x32_bf16 v[114:117], v[176:179], v[184:187], v[114:117]
	v_mfma_f32_16x16x32_bf16 v[106:109], v[168:171], v[192:195], v[106:109]
	v_mfma_f32_16x16x32_bf16 v[98:101], v[176:179], v[192:195], v[98:101]
	v_mfma_f32_16x16x32_bf16 v[90:93], v[168:171], v[200:203], v[90:93]
	v_mfma_f32_16x16x32_bf16 v[82:85], v[176:179], v[200:203], v[82:85]
	v_mfma_f32_16x16x32_bf16 v[74:77], v[168:171], v[208:211], v[74:77]
	v_mfma_f32_16x16x32_bf16 v[66:69], v[176:179], v[208:211], v[66:69]
	v_mfma_f32_16x16x32_bf16 v[122:125], v[172:175], v[188:191], v[122:125]
	v_mfma_f32_16x16x32_bf16 v[114:117], v[180:183], v[188:191], v[114:117]
	v_mfma_f32_16x16x32_bf16 v[106:109], v[172:175], v[196:199], v[106:109]
	v_mfma_f32_16x16x32_bf16 v[98:101], v[180:183], v[196:199], v[98:101]
	v_mfma_f32_16x16x32_bf16 v[90:93], v[172:175], v[204:207], v[90:93]
	v_mfma_f32_16x16x32_bf16 v[82:85], v[180:183], v[204:207], v[82:85]
	v_mfma_f32_16x16x32_bf16 v[74:77], v[172:175], v[212:215], v[74:77]
	v_mfma_f32_16x16x32_bf16 v[66:69], v[180:183], v[212:215], v[66:69]
	s_barrier
	s_add_i32 s26, s86, s35
	v_lshl_add_u64 v[224:225], v[216:217], 0, s[16:17]
	s_mov_b32 m0, s26
	ds_read_b128 v[184:187], v153 offset:49152
	ds_read_b128 v[188:191], v153 offset:50176
	ds_read_b128 v[192:195], v153 offset:51200
	ds_read_b128 v[196:199], v153 offset:52224
	ds_read_b128 v[200:203], v153 offset:53248
	ds_read_b128 v[204:207], v153 offset:54272
	ds_read_b128 v[208:211], v153 offset:55296
	ds_read_b128 v[212:215], v153 offset:56320
	global_load_lds_dwordx4 v[224:225], off
	v_lshl_add_u64 v[224:225], v[216:217], 0, s[18:19]
	s_add_i32 m0, s26, 0x2000
	s_add_i32 s26, s87, s35
	global_load_lds_dwordx4 v[224:225], off
	v_lshl_add_u64 v[224:225], v[216:217], 0, s[22:23]
	s_mov_b32 m0, s26
	v_lshl_add_u64 v[216:217], v[216:217], 0, s[24:25]
	global_load_lds_dwordx4 v[224:225], off
	s_add_i32 m0, s26, 0x2000
	s_nop 0
	global_load_lds_dwordx4 v[216:217], off
	v_lshl_add_u64 v[216:217], v[220:221], 0, s[20:21]
	s_mov_b32 m0, s70
	s_nop 0
	global_load_lds_dwordx4 v[216:217], off
	v_lshl_add_u64 v[216:217], v[222:223], 0, s[20:21]
	s_mov_b32 m0, s71
	s_nop 0
	global_load_lds_dwordx4 v[216:217], off
	s_waitcnt vmcnt(8)
	s_waitcnt lgkmcnt(0)
	s_barrier
	s_waitcnt lgkmcnt(0)
	v_mfma_f32_16x16x32_bf16 v[62:65], v[144:147], v[184:187], v[62:65]
	v_mfma_f32_16x16x32_bf16 v[54:57], v[160:163], v[184:187], v[54:57]
	v_mfma_f32_16x16x32_bf16 v[46:49], v[144:147], v[192:195], v[46:49]
	v_mfma_f32_16x16x32_bf16 v[38:41], v[160:163], v[192:195], v[38:41]
	v_mfma_f32_16x16x32_bf16 v[30:33], v[144:147], v[200:203], v[30:33]
	v_mfma_f32_16x16x32_bf16 v[22:25], v[160:163], v[200:203], v[22:25]
	v_mfma_f32_16x16x32_bf16 v[14:17], v[144:147], v[208:211], v[14:17]
	v_mfma_f32_16x16x32_bf16 v[6:9], v[160:163], v[208:211], v[6:9]
	v_mfma_f32_16x16x32_bf16 v[62:65], v[156:159], v[188:191], v[62:65]
	v_mfma_f32_16x16x32_bf16 v[54:57], v[164:167], v[188:191], v[54:57]
	v_mfma_f32_16x16x32_bf16 v[46:49], v[156:159], v[196:199], v[46:49]
	v_mfma_f32_16x16x32_bf16 v[38:41], v[164:167], v[196:199], v[38:41]
	v_mfma_f32_16x16x32_bf16 v[30:33], v[156:159], v[204:207], v[30:33]
	v_mfma_f32_16x16x32_bf16 v[22:25], v[164:167], v[204:207], v[22:25]
	v_mfma_f32_16x16x32_bf16 v[14:17], v[156:159], v[212:215], v[14:17]
	v_mfma_f32_16x16x32_bf16 v[6:9], v[164:167], v[212:215], v[6:9]
	v_mfma_f32_16x16x32_bf16 v[58:61], v[168:171], v[184:187], v[58:61]
	v_mfma_f32_16x16x32_bf16 v[50:53], v[176:179], v[184:187], v[50:53]
	v_mfma_f32_16x16x32_bf16 v[42:45], v[168:171], v[192:195], v[42:45]
	v_mfma_f32_16x16x32_bf16 v[34:37], v[176:179], v[192:195], v[34:37]
	v_mfma_f32_16x16x32_bf16 v[26:29], v[168:171], v[200:203], v[26:29]
	v_mfma_f32_16x16x32_bf16 v[18:21], v[176:179], v[200:203], v[18:21]
	v_mfma_f32_16x16x32_bf16 v[10:13], v[168:171], v[208:211], v[10:13]
	v_mfma_f32_16x16x32_bf16 v[2:5], v[176:179], v[208:211], v[2:5]
	v_mfma_f32_16x16x32_bf16 v[58:61], v[172:175], v[188:191], v[58:61]
	v_mfma_f32_16x16x32_bf16 v[50:53], v[180:183], v[188:191], v[50:53]
	v_mfma_f32_16x16x32_bf16 v[42:45], v[172:175], v[196:199], v[42:45]
	v_mfma_f32_16x16x32_bf16 v[34:37], v[180:183], v[196:199], v[34:37]
	v_mfma_f32_16x16x32_bf16 v[26:29], v[172:175], v[204:207], v[26:29]
	v_mfma_f32_16x16x32_bf16 v[18:21], v[180:183], v[204:207], v[18:21]
	v_mfma_f32_16x16x32_bf16 v[10:13], v[172:175], v[212:215], v[10:13]
	v_mfma_f32_16x16x32_bf16 v[2:5], v[180:183], v[212:215], v[2:5]
	s_barrier
	s_add_i32 s85, s85, 2
	s_add_u32 s83, s83, 0x10000
	s_addc_u32 s84, s84, 0
	s_add_u32 s62, s62, 0x100
	s_addc_u32 s63, s63, 0
	s_cmp_gt_u32 s85, 29

.LBB0_857:
	s_add_u32 s72, s50, 0x10000
	s_addc_u32 s73, s51, 0
	s_add_u32 s50, s52, 0xb0080
	s_addc_u32 s51, s53, 0
	s_mov_b32 s74, -2
	ds_read_b128 v[26:29], v185
	ds_read_b128 v[30:33], v185 offset:1024
	ds_read_b128 v[18:21], v185 offset:2048
	ds_read_b128 v[22:25], v185 offset:3072
	ds_read_b128 v[10:13], v186
	ds_read_b128 v[14:17], v186 offset:1024
	ds_read_b128 v[2:5], v186 offset:2048
	ds_read_b128 v[6:9], v186 offset:3072
	s_add_u32 s26, s50, 0xfff50080
	s_addc_u32 s27, s51, -1
	s_cmp_eq_u32 s74, 40
	s_cselect_b32 s53, s5, s27
	s_cselect_b32 s52, s4, s26
	s_cselect_b32 s55, s45, s73
	s_cselect_b32 s54, s44, s72
	v_lshl_add_u64 v[176:177], s[50:51], 0, v[168:169]
	s_add_i32 m0, s59, 0xc000
	ds_read_b128 v[190:193], v187
	ds_read_b128 v[194:197], v187 offset:1024
	ds_read_b128 v[198:201], v187 offset:2048
	ds_read_b128 v[202:205], v187 offset:3072
	ds_read_b128 v[206:209], v187 offset:4096
	ds_read_b128 v[210:213], v187 offset:5120
	ds_read_b128 v[220:223], v187 offset:6144
	ds_read_b128 v[224:227], v187 offset:7168
	global_load_lds_dwordx4 v[176:177], off
	v_lshl_add_u64 v[176:177], s[50:51], 0, v[170:171]
	s_add_i32 m0, s59, 0xe000
	s_nop 0
	global_load_lds_dwordx4 v[176:177], off
	s_waitcnt vmcnt(8)
	s_waitcnt lgkmcnt(0)
	s_barrier
	s_waitcnt lgkmcnt(0)
	v_mfma_scale_f32_16x16x128_f8f6f4 v[158:161], v[26:33], v[190:197], 0, v188, v189 op_sel_hi:[0,0,0]
	v_mfma_scale_f32_16x16x128_f8f6f4 v[154:157], v[18:25], v[190:197], 0, v188, v189 op_sel_hi:[0,0,0]
	v_mfma_scale_f32_16x16x128_f8f6f4 v[150:153], v[26:33], v[198:205], 0, v188, v189 op_sel_hi:[0,0,0]
	v_mfma_scale_f32_16x16x128_f8f6f4 v[146:149], v[18:25], v[198:205], 0, v188, v189 op_sel_hi:[0,0,0]
	v_mfma_scale_f32_16x16x128_f8f6f4 v[138:141], v[26:33], v[206:213], 0, v188, v189 op_sel_hi:[0,0,0]
	v_mfma_scale_f32_16x16x128_f8f6f4 v[130:133], v[18:25], v[206:213], 0, v188, v189 op_sel_hi:[0,0,0]
	v_mfma_scale_f32_16x16x128_f8f6f4 v[122:125], v[26:33], v[220:227], 0, v188, v189 op_sel_hi:[0,0,0]
	v_mfma_scale_f32_16x16x128_f8f6f4 v[114:117], v[18:25], v[220:227], 0, v188, v189 op_sel_hi:[0,0,0]
	v_mfma_scale_f32_16x16x128_f8f6f4 v[142:145], v[10:17], v[190:197], 0, v188, v189 op_sel_hi:[0,0,0]
	v_mfma_scale_f32_16x16x128_f8f6f4 v[134:137], v[2:9], v[190:197], 0, v188, v189 op_sel_hi:[0,0,0]
	v_mfma_scale_f32_16x16x128_f8f6f4 v[126:129], v[10:17], v[198:205], 0, v188, v189 op_sel_hi:[0,0,0]
	v_mfma_scale_f32_16x16x128_f8f6f4 v[118:121], v[2:9], v[198:205], 0, v188, v189 op_sel_hi:[0,0,0]
	v_mfma_scale_f32_16x16x128_f8f6f4 v[110:113], v[10:17], v[206:213], 0, v188, v189 op_sel_hi:[0,0,0]
	v_mfma_scale_f32_16x16x128_f8f6f4 v[106:109], v[2:9], v[206:213], 0, v188, v189 op_sel_hi:[0,0,0]
	v_mfma_scale_f32_16x16x128_f8f6f4 v[102:105], v[10:17], v[220:227], 0, v188, v189 op_sel_hi:[0,0,0]
	v_mfma_scale_f32_16x16x128_f8f6f4 v[98:101], v[2:9], v[220:227], 0, v188, v189 op_sel_hi:[0,0,0]
	s_barrier
	s_add_i32 s26, s67, s57
	v_lshl_add_u64 v[176:177], s[54:55], 0, v[162:163]
	s_mov_b32 m0, s26
	ds_read_b128 v[190:193], v187 offset:16384
	ds_read_b128 v[194:197], v187 offset:17408
	ds_read_b128 v[198:201], v187 offset:18432
	ds_read_b128 v[202:205], v187 offset:19456
	ds_read_b128 v[206:209], v187 offset:20480
	ds_read_b128 v[210:213], v187 offset:21504
	ds_read_b128 v[220:223], v187 offset:22528
	ds_read_b128 v[224:227], v187 offset:23552
	global_load_lds_dwordx4 v[176:177], off
	v_lshl_add_u64 v[178:179], v[176:177], 0, s[8:9]
	s_add_i32 m0, s26, 0x2000
	s_add_i32 s26, s68, s57
	global_load_lds_dwordx4 v[178:179], off
	v_lshl_add_u64 v[178:179], v[176:177], 0, s[10:11]
	s_mov_b32 m0, s26
	v_lshl_add_u64 v[180:181], s[52:53], 0, v[166:167]
	global_load_lds_dwordx4 v[178:179], off
	v_lshl_add_u64 v[178:179], v[176:177], 0, s[12:13]
	s_add_i32 m0, s26, 0x2000
	s_nop 0
	global_load_lds_dwordx4 v[178:179], off
	v_lshl_add_u64 v[178:179], s[52:53], 0, v[164:165]
	s_mov_b32 m0, s59
	s_nop 0
	global_load_lds_dwordx4 v[178:179], off
	s_mov_b32 m0, s60
	s_nop 0
	global_load_lds_dwordx4 v[180:181], off
	s_waitcnt vmcnt(8)
	s_waitcnt lgkmcnt(0)
	s_barrier
	s_waitcnt lgkmcnt(0)
	v_mfma_scale_f32_16x16x128_f8f6f4 v[94:97], v[26:33], v[190:197], 0, v188, v189 op_sel_hi:[0,0,0]
	v_mfma_scale_f32_16x16x128_f8f6f4 v[90:93], v[18:25], v[190:197], 0, v188, v189 op_sel_hi:[0,0,0]
	v_mfma_scale_f32_16x16x128_f8f6f4 v[86:89], v[26:33], v[198:205], 0, v188, v189 op_sel_hi:[0,0,0]
	v_mfma_scale_f32_16x16x128_f8f6f4 v[78:81], v[18:25], v[198:205], 0, v188, v189 op_sel_hi:[0,0,0]
	v_mfma_scale_f32_16x16x128_f8f6f4 v[70:73], v[26:33], v[206:213], 0, v188, v189 op_sel_hi:[0,0,0]
	v_mfma_scale_f32_16x16x128_f8f6f4 v[62:65], v[18:25], v[206:213], 0, v188, v189 op_sel_hi:[0,0,0]
	v_mfma_scale_f32_16x16x128_f8f6f4 v[54:57], v[26:33], v[220:227], 0, v188, v189 op_sel_hi:[0,0,0]
	v_mfma_scale_f32_16x16x128_f8f6f4 v[46:49], v[18:25], v[220:227], 0, v188, v189 op_sel_hi:[0,0,0]
	v_mfma_scale_f32_16x16x128_f8f6f4 v[82:85], v[10:17], v[190:197], 0, v188, v189 op_sel_hi:[0,0,0]
	v_mfma_scale_f32_16x16x128_f8f6f4 v[74:77], v[2:9], v[190:197], 0, v188, v189 op_sel_hi:[0,0,0]
	v_mfma_scale_f32_16x16x128_f8f6f4 v[66:69], v[10:17], v[198:205], 0, v188, v189 op_sel_hi:[0,0,0]
	v_mfma_scale_f32_16x16x128_f8f6f4 v[58:61], v[2:9], v[198:205], 0, v188, v189 op_sel_hi:[0,0,0]
	v_mfma_scale_f32_16x16x128_f8f6f4 v[50:53], v[10:17], v[206:213], 0, v188, v189 op_sel_hi:[0,0,0]
	v_mfma_scale_f32_16x16x128_f8f6f4 v[42:45], v[2:9], v[206:213], 0, v188, v189 op_sel_hi:[0,0,0]
	v_mfma_scale_f32_16x16x128_f8f6f4 v[38:41], v[10:17], v[220:227], 0, v188, v189 op_sel_hi:[0,0,0]
	v_mfma_scale_f32_16x16x128_f8f6f4 v[34:37], v[2:9], v[220:227], 0, v188, v189 op_sel_hi:[0,0,0]
	s_barrier
	s_add_i32 s54, 0, 0x18000
	s_add_i32 s55, 0, 0x1c000
	v_add_u32_e32 v14, s54, v183
	v_add_u32_e32 v30, s55, v183
	ds_read_b128 v[2:5], v14
	ds_read_b128 v[6:9], v14 offset:1024
	ds_read_b128 v[10:13], v14 offset:2048
	ds_read_b128 v[14:17], v14 offset:3072
	ds_read_b128 v[18:21], v30
	ds_read_b128 v[22:25], v30 offset:1024
	ds_read_b128 v[26:29], v30 offset:2048
	ds_read_b128 v[30:33], v30 offset:3072
	s_add_u32 s26, s52, 0xb0000
	s_addc_u32 s27, s53, 0
	s_mov_b32 m0, s61
	v_lshl_add_u64 v[214:215], s[26:27], 0, v[164:165]
	ds_read_b128 v[190:193], v187 offset:32768
	ds_read_b128 v[194:197], v187 offset:33792
	ds_read_b128 v[198:201], v187 offset:34816
	ds_read_b128 v[202:205], v187 offset:35840
	ds_read_b128 v[206:209], v187 offset:36864
	ds_read_b128 v[210:213], v187 offset:37888
	ds_read_b128 v[220:223], v187 offset:38912
	ds_read_b128 v[224:227], v187 offset:39936
	global_load_lds_dwordx4 v[214:215], off
	v_lshl_add_u64 v[214:215], s[26:27], 0, v[166:167]
	s_mov_b32 m0, s62
	s_nop 0
	global_load_lds_dwordx4 v[214:215], off
	s_waitcnt vmcnt(8)
	s_waitcnt lgkmcnt(0)
	s_barrier
	s_waitcnt lgkmcnt(0)
	v_mfma_scale_f32_16x16x128_f8f6f4 v[158:161], v[2:9], v[190:197], v[158:161], v188, v189 op_sel_hi:[0,0,0]
	v_mfma_scale_f32_16x16x128_f8f6f4 v[154:157], v[10:17], v[190:197], v[154:157], v188, v189 op_sel_hi:[0,0,0]
	v_mfma_scale_f32_16x16x128_f8f6f4 v[150:153], v[2:9], v[198:205], v[150:153], v188, v189 op_sel_hi:[0,0,0]
	v_mfma_scale_f32_16x16x128_f8f6f4 v[146:149], v[10:17], v[198:205], v[146:149], v188, v189 op_sel_hi:[0,0,0]
	v_mfma_scale_f32_16x16x128_f8f6f4 v[138:141], v[2:9], v[206:213], v[138:141], v188, v189 op_sel_hi:[0,0,0]
	v_mfma_scale_f32_16x16x128_f8f6f4 v[130:133], v[10:17], v[206:213], v[130:133], v188, v189 op_sel_hi:[0,0,0]
	v_mfma_scale_f32_16x16x128_f8f6f4 v[122:125], v[2:9], v[220:227], v[122:125], v188, v189 op_sel_hi:[0,0,0]
	v_mfma_scale_f32_16x16x128_f8f6f4 v[114:117], v[10:17], v[220:227], v[114:117], v188, v189 op_sel_hi:[0,0,0]
	v_mfma_scale_f32_16x16x128_f8f6f4 v[142:145], v[18:25], v[190:197], v[142:145], v188, v189 op_sel_hi:[0,0,0]
	v_mfma_scale_f32_16x16x128_f8f6f4 v[134:137], v[26:33], v[190:197], v[134:137], v188, v189 op_sel_hi:[0,0,0]
	v_mfma_scale_f32_16x16x128_f8f6f4 v[126:129], v[18:25], v[198:205], v[126:129], v188, v189 op_sel_hi:[0,0,0]
	v_mfma_scale_f32_16x16x128_f8f6f4 v[118:121], v[26:33], v[198:205], v[118:121], v188, v189 op_sel_hi:[0,0,0]
	v_mfma_scale_f32_16x16x128_f8f6f4 v[110:113], v[18:25], v[206:213], v[110:113], v188, v189 op_sel_hi:[0,0,0]
	v_mfma_scale_f32_16x16x128_f8f6f4 v[106:109], v[26:33], v[206:213], v[106:109], v188, v189 op_sel_hi:[0,0,0]
	v_mfma_scale_f32_16x16x128_f8f6f4 v[102:105], v[18:25], v[220:227], v[102:105], v188, v189 op_sel_hi:[0,0,0]
	v_mfma_scale_f32_16x16x128_f8f6f4 v[98:101], v[26:33], v[220:227], v[98:101], v188, v189 op_sel_hi:[0,0,0]
	s_barrier
	s_add_i32 s26, s54, s57
	v_lshl_add_u64 v[214:215], v[176:177], 0, s[16:17]
	s_mov_b32 m0, s26
	ds_read_b128 v[190:193], v187 offset:49152
	ds_read_b128 v[194:197], v187 offset:50176
	ds_read_b128 v[198:201], v187 offset:51200
	ds_read_b128 v[202:205], v187 offset:52224
	ds_read_b128 v[206:209], v187 offset:53248
	ds_read_b128 v[210:213], v187 offset:54272
	ds_read_b128 v[220:223], v187 offset:55296
	ds_read_b128 v[224:227], v187 offset:56320
	global_load_lds_dwordx4 v[214:215], off
	v_lshl_add_u64 v[214:215], v[176:177], 0, s[18:19]
	s_add_i32 m0, s26, 0x2000
	s_add_i32 s26, s55, s57
	global_load_lds_dwordx4 v[214:215], off
	v_lshl_add_u64 v[214:215], v[176:177], 0, s[22:23]
	s_mov_b32 m0, s26
	v_lshl_add_u64 v[176:177], v[176:177], 0, s[24:25]
	global_load_lds_dwordx4 v[214:215], off
	s_add_i32 m0, s26, 0x2000
	s_nop 0
	global_load_lds_dwordx4 v[176:177], off
	v_lshl_add_u64 v[176:177], v[178:179], 0, s[20:21]
	s_mov_b32 m0, s64
	s_nop 0
	global_load_lds_dwordx4 v[176:177], off
	v_lshl_add_u64 v[176:177], v[180:181], 0, s[20:21]
	s_mov_b32 m0, s65
	s_nop 0
	global_load_lds_dwordx4 v[176:177], off
	s_waitcnt vmcnt(8)
	s_waitcnt lgkmcnt(0)
	s_barrier
	s_waitcnt lgkmcnt(0)
	v_mfma_scale_f32_16x16x128_f8f6f4 v[94:97], v[2:9], v[190:197], v[94:97], v188, v189 op_sel_hi:[0,0,0]
	v_mfma_scale_f32_16x16x128_f8f6f4 v[90:93], v[10:17], v[190:197], v[90:93], v188, v189 op_sel_hi:[0,0,0]
	v_mfma_scale_f32_16x16x128_f8f6f4 v[86:89], v[2:9], v[198:205], v[86:89], v188, v189 op_sel_hi:[0,0,0]
	v_mfma_scale_f32_16x16x128_f8f6f4 v[78:81], v[10:17], v[198:205], v[78:81], v188, v189 op_sel_hi:[0,0,0]
	v_mfma_scale_f32_16x16x128_f8f6f4 v[70:73], v[2:9], v[206:213], v[70:73], v188, v189 op_sel_hi:[0,0,0]
	v_mfma_scale_f32_16x16x128_f8f6f4 v[62:65], v[10:17], v[206:213], v[62:65], v188, v189 op_sel_hi:[0,0,0]
	v_mfma_scale_f32_16x16x128_f8f6f4 v[54:57], v[2:9], v[220:227], v[54:57], v188, v189 op_sel_hi:[0,0,0]
	v_mfma_scale_f32_16x16x128_f8f6f4 v[46:49], v[10:17], v[220:227], v[46:49], v188, v189 op_sel_hi:[0,0,0]
	v_mfma_scale_f32_16x16x128_f8f6f4 v[82:85], v[18:25], v[190:197], v[82:85], v188, v189 op_sel_hi:[0,0,0]
	v_mfma_scale_f32_16x16x128_f8f6f4 v[74:77], v[26:33], v[190:197], v[74:77], v188, v189 op_sel_hi:[0,0,0]
	v_mfma_scale_f32_16x16x128_f8f6f4 v[66:69], v[18:25], v[198:205], v[66:69], v188, v189 op_sel_hi:[0,0,0]
	v_mfma_scale_f32_16x16x128_f8f6f4 v[58:61], v[26:33], v[198:205], v[58:61], v188, v189 op_sel_hi:[0,0,0]
	v_mfma_scale_f32_16x16x128_f8f6f4 v[50:53], v[18:25], v[206:213], v[50:53], v188, v189 op_sel_hi:[0,0,0]
	v_mfma_scale_f32_16x16x128_f8f6f4 v[42:45], v[26:33], v[206:213], v[42:45], v188, v189 op_sel_hi:[0,0,0]
	v_mfma_scale_f32_16x16x128_f8f6f4 v[38:41], v[18:25], v[220:227], v[38:41], v188, v189 op_sel_hi:[0,0,0]
	v_mfma_scale_f32_16x16x128_f8f6f4 v[34:37], v[26:33], v[220:227], v[34:37], v188, v189 op_sel_hi:[0,0,0]
	s_barrier
	s_add_i32 s74, s74, 2
	s_add_u32 s72, s72, 0x10000
	s_addc_u32 s73, s73, 0
	s_add_u32 s50, s50, 0x100
	s_addc_u32 s51, s51, 0
	s_cmp_gt_u32 s74, 41

.LBB0_984:
	s_ashr_i32 s45, s44, 31
	s_lshl_b64 s[26:27], s[44:45], 19
	v_readlane_b32 s50, v254, 56
	v_readlane_b32 s51, v254, 57
	s_add_u32 s50, s50, s26
	s_addc_u32 s51, s51, s27
	s_and_b64 s[26:27], s[0:1], exec
	s_cselect_b32 s45, s51, s59
	s_cselect_b32 s72, s50, s58
	s_ashr_i32 s41, s40, 31
	s_lshl_b64 s[26:27], s[40:41], 19
	s_add_u32 s52, s3, s26
	s_addc_u32 s53, s33, s27
	s_and_b64 s[26:27], s[0:1], exec
	s_cselect_b32 s41, s53, s57
	s_cselect_b32 s73, s52, s56
	s_add_u32 s74, s56, 0x10000
	s_addc_u32 s75, s57, 0
	s_add_u32 s56, s58, 0x40080
	s_addc_u32 s57, s59, 0
	s_mov_b32 s80, -2
	ds_read_b128 v[26:29], v185
	ds_read_b128 v[30:33], v185 offset:1024
	ds_read_b128 v[18:21], v185 offset:2048
	ds_read_b128 v[22:25], v185 offset:3072
	ds_read_b128 v[10:13], v186
	ds_read_b128 v[14:17], v186 offset:1024
	ds_read_b128 v[2:5], v186 offset:2048
	ds_read_b128 v[6:9], v186 offset:3072
	s_add_u32 s26, s56, 0xfffc0080
	s_addc_u32 s27, s57, -1
	s_cmp_eq_u32 s80, 12
	s_cselect_b32 s59, s45, s27
	s_cselect_b32 s58, s72, s26
	s_cselect_b32 s61, s41, s75
	s_cselect_b32 s60, s73, s74
	v_lshl_add_u64 v[176:177], s[56:57], 0, v[168:169]
	s_add_i32 m0, s55, 0xc000
	ds_read_b128 v[192:195], v187
	ds_read_b128 v[196:199], v187 offset:1024
	ds_read_b128 v[200:203], v187 offset:2048
	ds_read_b128 v[204:207], v187 offset:3072
	ds_read_b128 v[208:211], v187 offset:4096
	ds_read_b128 v[212:215], v187 offset:5120
	ds_read_b128 v[220:223], v187 offset:6144
	ds_read_b128 v[224:227], v187 offset:7168
	global_load_lds_dwordx4 v[176:177], off
	v_lshl_add_u64 v[176:177], s[56:57], 0, v[170:171]
	s_add_i32 m0, s55, 0xe000
	s_nop 0
	global_load_lds_dwordx4 v[176:177], off
	s_waitcnt vmcnt(8)
	s_waitcnt lgkmcnt(0)
	s_barrier
	s_waitcnt lgkmcnt(0)
	v_mfma_scale_f32_16x16x128_f8f6f4 v[158:161], v[26:33], v[192:199], 0, v188, v189 op_sel_hi:[0,0,0]
	v_mfma_scale_f32_16x16x128_f8f6f4 v[154:157], v[18:25], v[192:199], 0, v188, v189 op_sel_hi:[0,0,0]
	v_mfma_scale_f32_16x16x128_f8f6f4 v[146:149], v[26:33], v[200:207], 0, v188, v189 op_sel_hi:[0,0,0]
	v_mfma_scale_f32_16x16x128_f8f6f4 v[138:141], v[18:25], v[200:207], 0, v188, v189 op_sel_hi:[0,0,0]
	v_mfma_scale_f32_16x16x128_f8f6f4 v[130:133], v[26:33], v[208:215], 0, v188, v189 op_sel_hi:[0,0,0]
	v_mfma_scale_f32_16x16x128_f8f6f4 v[122:125], v[18:25], v[208:215], 0, v188, v189 op_sel_hi:[0,0,0]
	v_mfma_scale_f32_16x16x128_f8f6f4 v[114:117], v[26:33], v[220:227], 0, v188, v189 op_sel_hi:[0,0,0]
	v_mfma_scale_f32_16x16x128_f8f6f4 v[106:109], v[18:25], v[220:227], 0, v188, v189 op_sel_hi:[0,0,0]
	v_mfma_scale_f32_16x16x128_f8f6f4 v[150:153], v[10:17], v[192:199], 0, v188, v189 op_sel_hi:[0,0,0]
	v_mfma_scale_f32_16x16x128_f8f6f4 v[142:145], v[2:9], v[192:199], 0, v188, v189 op_sel_hi:[0,0,0]
	v_mfma_scale_f32_16x16x128_f8f6f4 v[134:137], v[10:17], v[200:207], 0, v188, v189 op_sel_hi:[0,0,0]
	v_mfma_scale_f32_16x16x128_f8f6f4 v[126:129], v[2:9], v[200:207], 0, v188, v189 op_sel_hi:[0,0,0]
	v_mfma_scale_f32_16x16x128_f8f6f4 v[118:121], v[10:17], v[208:215], 0, v188, v189 op_sel_hi:[0,0,0]
	v_mfma_scale_f32_16x16x128_f8f6f4 v[110:113], v[2:9], v[208:215], 0, v188, v189 op_sel_hi:[0,0,0]
	v_mfma_scale_f32_16x16x128_f8f6f4 v[102:105], v[10:17], v[220:227], 0, v188, v189 op_sel_hi:[0,0,0]
	v_mfma_scale_f32_16x16x128_f8f6f4 v[98:101], v[2:9], v[220:227], 0, v188, v189 op_sel_hi:[0,0,0]
	s_barrier
	s_add_i32 s26, s70, s35
	v_lshl_add_u64 v[176:177], s[60:61], 0, v[162:163]
	s_mov_b32 m0, s26
	ds_read_b128 v[192:195], v187 offset:16384
	ds_read_b128 v[196:199], v187 offset:17408
	ds_read_b128 v[200:203], v187 offset:18432
	ds_read_b128 v[204:207], v187 offset:19456
	ds_read_b128 v[208:211], v187 offset:20480
	ds_read_b128 v[212:215], v187 offset:21504
	ds_read_b128 v[220:223], v187 offset:22528
	ds_read_b128 v[224:227], v187 offset:23552
	global_load_lds_dwordx4 v[176:177], off
	v_lshl_add_u64 v[178:179], v[176:177], 0, s[6:7]
	s_add_i32 m0, s26, 0x2000
	s_add_i32 s26, s71, s35
	global_load_lds_dwordx4 v[178:179], off
	v_lshl_add_u64 v[178:179], v[176:177], 0, s[8:9]
	s_mov_b32 m0, s26
	v_lshl_add_u64 v[180:181], s[58:59], 0, v[166:167]
	global_load_lds_dwordx4 v[178:179], off
	v_lshl_add_u64 v[178:179], v[176:177], 0, s[10:11]
	s_add_i32 m0, s26, 0x2000
	s_nop 0
	global_load_lds_dwordx4 v[178:179], off
	v_lshl_add_u64 v[178:179], s[58:59], 0, v[164:165]
	s_mov_b32 m0, s55
	s_nop 0
	global_load_lds_dwordx4 v[178:179], off
	s_mov_b32 m0, s63
	s_nop 0
	global_load_lds_dwordx4 v[180:181], off
	s_waitcnt vmcnt(8)
	s_waitcnt lgkmcnt(0)
	s_barrier
	s_waitcnt lgkmcnt(0)
	v_mfma_scale_f32_16x16x128_f8f6f4 v[94:97], v[26:33], v[192:199], 0, v188, v189 op_sel_hi:[0,0,0]
	v_mfma_scale_f32_16x16x128_f8f6f4 v[90:93], v[18:25], v[192:199], 0, v188, v189 op_sel_hi:[0,0,0]
	v_mfma_scale_f32_16x16x128_f8f6f4 v[82:85], v[26:33], v[200:207], 0, v188, v189 op_sel_hi:[0,0,0]
	v_mfma_scale_f32_16x16x128_f8f6f4 v[74:77], v[18:25], v[200:207], 0, v188, v189 op_sel_hi:[0,0,0]
	v_mfma_scale_f32_16x16x128_f8f6f4 v[66:69], v[26:33], v[208:215], 0, v188, v189 op_sel_hi:[0,0,0]
	v_mfma_scale_f32_16x16x128_f8f6f4 v[58:61], v[18:25], v[208:215], 0, v188, v189 op_sel_hi:[0,0,0]
	v_mfma_scale_f32_16x16x128_f8f6f4 v[50:53], v[26:33], v[220:227], 0, v188, v189 op_sel_hi:[0,0,0]
	v_mfma_scale_f32_16x16x128_f8f6f4 v[42:45], v[18:25], v[220:227], 0, v188, v189 op_sel_hi:[0,0,0]
	v_mfma_scale_f32_16x16x128_f8f6f4 v[86:89], v[10:17], v[192:199], 0, v188, v189 op_sel_hi:[0,0,0]
	v_mfma_scale_f32_16x16x128_f8f6f4 v[78:81], v[2:9], v[192:199], 0, v188, v189 op_sel_hi:[0,0,0]
	v_mfma_scale_f32_16x16x128_f8f6f4 v[70:73], v[10:17], v[200:207], 0, v188, v189 op_sel_hi:[0,0,0]
	v_mfma_scale_f32_16x16x128_f8f6f4 v[62:65], v[2:9], v[200:207], 0, v188, v189 op_sel_hi:[0,0,0]
	v_mfma_scale_f32_16x16x128_f8f6f4 v[54:57], v[10:17], v[208:215], 0, v188, v189 op_sel_hi:[0,0,0]
	v_mfma_scale_f32_16x16x128_f8f6f4 v[46:49], v[2:9], v[208:215], 0, v188, v189 op_sel_hi:[0,0,0]
	v_mfma_scale_f32_16x16x128_f8f6f4 v[38:41], v[10:17], v[220:227], 0, v188, v189 op_sel_hi:[0,0,0]
	v_mfma_scale_f32_16x16x128_f8f6f4 v[34:37], v[2:9], v[220:227], 0, v188, v189 op_sel_hi:[0,0,0]
	s_barrier
	s_add_i32 s60, 0, 0x18000
	s_add_i32 s61, 0, 0x1c000
	v_add_u32_e32 v14, s60, v183
	v_add_u32_e32 v30, s61, v183
	ds_read_b128 v[2:5], v14
	ds_read_b128 v[6:9], v14 offset:1024
	ds_read_b128 v[10:13], v14 offset:2048
	ds_read_b128 v[14:17], v14 offset:3072
	ds_read_b128 v[18:21], v30
	ds_read_b128 v[22:25], v30 offset:1024
	ds_read_b128 v[26:29], v30 offset:2048
	ds_read_b128 v[30:33], v30 offset:3072
	s_add_u32 s26, s58, 0x40000
	s_addc_u32 s27, s59, 0
	s_mov_b32 m0, s64
	v_lshl_add_u64 v[216:217], s[26:27], 0, v[164:165]
	ds_read_b128 v[192:195], v187 offset:32768
	ds_read_b128 v[196:199], v187 offset:33792
	ds_read_b128 v[200:203], v187 offset:34816
	ds_read_b128 v[204:207], v187 offset:35840
	ds_read_b128 v[208:211], v187 offset:36864
	ds_read_b128 v[212:215], v187 offset:37888
	ds_read_b128 v[220:223], v187 offset:38912
	ds_read_b128 v[224:227], v187 offset:39936
	global_load_lds_dwordx4 v[216:217], off
	v_lshl_add_u64 v[216:217], s[26:27], 0, v[166:167]
	s_mov_b32 m0, s65
	s_nop 0
	global_load_lds_dwordx4 v[216:217], off
	s_waitcnt vmcnt(8)
	s_waitcnt lgkmcnt(0)
	s_barrier
	s_waitcnt lgkmcnt(0)
	v_mfma_scale_f32_16x16x128_f8f6f4 v[158:161], v[2:9], v[192:199], v[158:161], v188, v189 op_sel_hi:[0,0,0]
	v_mfma_scale_f32_16x16x128_f8f6f4 v[154:157], v[10:17], v[192:199], v[154:157], v188, v189 op_sel_hi:[0,0,0]
	v_mfma_scale_f32_16x16x128_f8f6f4 v[146:149], v[2:9], v[200:207], v[146:149], v188, v189 op_sel_hi:[0,0,0]
	v_mfma_scale_f32_16x16x128_f8f6f4 v[138:141], v[10:17], v[200:207], v[138:141], v188, v189 op_sel_hi:[0,0,0]
	v_mfma_scale_f32_16x16x128_f8f6f4 v[130:133], v[2:9], v[208:215], v[130:133], v188, v189 op_sel_hi:[0,0,0]
	v_mfma_scale_f32_16x16x128_f8f6f4 v[122:125], v[10:17], v[208:215], v[122:125], v188, v189 op_sel_hi:[0,0,0]
	v_mfma_scale_f32_16x16x128_f8f6f4 v[114:117], v[2:9], v[220:227], v[114:117], v188, v189 op_sel_hi:[0,0,0]
	v_mfma_scale_f32_16x16x128_f8f6f4 v[106:109], v[10:17], v[220:227], v[106:109], v188, v189 op_sel_hi:[0,0,0]
	v_mfma_scale_f32_16x16x128_f8f6f4 v[150:153], v[18:25], v[192:199], v[150:153], v188, v189 op_sel_hi:[0,0,0]
	v_mfma_scale_f32_16x16x128_f8f6f4 v[142:145], v[26:33], v[192:199], v[142:145], v188, v189 op_sel_hi:[0,0,0]
	v_mfma_scale_f32_16x16x128_f8f6f4 v[134:137], v[18:25], v[200:207], v[134:137], v188, v189 op_sel_hi:[0,0,0]
	v_mfma_scale_f32_16x16x128_f8f6f4 v[126:129], v[26:33], v[200:207], v[126:129], v188, v189 op_sel_hi:[0,0,0]
	v_mfma_scale_f32_16x16x128_f8f6f4 v[118:121], v[18:25], v[208:215], v[118:121], v188, v189 op_sel_hi:[0,0,0]
	v_mfma_scale_f32_16x16x128_f8f6f4 v[110:113], v[26:33], v[208:215], v[110:113], v188, v189 op_sel_hi:[0,0,0]
	v_mfma_scale_f32_16x16x128_f8f6f4 v[102:105], v[18:25], v[220:227], v[102:105], v188, v189 op_sel_hi:[0,0,0]
	v_mfma_scale_f32_16x16x128_f8f6f4 v[98:101], v[26:33], v[220:227], v[98:101], v188, v189 op_sel_hi:[0,0,0]
	s_barrier
	s_add_i32 s26, s60, s35
	v_lshl_add_u64 v[216:217], v[176:177], 0, s[14:15]
	s_mov_b32 m0, s26
	ds_read_b128 v[192:195], v187 offset:49152
	ds_read_b128 v[196:199], v187 offset:50176
	ds_read_b128 v[200:203], v187 offset:51200
	ds_read_b128 v[204:207], v187 offset:52224
	ds_read_b128 v[208:211], v187 offset:53248
	ds_read_b128 v[212:215], v187 offset:54272
	ds_read_b128 v[220:223], v187 offset:55296
	ds_read_b128 v[224:227], v187 offset:56320
	global_load_lds_dwordx4 v[216:217], off
	v_lshl_add_u64 v[216:217], v[176:177], 0, s[16:17]
	s_add_i32 m0, s26, 0x2000
	s_add_i32 s26, s61, s35
	global_load_lds_dwordx4 v[216:217], off
	v_lshl_add_u64 v[216:217], v[176:177], 0, s[20:21]
	s_mov_b32 m0, s26
	v_lshl_add_u64 v[176:177], v[176:177], 0, s[22:23]
	global_load_lds_dwordx4 v[216:217], off
	s_add_i32 m0, s26, 0x2000
	s_nop 0
	global_load_lds_dwordx4 v[176:177], off
	v_lshl_add_u64 v[176:177], v[178:179], 0, s[18:19]
	s_mov_b32 m0, s67
	s_nop 0
	global_load_lds_dwordx4 v[176:177], off
	v_lshl_add_u64 v[176:177], v[180:181], 0, s[18:19]
	s_mov_b32 m0, s68
	s_nop 0
	global_load_lds_dwordx4 v[176:177], off
	s_waitcnt vmcnt(8)
	s_waitcnt lgkmcnt(0)
	s_barrier
	s_waitcnt lgkmcnt(0)
	v_mfma_scale_f32_16x16x128_f8f6f4 v[94:97], v[2:9], v[192:199], v[94:97], v188, v189 op_sel_hi:[0,0,0]
	v_mfma_scale_f32_16x16x128_f8f6f4 v[90:93], v[10:17], v[192:199], v[90:93], v188, v189 op_sel_hi:[0,0,0]
	v_mfma_scale_f32_16x16x128_f8f6f4 v[82:85], v[2:9], v[200:207], v[82:85], v188, v189 op_sel_hi:[0,0,0]
	v_mfma_scale_f32_16x16x128_f8f6f4 v[74:77], v[10:17], v[200:207], v[74:77], v188, v189 op_sel_hi:[0,0,0]
	v_mfma_scale_f32_16x16x128_f8f6f4 v[66:69], v[2:9], v[208:215], v[66:69], v188, v189 op_sel_hi:[0,0,0]
	v_mfma_scale_f32_16x16x128_f8f6f4 v[58:61], v[10:17], v[208:215], v[58:61], v188, v189 op_sel_hi:[0,0,0]
	v_mfma_scale_f32_16x16x128_f8f6f4 v[50:53], v[2:9], v[220:227], v[50:53], v188, v189 op_sel_hi:[0,0,0]
	v_mfma_scale_f32_16x16x128_f8f6f4 v[42:45], v[10:17], v[220:227], v[42:45], v188, v189 op_sel_hi:[0,0,0]
	v_mfma_scale_f32_16x16x128_f8f6f4 v[86:89], v[18:25], v[192:199], v[86:89], v188, v189 op_sel_hi:[0,0,0]
	v_mfma_scale_f32_16x16x128_f8f6f4 v[78:81], v[26:33], v[192:199], v[78:81], v188, v189 op_sel_hi:[0,0,0]
	v_mfma_scale_f32_16x16x128_f8f6f4 v[70:73], v[18:25], v[200:207], v[70:73], v188, v189 op_sel_hi:[0,0,0]
	v_mfma_scale_f32_16x16x128_f8f6f4 v[62:65], v[26:33], v[200:207], v[62:65], v188, v189 op_sel_hi:[0,0,0]
	v_mfma_scale_f32_16x16x128_f8f6f4 v[54:57], v[18:25], v[208:215], v[54:57], v188, v189 op_sel_hi:[0,0,0]
	v_mfma_scale_f32_16x16x128_f8f6f4 v[46:49], v[26:33], v[208:215], v[46:49], v188, v189 op_sel_hi:[0,0,0]
	v_mfma_scale_f32_16x16x128_f8f6f4 v[38:41], v[18:25], v[220:227], v[38:41], v188, v189 op_sel_hi:[0,0,0]
	v_mfma_scale_f32_16x16x128_f8f6f4 v[34:37], v[26:33], v[220:227], v[34:37], v188, v189 op_sel_hi:[0,0,0]
	s_barrier
	s_add_i32 s80, s80, 2
	s_add_u32 s74, s74, 0x10000
	s_addc_u32 s75, s75, 0
	s_add_u32 s56, s56, 0x100
	s_addc_u32 s57, s57, 0
	s_cmp_gt_u32 s80, 13

.LBB0_1191:
	s_ashr_i32 s45, s44, 31
	s_lshl_b64 s[26:27], s[44:45], 19
	s_add_u32 s50, s4, s26
	s_addc_u32 s51, s5, s27
	s_and_b64 s[26:27], s[0:1], exec
	s_cselect_b32 s45, s51, s59
	s_cselect_b32 s69, s50, s58
	s_ashr_i32 s41, s40, 31
	s_lshl_b64 s[26:27], s[40:41], 19
	s_add_u32 s52, s3, s26
	s_addc_u32 s53, s33, s27
	s_and_b64 s[26:27], s[0:1], exec
	s_cselect_b32 s41, s53, s57
	s_cselect_b32 s70, s52, s56
	s_add_u32 s71, s56, 0x10000
	s_addc_u32 s72, s57, 0
	s_add_u32 s56, s58, 0x40080
	s_addc_u32 s57, s59, 0
	s_mov_b32 s73, -2
	ds_read_b128 v[66:69], v199
	ds_read_b128 v[70:73], v199 offset:1024
	ds_read_b128 v[82:85], v199 offset:2048
	ds_read_b128 v[86:89], v199 offset:3072
	ds_read_b128 v[146:149], v200
	ds_read_b128 v[150:153], v200 offset:1024
	ds_read_b128 v[154:157], v200 offset:2048
	ds_read_b128 v[158:161], v200 offset:3072
	s_add_u32 s26, s56, 0xfffc0080
	s_addc_u32 s27, s57, -1
	s_cmp_eq_u32 s73, 12
	s_cselect_b32 s59, s45, s27
	s_cselect_b32 s58, s69, s26
	s_cselect_b32 s27, s41, s72
	s_cselect_b32 s26, s70, s71
	v_lshl_add_u64 v[214:215], s[56:57], 0, v[176:177]
	s_add_i32 m0, s55, 0xc000
	ds_read_b128 v[162:165], v201
	ds_read_b128 v[166:169], v201 offset:1024
	ds_read_b128 v[184:187], v201 offset:2048
	ds_read_b128 v[188:191], v201 offset:3072
	ds_read_b128 v[192:195], v201 offset:4096
	ds_read_b128 v[202:205], v201 offset:5120
	ds_read_b128 v[206:209], v201 offset:6144
	ds_read_b128 v[210:213], v201 offset:7168
	global_load_lds_dwordx4 v[214:215], off
	v_lshl_add_u64 v[214:215], s[56:57], 0, v[178:179]
	s_add_i32 m0, s55, 0xe000
	s_nop 0
	global_load_lds_dwordx4 v[214:215], off
	s_waitcnt vmcnt(8)
	s_waitcnt lgkmcnt(0)
	s_barrier
	s_waitcnt lgkmcnt(0)
	v_mfma_f32_16x16x32_bf16 v[142:145], v[66:69], v[162:165], 0
	v_mfma_f32_16x16x32_bf16 v[138:141], v[82:85], v[162:165], 0
	v_mfma_f32_16x16x32_bf16 v[126:129], v[66:69], v[184:187], 0
	v_mfma_f32_16x16x32_bf16 v[122:125], v[82:85], v[184:187], 0
	v_mfma_f32_16x16x32_bf16 v[110:113], v[66:69], v[192:195], 0
	v_mfma_f32_16x16x32_bf16 v[106:109], v[82:85], v[192:195], 0
	v_mfma_f32_16x16x32_bf16 v[94:97], v[66:69], v[206:209], 0
	v_mfma_f32_16x16x32_bf16 v[90:93], v[82:85], v[206:209], 0
	v_mfma_f32_16x16x32_bf16 v[142:145], v[70:73], v[166:169], v[142:145]
	v_mfma_f32_16x16x32_bf16 v[138:141], v[86:89], v[166:169], v[138:141]
	v_mfma_f32_16x16x32_bf16 v[126:129], v[70:73], v[188:191], v[126:129]
	v_mfma_f32_16x16x32_bf16 v[122:125], v[86:89], v[188:191], v[122:125]
	v_mfma_f32_16x16x32_bf16 v[110:113], v[70:73], v[202:205], v[110:113]
	v_mfma_f32_16x16x32_bf16 v[106:109], v[86:89], v[202:205], v[106:109]
	v_mfma_f32_16x16x32_bf16 v[94:97], v[70:73], v[210:213], v[94:97]
	v_mfma_f32_16x16x32_bf16 v[90:93], v[86:89], v[210:213], v[90:93]
	v_mfma_f32_16x16x32_bf16 v[134:137], v[146:149], v[162:165], 0
	v_mfma_f32_16x16x32_bf16 v[130:133], v[154:157], v[162:165], 0
	v_mfma_f32_16x16x32_bf16 v[118:121], v[146:149], v[184:187], 0
	v_mfma_f32_16x16x32_bf16 v[114:117], v[154:157], v[184:187], 0
	v_mfma_f32_16x16x32_bf16 v[102:105], v[146:149], v[192:195], 0
	v_mfma_f32_16x16x32_bf16 v[98:101], v[154:157], v[192:195], 0
	v_mfma_f32_16x16x32_bf16 v[78:81], v[146:149], v[206:209], 0
	v_mfma_f32_16x16x32_bf16 v[74:77], v[154:157], v[206:209], 0
	v_mfma_f32_16x16x32_bf16 v[134:137], v[150:153], v[166:169], v[134:137]
	v_mfma_f32_16x16x32_bf16 v[130:133], v[158:161], v[166:169], v[130:133]
	v_mfma_f32_16x16x32_bf16 v[118:121], v[150:153], v[188:191], v[118:121]
	v_mfma_f32_16x16x32_bf16 v[114:117], v[158:161], v[188:191], v[114:117]
	v_mfma_f32_16x16x32_bf16 v[102:105], v[150:153], v[202:205], v[102:105]
	v_mfma_f32_16x16x32_bf16 v[98:101], v[158:161], v[202:205], v[98:101]
	v_mfma_f32_16x16x32_bf16 v[78:81], v[150:153], v[210:213], v[78:81]
	v_mfma_f32_16x16x32_bf16 v[74:77], v[158:161], v[210:213], v[74:77]
	s_barrier
	v_lshl_add_u64 v[214:215], s[26:27], 0, v[170:171]
	s_add_i32 s26, s67, s35
	s_mov_b32 m0, s26
	ds_read_b128 v[162:165], v201 offset:16384
	ds_read_b128 v[166:169], v201 offset:17408
	ds_read_b128 v[184:187], v201 offset:18432
	ds_read_b128 v[188:191], v201 offset:19456
	ds_read_b128 v[192:195], v201 offset:20480
	ds_read_b128 v[202:205], v201 offset:21504
	ds_read_b128 v[206:209], v201 offset:22528
	ds_read_b128 v[210:213], v201 offset:23552
	global_load_lds_dwordx4 v[214:215], off
	v_lshl_add_u64 v[216:217], v[214:215], 0, s[6:7]
	s_add_i32 m0, s26, 0x2000
	s_add_i32 s26, s68, s35
	global_load_lds_dwordx4 v[216:217], off
	v_lshl_add_u64 v[216:217], v[214:215], 0, s[10:11]
	s_mov_b32 m0, s26
	v_lshl_add_u64 v[220:221], s[58:59], 0, v[174:175]
	global_load_lds_dwordx4 v[216:217], off
	v_lshl_add_u64 v[216:217], v[214:215], 0, s[12:13]
	s_add_i32 m0, s26, 0x2000
	s_nop 0
	global_load_lds_dwordx4 v[216:217], off
	v_lshl_add_u64 v[216:217], s[58:59], 0, v[172:173]
	s_mov_b32 m0, s55
	s_nop 0
	global_load_lds_dwordx4 v[216:217], off
	s_mov_b32 m0, s60
	s_nop 0
	global_load_lds_dwordx4 v[220:221], off
	s_waitcnt vmcnt(8)
	s_waitcnt lgkmcnt(0)
	s_barrier
	s_waitcnt lgkmcnt(0)
	v_mfma_f32_16x16x32_bf16 v[62:65], v[66:69], v[162:165], 0
	v_mfma_f32_16x16x32_bf16 v[58:61], v[82:85], v[162:165], 0
	v_mfma_f32_16x16x32_bf16 v[46:49], v[66:69], v[184:187], 0
	v_mfma_f32_16x16x32_bf16 v[42:45], v[82:85], v[184:187], 0
	v_mfma_f32_16x16x32_bf16 v[30:33], v[66:69], v[192:195], 0
	v_mfma_f32_16x16x32_bf16 v[26:29], v[82:85], v[192:195], 0
	v_mfma_f32_16x16x32_bf16 v[14:17], v[66:69], v[206:209], 0
	v_mfma_f32_16x16x32_bf16 v[10:13], v[82:85], v[206:209], 0
	v_mfma_f32_16x16x32_bf16 v[62:65], v[70:73], v[166:169], v[62:65]
	v_mfma_f32_16x16x32_bf16 v[58:61], v[86:89], v[166:169], v[58:61]
	v_mfma_f32_16x16x32_bf16 v[46:49], v[70:73], v[188:191], v[46:49]
	v_mfma_f32_16x16x32_bf16 v[42:45], v[86:89], v[188:191], v[42:45]
	v_mfma_f32_16x16x32_bf16 v[30:33], v[70:73], v[202:205], v[30:33]
	v_mfma_f32_16x16x32_bf16 v[26:29], v[86:89], v[202:205], v[26:29]
	v_mfma_f32_16x16x32_bf16 v[14:17], v[70:73], v[210:213], v[14:17]
	v_mfma_f32_16x16x32_bf16 v[10:13], v[86:89], v[210:213], v[10:13]
	v_mfma_f32_16x16x32_bf16 v[54:57], v[146:149], v[162:165], 0
	v_mfma_f32_16x16x32_bf16 v[50:53], v[154:157], v[162:165], 0
	v_mfma_f32_16x16x32_bf16 v[38:41], v[146:149], v[184:187], 0
	v_mfma_f32_16x16x32_bf16 v[34:37], v[154:157], v[184:187], 0
	v_mfma_f32_16x16x32_bf16 v[22:25], v[146:149], v[192:195], 0
	v_mfma_f32_16x16x32_bf16 v[18:21], v[154:157], v[192:195], 0
	v_mfma_f32_16x16x32_bf16 v[6:9], v[146:149], v[206:209], 0
	v_mfma_f32_16x16x32_bf16 v[2:5], v[154:157], v[206:209], 0
	v_mfma_f32_16x16x32_bf16 v[54:57], v[150:153], v[166:169], v[54:57]
	v_mfma_f32_16x16x32_bf16 v[50:53], v[158:161], v[166:169], v[50:53]
	v_mfma_f32_16x16x32_bf16 v[38:41], v[150:153], v[188:191], v[38:41]
	v_mfma_f32_16x16x32_bf16 v[34:37], v[158:161], v[188:191], v[34:37]
	v_mfma_f32_16x16x32_bf16 v[22:25], v[150:153], v[202:205], v[22:25]
	v_mfma_f32_16x16x32_bf16 v[18:21], v[158:161], v[202:205], v[18:21]
	v_mfma_f32_16x16x32_bf16 v[6:9], v[150:153], v[210:213], v[6:9]
	v_mfma_f32_16x16x32_bf16 v[2:5], v[158:161], v[210:213], v[2:5]
	s_barrier
	s_add_i32 s74, 0, 0x18000
	s_add_i32 s75, 0, 0x1c000
	v_add_u32_e32 v86, s74, v197
	v_add_u32_e32 v158, s75, v197
	ds_read_b128 v[66:69], v86
	ds_read_b128 v[70:73], v86 offset:1024
	ds_read_b128 v[82:85], v86 offset:2048
	ds_read_b128 v[86:89], v86 offset:3072
	ds_read_b128 v[146:149], v158
	ds_read_b128 v[150:153], v158 offset:1024
	ds_read_b128 v[154:157], v158 offset:2048
	ds_read_b128 v[158:161], v158 offset:3072
	s_add_u32 s26, s58, 0x40000
	s_addc_u32 s27, s59, 0
	s_mov_b32 m0, s61
	v_lshl_add_u64 v[222:223], s[26:27], 0, v[172:173]
	ds_read_b128 v[162:165], v201 offset:32768
	ds_read_b128 v[166:169], v201 offset:33792
	ds_read_b128 v[184:187], v201 offset:34816
	ds_read_b128 v[188:191], v201 offset:35840
	ds_read_b128 v[192:195], v201 offset:36864
	ds_read_b128 v[202:205], v201 offset:37888
	ds_read_b128 v[206:209], v201 offset:38912
	ds_read_b128 v[210:213], v201 offset:39936
	global_load_lds_dwordx4 v[222:223], off
	v_lshl_add_u64 v[222:223], s[26:27], 0, v[174:175]
	s_mov_b32 m0, s62
	s_nop 0
	global_load_lds_dwordx4 v[222:223], off
	s_waitcnt vmcnt(8)
	s_waitcnt lgkmcnt(0)
	s_barrier
	s_waitcnt lgkmcnt(0)
	v_mfma_f32_16x16x32_bf16 v[142:145], v[66:69], v[162:165], v[142:145]
	v_mfma_f32_16x16x32_bf16 v[138:141], v[82:85], v[162:165], v[138:141]
	v_mfma_f32_16x16x32_bf16 v[126:129], v[66:69], v[184:187], v[126:129]
	v_mfma_f32_16x16x32_bf16 v[122:125], v[82:85], v[184:187], v[122:125]
	v_mfma_f32_16x16x32_bf16 v[110:113], v[66:69], v[192:195], v[110:113]
	v_mfma_f32_16x16x32_bf16 v[106:109], v[82:85], v[192:195], v[106:109]
	v_mfma_f32_16x16x32_bf16 v[94:97], v[66:69], v[206:209], v[94:97]
	v_mfma_f32_16x16x32_bf16 v[90:93], v[82:85], v[206:209], v[90:93]
	v_mfma_f32_16x16x32_bf16 v[142:145], v[70:73], v[166:169], v[142:145]
	v_mfma_f32_16x16x32_bf16 v[138:141], v[86:89], v[166:169], v[138:141]
	v_mfma_f32_16x16x32_bf16 v[126:129], v[70:73], v[188:191], v[126:129]
	v_mfma_f32_16x16x32_bf16 v[122:125], v[86:89], v[188:191], v[122:125]
	v_mfma_f32_16x16x32_bf16 v[110:113], v[70:73], v[202:205], v[110:113]
	v_mfma_f32_16x16x32_bf16 v[106:109], v[86:89], v[202:205], v[106:109]
	v_mfma_f32_16x16x32_bf16 v[94:97], v[70:73], v[210:213], v[94:97]
	v_mfma_f32_16x16x32_bf16 v[90:93], v[86:89], v[210:213], v[90:93]
	v_mfma_f32_16x16x32_bf16 v[134:137], v[146:149], v[162:165], v[134:137]
	v_mfma_f32_16x16x32_bf16 v[130:133], v[154:157], v[162:165], v[130:133]
	v_mfma_f32_16x16x32_bf16 v[118:121], v[146:149], v[184:187], v[118:121]
	v_mfma_f32_16x16x32_bf16 v[114:117], v[154:157], v[184:187], v[114:117]
	v_mfma_f32_16x16x32_bf16 v[102:105], v[146:149], v[192:195], v[102:105]
	v_mfma_f32_16x16x32_bf16 v[98:101], v[154:157], v[192:195], v[98:101]
	v_mfma_f32_16x16x32_bf16 v[78:81], v[146:149], v[206:209], v[78:81]
	v_mfma_f32_16x16x32_bf16 v[74:77], v[154:157], v[206:209], v[74:77]
	v_mfma_f32_16x16x32_bf16 v[134:137], v[150:153], v[166:169], v[134:137]
	v_mfma_f32_16x16x32_bf16 v[130:133], v[158:161], v[166:169], v[130:133]
	v_mfma_f32_16x16x32_bf16 v[118:121], v[150:153], v[188:191], v[118:121]
	v_mfma_f32_16x16x32_bf16 v[114:117], v[158:161], v[188:191], v[114:117]
	v_mfma_f32_16x16x32_bf16 v[102:105], v[150:153], v[202:205], v[102:105]
	v_mfma_f32_16x16x32_bf16 v[98:101], v[158:161], v[202:205], v[98:101]
	v_mfma_f32_16x16x32_bf16 v[78:81], v[150:153], v[210:213], v[78:81]
	v_mfma_f32_16x16x32_bf16 v[74:77], v[158:161], v[210:213], v[74:77]
	s_barrier
	s_add_i32 s26, s74, s35
	v_lshl_add_u64 v[222:223], v[214:215], 0, s[16:17]
	s_mov_b32 m0, s26
	ds_read_b128 v[162:165], v201 offset:49152
	ds_read_b128 v[166:169], v201 offset:50176
	ds_read_b128 v[184:187], v201 offset:51200
	ds_read_b128 v[188:191], v201 offset:52224
	ds_read_b128 v[192:195], v201 offset:53248
	ds_read_b128 v[202:205], v201 offset:54272
	ds_read_b128 v[206:209], v201 offset:55296
	ds_read_b128 v[210:213], v201 offset:56320
	global_load_lds_dwordx4 v[222:223], off
	v_lshl_add_u64 v[222:223], v[214:215], 0, s[18:19]
	s_add_i32 m0, s26, 0x2000
	s_add_i32 s26, s75, s35
	global_load_lds_dwordx4 v[222:223], off
	v_lshl_add_u64 v[222:223], v[214:215], 0, s[22:23]
	s_mov_b32 m0, s26
	v_lshl_add_u64 v[214:215], v[214:215], 0, s[24:25]
	global_load_lds_dwordx4 v[222:223], off
	s_add_i32 m0, s26, 0x2000
	s_nop 0
	global_load_lds_dwordx4 v[214:215], off
	v_lshl_add_u64 v[214:215], v[216:217], 0, s[20:21]
	s_mov_b32 m0, s64
	s_nop 0
	global_load_lds_dwordx4 v[214:215], off
	v_lshl_add_u64 v[214:215], v[220:221], 0, s[20:21]
	s_mov_b32 m0, s65
	s_nop 0
	global_load_lds_dwordx4 v[214:215], off
	s_waitcnt vmcnt(8)
	s_waitcnt lgkmcnt(0)
	s_barrier
	s_waitcnt lgkmcnt(0)
	v_mfma_f32_16x16x32_bf16 v[62:65], v[66:69], v[162:165], v[62:65]
	v_mfma_f32_16x16x32_bf16 v[58:61], v[82:85], v[162:165], v[58:61]
	v_mfma_f32_16x16x32_bf16 v[46:49], v[66:69], v[184:187], v[46:49]
	v_mfma_f32_16x16x32_bf16 v[42:45], v[82:85], v[184:187], v[42:45]
	v_mfma_f32_16x16x32_bf16 v[30:33], v[66:69], v[192:195], v[30:33]
	v_mfma_f32_16x16x32_bf16 v[26:29], v[82:85], v[192:195], v[26:29]
	v_mfma_f32_16x16x32_bf16 v[14:17], v[66:69], v[206:209], v[14:17]
	v_mfma_f32_16x16x32_bf16 v[10:13], v[82:85], v[206:209], v[10:13]
	v_mfma_f32_16x16x32_bf16 v[62:65], v[70:73], v[166:169], v[62:65]
	v_mfma_f32_16x16x32_bf16 v[58:61], v[86:89], v[166:169], v[58:61]
	v_mfma_f32_16x16x32_bf16 v[46:49], v[70:73], v[188:191], v[46:49]
	v_mfma_f32_16x16x32_bf16 v[42:45], v[86:89], v[188:191], v[42:45]
	v_mfma_f32_16x16x32_bf16 v[30:33], v[70:73], v[202:205], v[30:33]
	v_mfma_f32_16x16x32_bf16 v[26:29], v[86:89], v[202:205], v[26:29]
	v_mfma_f32_16x16x32_bf16 v[14:17], v[70:73], v[210:213], v[14:17]
	v_mfma_f32_16x16x32_bf16 v[10:13], v[86:89], v[210:213], v[10:13]
	v_mfma_f32_16x16x32_bf16 v[54:57], v[146:149], v[162:165], v[54:57]
	v_mfma_f32_16x16x32_bf16 v[50:53], v[154:157], v[162:165], v[50:53]
	v_mfma_f32_16x16x32_bf16 v[38:41], v[146:149], v[184:187], v[38:41]
	v_mfma_f32_16x16x32_bf16 v[34:37], v[154:157], v[184:187], v[34:37]
	v_mfma_f32_16x16x32_bf16 v[22:25], v[146:149], v[192:195], v[22:25]
	v_mfma_f32_16x16x32_bf16 v[18:21], v[154:157], v[192:195], v[18:21]
	v_mfma_f32_16x16x32_bf16 v[6:9], v[146:149], v[206:209], v[6:9]
	v_mfma_f32_16x16x32_bf16 v[2:5], v[154:157], v[206:209], v[2:5]
	v_mfma_f32_16x16x32_bf16 v[54:57], v[150:153], v[166:169], v[54:57]
	v_mfma_f32_16x16x32_bf16 v[50:53], v[158:161], v[166:169], v[50:53]
	v_mfma_f32_16x16x32_bf16 v[38:41], v[150:153], v[188:191], v[38:41]
	v_mfma_f32_16x16x32_bf16 v[34:37], v[158:161], v[188:191], v[34:37]
	v_mfma_f32_16x16x32_bf16 v[22:25], v[150:153], v[202:205], v[22:25]
	v_mfma_f32_16x16x32_bf16 v[18:21], v[158:161], v[202:205], v[18:21]
	v_mfma_f32_16x16x32_bf16 v[6:9], v[150:153], v[210:213], v[6:9]
	v_mfma_f32_16x16x32_bf16 v[2:5], v[158:161], v[210:213], v[2:5]
	s_barrier
	s_add_i32 s73, s73, 2
	s_add_u32 s71, s71, 0x10000
	s_addc_u32 s72, s72, 0
	s_add_u32 s56, s56, 0x100
	s_addc_u32 s57, s57, 0
	s_cmp_gt_u32 s73, 13

.LBB0_1270:
	s_ashr_i32 s51, s50, 31
	s_lshl_b64 s[26:27], s[50:51], 20
	v_readlane_b32 s52, v254, 58
	v_readlane_b32 s53, v254, 59
	s_add_u32 s52, s52, s26
	s_addc_u32 s53, s53, s27
	s_and_b64 s[26:27], s[0:1], exec
	s_cselect_b32 s51, s53, s61
	s_cselect_b32 s57, s52, s60
	s_ashr_i32 s45, s44, 31
	s_lshl_b64 s[26:27], s[44:45], 20
	s_add_u32 s54, s3, s26
	s_addc_u32 s55, s33, s27
	s_and_b64 s[26:27], s[0:1], exec
	s_cselect_b32 s45, s55, s59
	s_cselect_b32 s73, s54, s58
	s_add_u32 s74, s58, 0x10000
	s_addc_u32 s75, s59, 0
	s_add_u32 s58, s60, 0x80080
	s_addc_u32 s59, s61, 0
	s_mov_b32 s80, -2
	ds_read_b128 v[144:147], v158
	ds_read_b128 v[148:151], v158 offset:1024
	ds_read_b128 v[152:155], v158 offset:2048
	ds_read_b128 v[162:165], v158 offset:3072
	ds_read_b128 v[166:169], v159
	ds_read_b128 v[170:173], v159 offset:1024
	ds_read_b128 v[174:177], v159 offset:2048
	ds_read_b128 v[178:181], v159 offset:3072
	s_add_u32 s26, s58, 0xfff80080
	s_addc_u32 s27, s59, -1
	s_cmp_eq_u32 s80, 28
	s_cselect_b32 s61, s51, s27
	s_cselect_b32 s60, s57, s26
	s_cselect_b32 s27, s45, s75
	s_cselect_b32 s26, s73, s74
	v_lshl_add_u64 v[214:215], s[58:59], 0, v[136:137]
	s_add_i32 m0, s63, 0xc000
	ds_read_b128 v[182:185], v160
	ds_read_b128 v[186:189], v160 offset:1024
	ds_read_b128 v[190:193], v160 offset:2048
	ds_read_b128 v[194:197], v160 offset:3072
	ds_read_b128 v[198:201], v160 offset:4096
	ds_read_b128 v[202:205], v160 offset:5120
	ds_read_b128 v[206:209], v160 offset:6144
	ds_read_b128 v[210:213], v160 offset:7168
	global_load_lds_dwordx4 v[214:215], off
	v_lshl_add_u64 v[214:215], s[58:59], 0, v[138:139]
	s_add_i32 m0, s63, 0xe000
	s_nop 0
	global_load_lds_dwordx4 v[214:215], off
	s_waitcnt vmcnt(8)
	s_waitcnt lgkmcnt(0)
	s_barrier
	s_waitcnt lgkmcnt(0)
	v_mfma_f32_16x16x32_bf16 v[126:129], v[144:147], v[182:185], 0
	v_mfma_f32_16x16x32_bf16 v[122:125], v[152:155], v[182:185], 0
	v_mfma_f32_16x16x32_bf16 v[118:121], v[144:147], v[190:193], 0
	v_mfma_f32_16x16x32_bf16 v[114:117], v[152:155], v[190:193], 0
	v_mfma_f32_16x16x32_bf16 v[106:109], v[144:147], v[198:201], 0
	v_mfma_f32_16x16x32_bf16 v[98:101], v[152:155], v[198:201], 0
	v_mfma_f32_16x16x32_bf16 v[90:93], v[144:147], v[206:209], 0
	v_mfma_f32_16x16x32_bf16 v[82:85], v[152:155], v[206:209], 0
	v_mfma_f32_16x16x32_bf16 v[126:129], v[148:151], v[186:189], v[126:129]
	v_mfma_f32_16x16x32_bf16 v[122:125], v[162:165], v[186:189], v[122:125]
	v_mfma_f32_16x16x32_bf16 v[118:121], v[148:151], v[194:197], v[118:121]
	v_mfma_f32_16x16x32_bf16 v[114:117], v[162:165], v[194:197], v[114:117]
	v_mfma_f32_16x16x32_bf16 v[106:109], v[148:151], v[202:205], v[106:109]
	v_mfma_f32_16x16x32_bf16 v[98:101], v[162:165], v[202:205], v[98:101]
	v_mfma_f32_16x16x32_bf16 v[90:93], v[148:151], v[210:213], v[90:93]
	v_mfma_f32_16x16x32_bf16 v[82:85], v[162:165], v[210:213], v[82:85]
	v_mfma_f32_16x16x32_bf16 v[110:113], v[166:169], v[182:185], 0
	v_mfma_f32_16x16x32_bf16 v[102:105], v[174:177], v[182:185], 0
	v_mfma_f32_16x16x32_bf16 v[94:97], v[166:169], v[190:193], 0
	v_mfma_f32_16x16x32_bf16 v[86:89], v[174:177], v[190:193], 0
	v_mfma_f32_16x16x32_bf16 v[78:81], v[166:169], v[198:201], 0
	v_mfma_f32_16x16x32_bf16 v[74:77], v[174:177], v[198:201], 0
	v_mfma_f32_16x16x32_bf16 v[70:73], v[166:169], v[206:209], 0
	v_mfma_f32_16x16x32_bf16 v[66:69], v[174:177], v[206:209], 0
	v_mfma_f32_16x16x32_bf16 v[110:113], v[170:173], v[186:189], v[110:113]
	v_mfma_f32_16x16x32_bf16 v[102:105], v[178:181], v[186:189], v[102:105]
	v_mfma_f32_16x16x32_bf16 v[94:97], v[170:173], v[194:197], v[94:97]
	v_mfma_f32_16x16x32_bf16 v[86:89], v[178:181], v[194:197], v[86:89]
	v_mfma_f32_16x16x32_bf16 v[78:81], v[170:173], v[202:205], v[78:81]
	v_mfma_f32_16x16x32_bf16 v[74:77], v[178:181], v[202:205], v[74:77]
	v_mfma_f32_16x16x32_bf16 v[70:73], v[170:173], v[210:213], v[70:73]
	v_mfma_f32_16x16x32_bf16 v[66:69], v[178:181], v[210:213], v[66:69]
	s_barrier
	v_lshl_add_u64 v[214:215], s[26:27], 0, v[130:131]
	s_add_i32 s26, s71, s35
	s_mov_b32 m0, s26
	ds_read_b128 v[182:185], v160 offset:16384
	ds_read_b128 v[186:189], v160 offset:17408
	ds_read_b128 v[190:193], v160 offset:18432
	ds_read_b128 v[194:197], v160 offset:19456
	ds_read_b128 v[198:201], v160 offset:20480
	ds_read_b128 v[202:205], v160 offset:21504
	ds_read_b128 v[206:209], v160 offset:22528
	ds_read_b128 v[210:213], v160 offset:23552
	global_load_lds_dwordx4 v[214:215], off
	v_lshl_add_u64 v[216:217], v[214:215], 0, s[6:7]
	s_add_i32 m0, s26, 0x2000
	s_add_i32 s26, s72, s35
	global_load_lds_dwordx4 v[216:217], off
	v_lshl_add_u64 v[216:217], v[214:215], 0, s[8:9]
	s_mov_b32 m0, s26
	v_lshl_add_u64 v[220:221], s[60:61], 0, v[134:135]
	global_load_lds_dwordx4 v[216:217], off
	v_lshl_add_u64 v[216:217], v[214:215], 0, s[10:11]
	s_add_i32 m0, s26, 0x2000
	s_nop 0
	global_load_lds_dwordx4 v[216:217], off
	v_lshl_add_u64 v[216:217], s[60:61], 0, v[132:133]
	s_mov_b32 m0, s63
	s_nop 0
	global_load_lds_dwordx4 v[216:217], off
	s_mov_b32 m0, s64
	s_nop 0
	global_load_lds_dwordx4 v[220:221], off
	s_waitcnt vmcnt(8)
	s_waitcnt lgkmcnt(0)
	s_barrier
	s_waitcnt lgkmcnt(0)
	v_mfma_f32_16x16x32_bf16 v[62:65], v[144:147], v[182:185], 0
	v_mfma_f32_16x16x32_bf16 v[58:61], v[152:155], v[182:185], 0
	v_mfma_f32_16x16x32_bf16 v[54:57], v[144:147], v[190:193], 0
	v_mfma_f32_16x16x32_bf16 v[46:49], v[152:155], v[190:193], 0
	v_mfma_f32_16x16x32_bf16 v[38:41], v[144:147], v[198:201], 0
	v_mfma_f32_16x16x32_bf16 v[30:33], v[152:155], v[198:201], 0
	v_mfma_f32_16x16x32_bf16 v[22:25], v[144:147], v[206:209], 0
	v_mfma_f32_16x16x32_bf16 v[14:17], v[152:155], v[206:209], 0
	v_mfma_f32_16x16x32_bf16 v[62:65], v[148:151], v[186:189], v[62:65]
	v_mfma_f32_16x16x32_bf16 v[58:61], v[162:165], v[186:189], v[58:61]
	v_mfma_f32_16x16x32_bf16 v[54:57], v[148:151], v[194:197], v[54:57]
	v_mfma_f32_16x16x32_bf16 v[46:49], v[162:165], v[194:197], v[46:49]
	v_mfma_f32_16x16x32_bf16 v[38:41], v[148:151], v[202:205], v[38:41]
	v_mfma_f32_16x16x32_bf16 v[30:33], v[162:165], v[202:205], v[30:33]
	v_mfma_f32_16x16x32_bf16 v[22:25], v[148:151], v[210:213], v[22:25]
	v_mfma_f32_16x16x32_bf16 v[14:17], v[162:165], v[210:213], v[14:17]
	v_mfma_f32_16x16x32_bf16 v[50:53], v[166:169], v[182:185], 0
	v_mfma_f32_16x16x32_bf16 v[42:45], v[174:177], v[182:185], 0
	v_mfma_f32_16x16x32_bf16 v[34:37], v[166:169], v[190:193], 0
	v_mfma_f32_16x16x32_bf16 v[26:29], v[174:177], v[190:193], 0
	v_mfma_f32_16x16x32_bf16 v[18:21], v[166:169], v[198:201], 0
	v_mfma_f32_16x16x32_bf16 v[10:13], v[174:177], v[198:201], 0
	v_mfma_f32_16x16x32_bf16 v[6:9], v[166:169], v[206:209], 0
	v_mfma_f32_16x16x32_bf16 v[2:5], v[174:177], v[206:209], 0
	v_mfma_f32_16x16x32_bf16 v[50:53], v[170:173], v[186:189], v[50:53]
	v_mfma_f32_16x16x32_bf16 v[42:45], v[178:181], v[186:189], v[42:45]
	v_mfma_f32_16x16x32_bf16 v[34:37], v[170:173], v[194:197], v[34:37]
	v_mfma_f32_16x16x32_bf16 v[26:29], v[178:181], v[194:197], v[26:29]
	v_mfma_f32_16x16x32_bf16 v[18:21], v[170:173], v[202:205], v[18:21]
	v_mfma_f32_16x16x32_bf16 v[10:13], v[178:181], v[202:205], v[10:13]
	v_mfma_f32_16x16x32_bf16 v[6:9], v[170:173], v[210:213], v[6:9]
	v_mfma_f32_16x16x32_bf16 v[2:5], v[178:181], v[210:213], v[2:5]
	s_barrier
	s_add_i32 s81, 0, 0x18000
	v_add_u32_e32 v161, s81, v156
	s_add_i32 s82, 0, 0x1c000
	ds_read_b128 v[144:147], v161
	ds_read_b128 v[148:151], v161 offset:1024
	ds_read_b128 v[152:155], v161 offset:2048
	ds_read_b128 v[162:165], v161 offset:3072
	v_add_u32_e32 v161, s82, v156
	ds_read_b128 v[166:169], v161
	ds_read_b128 v[170:173], v161 offset:1024
	ds_read_b128 v[174:177], v161 offset:2048
	ds_read_b128 v[178:181], v161 offset:3072
	s_add_u32 s26, s60, 0x80000
	s_addc_u32 s27, s61, 0
	s_mov_b32 m0, s65
	v_lshl_add_u64 v[222:223], s[26:27], 0, v[132:133]
	ds_read_b128 v[182:185], v160 offset:32768
	ds_read_b128 v[186:189], v160 offset:33792
	ds_read_b128 v[190:193], v160 offset:34816
	ds_read_b128 v[194:197], v160 offset:35840
	ds_read_b128 v[198:201], v160 offset:36864
	ds_read_b128 v[202:205], v160 offset:37888
	ds_read_b128 v[206:209], v160 offset:38912
	ds_read_b128 v[210:213], v160 offset:39936
	global_load_lds_dwordx4 v[222:223], off
	v_lshl_add_u64 v[222:223], s[26:27], 0, v[134:135]
	s_mov_b32 m0, s66
	s_nop 0
	global_load_lds_dwordx4 v[222:223], off
	s_waitcnt vmcnt(8)
	s_waitcnt lgkmcnt(0)
	s_barrier
	s_waitcnt lgkmcnt(0)
	v_mfma_f32_16x16x32_bf16 v[126:129], v[144:147], v[182:185], v[126:129]
	v_mfma_f32_16x16x32_bf16 v[122:125], v[152:155], v[182:185], v[122:125]
	v_mfma_f32_16x16x32_bf16 v[118:121], v[144:147], v[190:193], v[118:121]
	v_mfma_f32_16x16x32_bf16 v[114:117], v[152:155], v[190:193], v[114:117]
	v_mfma_f32_16x16x32_bf16 v[106:109], v[144:147], v[198:201], v[106:109]
	v_mfma_f32_16x16x32_bf16 v[98:101], v[152:155], v[198:201], v[98:101]
	v_mfma_f32_16x16x32_bf16 v[90:93], v[144:147], v[206:209], v[90:93]
	v_mfma_f32_16x16x32_bf16 v[82:85], v[152:155], v[206:209], v[82:85]
	v_mfma_f32_16x16x32_bf16 v[126:129], v[148:151], v[186:189], v[126:129]
	v_mfma_f32_16x16x32_bf16 v[122:125], v[162:165], v[186:189], v[122:125]
	v_mfma_f32_16x16x32_bf16 v[118:121], v[148:151], v[194:197], v[118:121]
	v_mfma_f32_16x16x32_bf16 v[114:117], v[162:165], v[194:197], v[114:117]
	v_mfma_f32_16x16x32_bf16 v[106:109], v[148:151], v[202:205], v[106:109]
	v_mfma_f32_16x16x32_bf16 v[98:101], v[162:165], v[202:205], v[98:101]
	v_mfma_f32_16x16x32_bf16 v[90:93], v[148:151], v[210:213], v[90:93]
	v_mfma_f32_16x16x32_bf16 v[82:85], v[162:165], v[210:213], v[82:85]
	v_mfma_f32_16x16x32_bf16 v[110:113], v[166:169], v[182:185], v[110:113]
	v_mfma_f32_16x16x32_bf16 v[102:105], v[174:177], v[182:185], v[102:105]
	v_mfma_f32_16x16x32_bf16 v[94:97], v[166:169], v[190:193], v[94:97]
	v_mfma_f32_16x16x32_bf16 v[86:89], v[174:177], v[190:193], v[86:89]
	v_mfma_f32_16x16x32_bf16 v[78:81], v[166:169], v[198:201], v[78:81]
	v_mfma_f32_16x16x32_bf16 v[74:77], v[174:177], v[198:201], v[74:77]
	v_mfma_f32_16x16x32_bf16 v[70:73], v[166:169], v[206:209], v[70:73]
	v_mfma_f32_16x16x32_bf16 v[66:69], v[174:177], v[206:209], v[66:69]
	v_mfma_f32_16x16x32_bf16 v[110:113], v[170:173], v[186:189], v[110:113]
	v_mfma_f32_16x16x32_bf16 v[102:105], v[178:181], v[186:189], v[102:105]
	v_mfma_f32_16x16x32_bf16 v[94:97], v[170:173], v[194:197], v[94:97]
	v_mfma_f32_16x16x32_bf16 v[86:89], v[178:181], v[194:197], v[86:89]
	v_mfma_f32_16x16x32_bf16 v[78:81], v[170:173], v[202:205], v[78:81]
	v_mfma_f32_16x16x32_bf16 v[74:77], v[178:181], v[202:205], v[74:77]
	v_mfma_f32_16x16x32_bf16 v[70:73], v[170:173], v[210:213], v[70:73]
	v_mfma_f32_16x16x32_bf16 v[66:69], v[178:181], v[210:213], v[66:69]
	s_barrier
	s_add_i32 s26, s81, s35
	v_lshl_add_u64 v[222:223], v[214:215], 0, s[14:15]
	s_mov_b32 m0, s26
	ds_read_b128 v[182:185], v160 offset:49152
	ds_read_b128 v[186:189], v160 offset:50176
	ds_read_b128 v[190:193], v160 offset:51200
	ds_read_b128 v[194:197], v160 offset:52224
	ds_read_b128 v[198:201], v160 offset:53248
	ds_read_b128 v[202:205], v160 offset:54272
	ds_read_b128 v[206:209], v160 offset:55296
	ds_read_b128 v[210:213], v160 offset:56320
	global_load_lds_dwordx4 v[222:223], off
	v_lshl_add_u64 v[222:223], v[214:215], 0, s[16:17]
	s_add_i32 m0, s26, 0x2000
	s_add_i32 s26, s82, s35
	global_load_lds_dwordx4 v[222:223], off
	v_lshl_add_u64 v[222:223], v[214:215], 0, s[20:21]
	s_mov_b32 m0, s26
	v_lshl_add_u64 v[214:215], v[214:215], 0, s[22:23]
	global_load_lds_dwordx4 v[222:223], off
	s_add_i32 m0, s26, 0x2000
	s_nop 0
	global_load_lds_dwordx4 v[214:215], off
	v_lshl_add_u64 v[214:215], v[216:217], 0, s[18:19]
	s_mov_b32 m0, s68
	s_nop 0
	global_load_lds_dwordx4 v[214:215], off
	v_lshl_add_u64 v[214:215], v[220:221], 0, s[18:19]
	s_mov_b32 m0, s69
	s_nop 0
	global_load_lds_dwordx4 v[214:215], off
	s_waitcnt vmcnt(8)
	s_waitcnt lgkmcnt(0)
	s_barrier
	s_waitcnt lgkmcnt(0)
	v_mfma_f32_16x16x32_bf16 v[62:65], v[144:147], v[182:185], v[62:65]
	v_mfma_f32_16x16x32_bf16 v[58:61], v[152:155], v[182:185], v[58:61]
	v_mfma_f32_16x16x32_bf16 v[54:57], v[144:147], v[190:193], v[54:57]
	v_mfma_f32_16x16x32_bf16 v[46:49], v[152:155], v[190:193], v[46:49]
	v_mfma_f32_16x16x32_bf16 v[38:41], v[144:147], v[198:201], v[38:41]
	v_mfma_f32_16x16x32_bf16 v[30:33], v[152:155], v[198:201], v[30:33]
	v_mfma_f32_16x16x32_bf16 v[22:25], v[144:147], v[206:209], v[22:25]
	v_mfma_f32_16x16x32_bf16 v[14:17], v[152:155], v[206:209], v[14:17]
	v_mfma_f32_16x16x32_bf16 v[62:65], v[148:151], v[186:189], v[62:65]
	v_mfma_f32_16x16x32_bf16 v[58:61], v[162:165], v[186:189], v[58:61]
	v_mfma_f32_16x16x32_bf16 v[54:57], v[148:151], v[194:197], v[54:57]
	v_mfma_f32_16x16x32_bf16 v[46:49], v[162:165], v[194:197], v[46:49]
	v_mfma_f32_16x16x32_bf16 v[38:41], v[148:151], v[202:205], v[38:41]
	v_mfma_f32_16x16x32_bf16 v[30:33], v[162:165], v[202:205], v[30:33]
	v_mfma_f32_16x16x32_bf16 v[22:25], v[148:151], v[210:213], v[22:25]
	v_mfma_f32_16x16x32_bf16 v[14:17], v[162:165], v[210:213], v[14:17]
	v_mfma_f32_16x16x32_bf16 v[50:53], v[166:169], v[182:185], v[50:53]
	v_mfma_f32_16x16x32_bf16 v[42:45], v[174:177], v[182:185], v[42:45]
	v_mfma_f32_16x16x32_bf16 v[34:37], v[166:169], v[190:193], v[34:37]
	v_mfma_f32_16x16x32_bf16 v[26:29], v[174:177], v[190:193], v[26:29]
	v_mfma_f32_16x16x32_bf16 v[18:21], v[166:169], v[198:201], v[18:21]
	v_mfma_f32_16x16x32_bf16 v[10:13], v[174:177], v[198:201], v[10:13]
	v_mfma_f32_16x16x32_bf16 v[6:9], v[166:169], v[206:209], v[6:9]
	v_mfma_f32_16x16x32_bf16 v[2:5], v[174:177], v[206:209], v[2:5]
	v_mfma_f32_16x16x32_bf16 v[50:53], v[170:173], v[186:189], v[50:53]
	v_mfma_f32_16x16x32_bf16 v[42:45], v[178:181], v[186:189], v[42:45]
	v_mfma_f32_16x16x32_bf16 v[34:37], v[170:173], v[194:197], v[34:37]
	v_mfma_f32_16x16x32_bf16 v[26:29], v[178:181], v[194:197], v[26:29]
	v_mfma_f32_16x16x32_bf16 v[18:21], v[170:173], v[202:205], v[18:21]
	v_mfma_f32_16x16x32_bf16 v[10:13], v[178:181], v[202:205], v[10:13]
	v_mfma_f32_16x16x32_bf16 v[6:9], v[170:173], v[210:213], v[6:9]
	v_mfma_f32_16x16x32_bf16 v[2:5], v[178:181], v[210:213], v[2:5]
	s_barrier
	s_add_i32 s80, s80, 2
	s_add_u32 s74, s74, 0x10000
	s_addc_u32 s75, s75, 0
	s_add_u32 s58, s58, 0x100
	s_addc_u32 s59, s59, 0
	s_cmp_gt_u32 s80, 29

.LBB0_1496:
	s_lshl_b64 s[50:51], s[48:49], 19
	s_add_u32 s50, s59, s50
	s_addc_u32 s51, s60, s51
	s_and_b64 s[4:5], s[4:5], exec
	s_cselect_b32 s2, s51, s57
	s_cselect_b32 s47, s50, s56
	s_add_u32 s4, s56, 0x40080
	v_lshl_add_u64 v[176:177], v[2:3], 0, s[40:41]
	s_addc_u32 s5, s57, 0
	s_mov_b32 s49, -2
	ds_read_b128 v[26:29], v186
	ds_read_b128 v[30:33], v186 offset:1024
	ds_read_b128 v[18:21], v186 offset:2048
	ds_read_b128 v[22:25], v186 offset:3072
	ds_read_b128 v[10:13], v187
	ds_read_b128 v[14:17], v187 offset:1024
	ds_read_b128 v[2:5], v187 offset:2048
	ds_read_b128 v[6:9], v187 offset:3072
	s_add_u32 s56, s4, 0xfffc0080
	s_addc_u32 s57, s5, -1
	s_cmp_eq_u32 s49, 12
	s_cselect_b64 vcc, -1, 0
	s_cselect_b32 s57, s2, s57
	s_cselect_b32 s56, s47, s56
	v_cndmask_b32_e32 v179, v177, v175, vcc
	v_cndmask_b32_e32 v178, v176, v174, vcc
	v_lshl_add_u64 v[180:181], s[4:5], 0, v[168:169]
	s_add_i32 m0, s62, 0xc000
	ds_read_b128 v[192:195], v188
	ds_read_b128 v[196:199], v188 offset:1024
	ds_read_b128 v[200:203], v188 offset:2048
	ds_read_b128 v[204:207], v188 offset:3072
	ds_read_b128 v[208:211], v188 offset:4096
	ds_read_b128 v[212:215], v188 offset:5120
	ds_read_b128 v[220:223], v188 offset:6144
	ds_read_b128 v[224:227], v188 offset:7168
	global_load_lds_dwordx4 v[180:181], off
	v_lshl_add_u64 v[180:181], s[4:5], 0, v[170:171]
	s_add_i32 m0, s62, 0xe000
	s_nop 0
	global_load_lds_dwordx4 v[180:181], off
	s_waitcnt vmcnt(8)
	s_waitcnt lgkmcnt(0)
	s_barrier
	s_waitcnt lgkmcnt(0)
	v_mfma_scale_f32_16x16x128_f8f6f4 v[158:161], v[26:33], v[192:199], 0, v189, v190 op_sel_hi:[0,0,0]
	v_mfma_scale_f32_16x16x128_f8f6f4 v[150:153], v[18:25], v[192:199], 0, v189, v190 op_sel_hi:[0,0,0]
	v_mfma_scale_f32_16x16x128_f8f6f4 v[142:145], v[26:33], v[200:207], 0, v189, v190 op_sel_hi:[0,0,0]
	v_mfma_scale_f32_16x16x128_f8f6f4 v[134:137], v[18:25], v[200:207], 0, v189, v190 op_sel_hi:[0,0,0]
	v_mfma_scale_f32_16x16x128_f8f6f4 v[126:129], v[26:33], v[208:215], 0, v189, v190 op_sel_hi:[0,0,0]
	v_mfma_scale_f32_16x16x128_f8f6f4 v[118:121], v[18:25], v[208:215], 0, v189, v190 op_sel_hi:[0,0,0]
	v_mfma_scale_f32_16x16x128_f8f6f4 v[110:113], v[26:33], v[220:227], 0, v189, v190 op_sel_hi:[0,0,0]
	v_mfma_scale_f32_16x16x128_f8f6f4 v[102:105], v[18:25], v[220:227], 0, v189, v190 op_sel_hi:[0,0,0]
	v_mfma_scale_f32_16x16x128_f8f6f4 v[154:157], v[10:17], v[192:199], 0, v189, v190 op_sel_hi:[0,0,0]
	v_mfma_scale_f32_16x16x128_f8f6f4 v[146:149], v[2:9], v[192:199], 0, v189, v190 op_sel_hi:[0,0,0]
	v_mfma_scale_f32_16x16x128_f8f6f4 v[138:141], v[10:17], v[200:207], 0, v189, v190 op_sel_hi:[0,0,0]
	v_mfma_scale_f32_16x16x128_f8f6f4 v[130:133], v[2:9], v[200:207], 0, v189, v190 op_sel_hi:[0,0,0]
	v_mfma_scale_f32_16x16x128_f8f6f4 v[122:125], v[10:17], v[208:215], 0, v189, v190 op_sel_hi:[0,0,0]
	v_mfma_scale_f32_16x16x128_f8f6f4 v[114:117], v[2:9], v[208:215], 0, v189, v190 op_sel_hi:[0,0,0]
	v_mfma_scale_f32_16x16x128_f8f6f4 v[106:109], v[10:17], v[220:227], 0, v189, v190 op_sel_hi:[0,0,0]
	v_mfma_scale_f32_16x16x128_f8f6f4 v[98:101], v[2:9], v[220:227], 0, v189, v190 op_sel_hi:[0,0,0]
	s_barrier
	s_add_i32 s73, s69, s61
	v_lshl_add_u64 v[178:179], v[178:179], 0, v[162:163]
	s_mov_b32 m0, s73
	ds_read_b128 v[192:195], v188 offset:16384
	ds_read_b128 v[196:199], v188 offset:17408
	ds_read_b128 v[200:203], v188 offset:18432
	ds_read_b128 v[204:207], v188 offset:19456
	ds_read_b128 v[208:211], v188 offset:20480
	ds_read_b128 v[212:215], v188 offset:21504
	ds_read_b128 v[220:223], v188 offset:22528
	ds_read_b128 v[224:227], v188 offset:23552
	global_load_lds_dwordx4 v[178:179], off
	v_lshl_add_u64 v[180:181], v[178:179], 0, s[10:11]
	s_add_i32 m0, s73, 0x2000
	s_add_i32 s73, s70, s61
	global_load_lds_dwordx4 v[180:181], off
	v_lshl_add_u64 v[180:181], v[178:179], 0, s[12:13]
	s_mov_b32 m0, s73
	v_lshl_add_u64 v[182:183], s[56:57], 0, v[166:167]
	global_load_lds_dwordx4 v[180:181], off
	v_lshl_add_u64 v[180:181], v[178:179], 0, s[14:15]
	s_add_i32 m0, s73, 0x2000
	s_nop 0
	global_load_lds_dwordx4 v[180:181], off
	v_lshl_add_u64 v[180:181], s[56:57], 0, v[164:165]
	s_mov_b32 m0, s62
	s_nop 0
	global_load_lds_dwordx4 v[180:181], off
	s_mov_b32 m0, s53
	s_nop 0
	global_load_lds_dwordx4 v[182:183], off
	s_waitcnt vmcnt(8)
	s_waitcnt lgkmcnt(0)
	s_barrier
	s_waitcnt lgkmcnt(0)
	v_mfma_scale_f32_16x16x128_f8f6f4 v[94:97], v[26:33], v[192:199], 0, v189, v190 op_sel_hi:[0,0,0]
	v_mfma_scale_f32_16x16x128_f8f6f4 v[86:89], v[18:25], v[192:199], 0, v189, v190 op_sel_hi:[0,0,0]
	v_mfma_scale_f32_16x16x128_f8f6f4 v[78:81], v[26:33], v[200:207], 0, v189, v190 op_sel_hi:[0,0,0]
	v_mfma_scale_f32_16x16x128_f8f6f4 v[70:73], v[18:25], v[200:207], 0, v189, v190 op_sel_hi:[0,0,0]
	v_mfma_scale_f32_16x16x128_f8f6f4 v[62:65], v[26:33], v[208:215], 0, v189, v190 op_sel_hi:[0,0,0]
	v_mfma_scale_f32_16x16x128_f8f6f4 v[54:57], v[18:25], v[208:215], 0, v189, v190 op_sel_hi:[0,0,0]
	v_mfma_scale_f32_16x16x128_f8f6f4 v[46:49], v[26:33], v[220:227], 0, v189, v190 op_sel_hi:[0,0,0]
	v_mfma_scale_f32_16x16x128_f8f6f4 v[38:41], v[18:25], v[220:227], 0, v189, v190 op_sel_hi:[0,0,0]
	v_mfma_scale_f32_16x16x128_f8f6f4 v[90:93], v[10:17], v[192:199], 0, v189, v190 op_sel_hi:[0,0,0]
	v_mfma_scale_f32_16x16x128_f8f6f4 v[82:85], v[2:9], v[192:199], 0, v189, v190 op_sel_hi:[0,0,0]
	v_mfma_scale_f32_16x16x128_f8f6f4 v[74:77], v[10:17], v[200:207], 0, v189, v190 op_sel_hi:[0,0,0]
	v_mfma_scale_f32_16x16x128_f8f6f4 v[66:69], v[2:9], v[200:207], 0, v189, v190 op_sel_hi:[0,0,0]
	v_mfma_scale_f32_16x16x128_f8f6f4 v[58:61], v[10:17], v[208:215], 0, v189, v190 op_sel_hi:[0,0,0]
	v_mfma_scale_f32_16x16x128_f8f6f4 v[50:53], v[2:9], v[208:215], 0, v189, v190 op_sel_hi:[0,0,0]
	v_mfma_scale_f32_16x16x128_f8f6f4 v[42:45], v[10:17], v[220:227], 0, v189, v190 op_sel_hi:[0,0,0]
	v_mfma_scale_f32_16x16x128_f8f6f4 v[34:37], v[2:9], v[220:227], 0, v189, v190 op_sel_hi:[0,0,0]
	s_barrier
	s_add_i32 s73, 0, 0x18000
	s_add_i32 s74, 0, 0x1c000
	v_add_u32_e32 v14, s73, v184
	v_add_u32_e32 v30, s74, v184
	ds_read_b128 v[2:5], v14
	ds_read_b128 v[6:9], v14 offset:1024
	ds_read_b128 v[10:13], v14 offset:2048
	ds_read_b128 v[14:17], v14 offset:3072
	ds_read_b128 v[18:21], v30
	ds_read_b128 v[22:25], v30 offset:1024
	ds_read_b128 v[26:29], v30 offset:2048
	ds_read_b128 v[30:33], v30 offset:3072
	s_add_u32 s56, s56, 0x40000
	s_addc_u32 s57, s57, 0
	s_mov_b32 m0, s63
	v_lshl_add_u64 v[216:217], s[56:57], 0, v[164:165]
	ds_read_b128 v[192:195], v188 offset:32768
	ds_read_b128 v[196:199], v188 offset:33792
	ds_read_b128 v[200:203], v188 offset:34816
	ds_read_b128 v[204:207], v188 offset:35840
	ds_read_b128 v[208:211], v188 offset:36864
	ds_read_b128 v[212:215], v188 offset:37888
	ds_read_b128 v[220:223], v188 offset:38912
	ds_read_b128 v[224:227], v188 offset:39936
	global_load_lds_dwordx4 v[216:217], off
	v_lshl_add_u64 v[216:217], s[56:57], 0, v[166:167]
	s_mov_b32 m0, s64
	s_nop 0
	global_load_lds_dwordx4 v[216:217], off
	s_waitcnt vmcnt(8)
	s_waitcnt lgkmcnt(0)
	s_barrier
	s_waitcnt lgkmcnt(0)
	v_mfma_scale_f32_16x16x128_f8f6f4 v[158:161], v[2:9], v[192:199], v[158:161], v189, v190 op_sel_hi:[0,0,0]
	v_mfma_scale_f32_16x16x128_f8f6f4 v[150:153], v[10:17], v[192:199], v[150:153], v189, v190 op_sel_hi:[0,0,0]
	v_mfma_scale_f32_16x16x128_f8f6f4 v[142:145], v[2:9], v[200:207], v[142:145], v189, v190 op_sel_hi:[0,0,0]
	v_mfma_scale_f32_16x16x128_f8f6f4 v[134:137], v[10:17], v[200:207], v[134:137], v189, v190 op_sel_hi:[0,0,0]
	v_mfma_scale_f32_16x16x128_f8f6f4 v[126:129], v[2:9], v[208:215], v[126:129], v189, v190 op_sel_hi:[0,0,0]
	v_mfma_scale_f32_16x16x128_f8f6f4 v[118:121], v[10:17], v[208:215], v[118:121], v189, v190 op_sel_hi:[0,0,0]
	v_mfma_scale_f32_16x16x128_f8f6f4 v[110:113], v[2:9], v[220:227], v[110:113], v189, v190 op_sel_hi:[0,0,0]
	v_mfma_scale_f32_16x16x128_f8f6f4 v[102:105], v[10:17], v[220:227], v[102:105], v189, v190 op_sel_hi:[0,0,0]
	v_mfma_scale_f32_16x16x128_f8f6f4 v[154:157], v[18:25], v[192:199], v[154:157], v189, v190 op_sel_hi:[0,0,0]
	v_mfma_scale_f32_16x16x128_f8f6f4 v[146:149], v[26:33], v[192:199], v[146:149], v189, v190 op_sel_hi:[0,0,0]
	v_mfma_scale_f32_16x16x128_f8f6f4 v[138:141], v[18:25], v[200:207], v[138:141], v189, v190 op_sel_hi:[0,0,0]
	v_mfma_scale_f32_16x16x128_f8f6f4 v[130:133], v[26:33], v[200:207], v[130:133], v189, v190 op_sel_hi:[0,0,0]
	v_mfma_scale_f32_16x16x128_f8f6f4 v[122:125], v[18:25], v[208:215], v[122:125], v189, v190 op_sel_hi:[0,0,0]
	v_mfma_scale_f32_16x16x128_f8f6f4 v[114:117], v[26:33], v[208:215], v[114:117], v189, v190 op_sel_hi:[0,0,0]
	v_mfma_scale_f32_16x16x128_f8f6f4 v[106:109], v[18:25], v[220:227], v[106:109], v189, v190 op_sel_hi:[0,0,0]
	v_mfma_scale_f32_16x16x128_f8f6f4 v[98:101], v[26:33], v[220:227], v[98:101], v189, v190 op_sel_hi:[0,0,0]
	s_barrier
	s_add_i32 s56, s73, s61
	v_lshl_add_u64 v[216:217], v[178:179], 0, s[20:21]
	s_mov_b32 m0, s56
	ds_read_b128 v[192:195], v188 offset:49152
	ds_read_b128 v[196:199], v188 offset:50176
	ds_read_b128 v[200:203], v188 offset:51200
	ds_read_b128 v[204:207], v188 offset:52224
	ds_read_b128 v[208:211], v188 offset:53248
	ds_read_b128 v[212:215], v188 offset:54272
	ds_read_b128 v[220:223], v188 offset:55296
	ds_read_b128 v[224:227], v188 offset:56320
	global_load_lds_dwordx4 v[216:217], off
	v_lshl_add_u64 v[216:217], v[178:179], 0, s[22:23]
	s_add_i32 m0, s56, 0x2000
	s_add_i32 s56, s74, s61
	global_load_lds_dwordx4 v[216:217], off
	v_lshl_add_u64 v[216:217], v[178:179], 0, s[26:27]
	s_mov_b32 m0, s56
	v_lshl_add_u64 v[178:179], v[178:179], 0, s[36:37]
	global_load_lds_dwordx4 v[216:217], off
	s_add_i32 m0, s56, 0x2000
	s_nop 0
	global_load_lds_dwordx4 v[178:179], off
	v_lshl_add_u64 v[178:179], v[180:181], 0, s[24:25]
	s_mov_b32 m0, s66
	s_nop 0
	global_load_lds_dwordx4 v[178:179], off
	v_lshl_add_u64 v[178:179], v[182:183], 0, s[24:25]
	s_mov_b32 m0, s67
	s_nop 0
	global_load_lds_dwordx4 v[178:179], off
	s_waitcnt vmcnt(8)
	s_waitcnt lgkmcnt(0)
	s_barrier
	s_waitcnt lgkmcnt(0)
	v_mfma_scale_f32_16x16x128_f8f6f4 v[94:97], v[2:9], v[192:199], v[94:97], v189, v190 op_sel_hi:[0,0,0]
	v_mfma_scale_f32_16x16x128_f8f6f4 v[86:89], v[10:17], v[192:199], v[86:89], v189, v190 op_sel_hi:[0,0,0]
	v_mfma_scale_f32_16x16x128_f8f6f4 v[78:81], v[2:9], v[200:207], v[78:81], v189, v190 op_sel_hi:[0,0,0]
	v_mfma_scale_f32_16x16x128_f8f6f4 v[70:73], v[10:17], v[200:207], v[70:73], v189, v190 op_sel_hi:[0,0,0]
	v_mfma_scale_f32_16x16x128_f8f6f4 v[62:65], v[2:9], v[208:215], v[62:65], v189, v190 op_sel_hi:[0,0,0]
	v_mfma_scale_f32_16x16x128_f8f6f4 v[54:57], v[10:17], v[208:215], v[54:57], v189, v190 op_sel_hi:[0,0,0]
	v_mfma_scale_f32_16x16x128_f8f6f4 v[46:49], v[2:9], v[220:227], v[46:49], v189, v190 op_sel_hi:[0,0,0]
	v_mfma_scale_f32_16x16x128_f8f6f4 v[38:41], v[10:17], v[220:227], v[38:41], v189, v190 op_sel_hi:[0,0,0]
	v_mfma_scale_f32_16x16x128_f8f6f4 v[90:93], v[18:25], v[192:199], v[90:93], v189, v190 op_sel_hi:[0,0,0]
	v_mfma_scale_f32_16x16x128_f8f6f4 v[82:85], v[26:33], v[192:199], v[82:85], v189, v190 op_sel_hi:[0,0,0]
	v_mfma_scale_f32_16x16x128_f8f6f4 v[74:77], v[18:25], v[200:207], v[74:77], v189, v190 op_sel_hi:[0,0,0]
	v_mfma_scale_f32_16x16x128_f8f6f4 v[66:69], v[26:33], v[200:207], v[66:69], v189, v190 op_sel_hi:[0,0,0]
	v_mfma_scale_f32_16x16x128_f8f6f4 v[58:61], v[18:25], v[208:215], v[58:61], v189, v190 op_sel_hi:[0,0,0]
	v_mfma_scale_f32_16x16x128_f8f6f4 v[50:53], v[26:33], v[208:215], v[50:53], v189, v190 op_sel_hi:[0,0,0]
	v_mfma_scale_f32_16x16x128_f8f6f4 v[42:45], v[18:25], v[220:227], v[42:45], v189, v190 op_sel_hi:[0,0,0]
	v_mfma_scale_f32_16x16x128_f8f6f4 v[34:37], v[26:33], v[220:227], v[34:37], v189, v190 op_sel_hi:[0,0,0]
	s_barrier
	s_add_i32 s49, s49, 2
	s_add_u32 s4, s4, 0x100
	s_addc_u32 s5, s5, 0
	s_cmp_gt_u32 s49, 13
	v_lshl_add_u64 v[176:177], v[176:177], 0, s[40:41]

.LBB0_1567:
	s_add_u32 s56, s56, 0xb0080
	v_lshl_add_u64 v[176:177], v[2:3], 0, s[44:45]
	s_addc_u32 s57, s57, 0
	s_mov_b32 s53, -2
	ds_read_b128 v[26:29], v186
	ds_read_b128 v[30:33], v186 offset:1024
	ds_read_b128 v[18:21], v186 offset:2048
	ds_read_b128 v[22:25], v186 offset:3072
	ds_read_b128 v[10:13], v187
	ds_read_b128 v[14:17], v187 offset:1024
	ds_read_b128 v[2:5], v187 offset:2048
	ds_read_b128 v[6:9], v187 offset:3072
	s_add_u32 s58, s56, 0xfff50080
	s_addc_u32 s59, s57, -1
	s_cmp_eq_u32 s53, 40
	s_cselect_b64 vcc, -1, 0
	s_cselect_b32 s59, s5, s59
	s_cselect_b32 s58, s4, s58
	v_cndmask_b32_e32 v179, v177, v175, vcc
	v_cndmask_b32_e32 v178, v176, v174, vcc
	v_lshl_add_u64 v[180:181], s[56:57], 0, v[170:171]
	s_add_i32 m0, s61, 0xc000
	ds_read_b128 v[192:195], v188
	ds_read_b128 v[196:199], v188 offset:1024
	ds_read_b128 v[200:203], v188 offset:2048
	ds_read_b128 v[204:207], v188 offset:3072
	ds_read_b128 v[208:211], v188 offset:4096
	ds_read_b128 v[212:215], v188 offset:5120
	ds_read_b128 v[220:223], v188 offset:6144
	ds_read_b128 v[224:227], v188 offset:7168
	global_load_lds_dwordx4 v[180:181], off
	v_lshl_add_u64 v[180:181], s[56:57], 0, v[172:173]
	s_add_i32 m0, s61, 0xe000
	s_nop 0
	global_load_lds_dwordx4 v[180:181], off
	s_waitcnt vmcnt(8)
	s_waitcnt lgkmcnt(0)
	s_barrier
	s_waitcnt lgkmcnt(0)
	v_mfma_scale_f32_16x16x128_f8f6f4 v[158:161], v[26:33], v[192:199], 0, v189, v190 op_sel_hi:[0,0,0]
	v_mfma_scale_f32_16x16x128_f8f6f4 v[154:157], v[18:25], v[192:199], 0, v189, v190 op_sel_hi:[0,0,0]
	v_mfma_scale_f32_16x16x128_f8f6f4 v[150:153], v[26:33], v[200:207], 0, v189, v190 op_sel_hi:[0,0,0]
	v_mfma_scale_f32_16x16x128_f8f6f4 v[142:145], v[18:25], v[200:207], 0, v189, v190 op_sel_hi:[0,0,0]
	v_mfma_scale_f32_16x16x128_f8f6f4 v[134:137], v[26:33], v[208:215], 0, v189, v190 op_sel_hi:[0,0,0]
	v_mfma_scale_f32_16x16x128_f8f6f4 v[126:129], v[18:25], v[208:215], 0, v189, v190 op_sel_hi:[0,0,0]
	v_mfma_scale_f32_16x16x128_f8f6f4 v[118:121], v[26:33], v[220:227], 0, v189, v190 op_sel_hi:[0,0,0]
	v_mfma_scale_f32_16x16x128_f8f6f4 v[110:113], v[18:25], v[220:227], 0, v189, v190 op_sel_hi:[0,0,0]
	v_mfma_scale_f32_16x16x128_f8f6f4 v[146:149], v[10:17], v[192:199], 0, v189, v190 op_sel_hi:[0,0,0]
	v_mfma_scale_f32_16x16x128_f8f6f4 v[138:141], v[2:9], v[192:199], 0, v189, v190 op_sel_hi:[0,0,0]
	v_mfma_scale_f32_16x16x128_f8f6f4 v[130:133], v[10:17], v[200:207], 0, v189, v190 op_sel_hi:[0,0,0]
	v_mfma_scale_f32_16x16x128_f8f6f4 v[122:125], v[2:9], v[200:207], 0, v189, v190 op_sel_hi:[0,0,0]
	v_mfma_scale_f32_16x16x128_f8f6f4 v[114:117], v[10:17], v[208:215], 0, v189, v190 op_sel_hi:[0,0,0]
	v_mfma_scale_f32_16x16x128_f8f6f4 v[106:109], v[2:9], v[208:215], 0, v189, v190 op_sel_hi:[0,0,0]
	v_mfma_scale_f32_16x16x128_f8f6f4 v[102:105], v[10:17], v[220:227], 0, v189, v190 op_sel_hi:[0,0,0]
	v_mfma_scale_f32_16x16x128_f8f6f4 v[98:101], v[2:9], v[220:227], 0, v189, v190 op_sel_hi:[0,0,0]
	s_barrier
	s_add_i32 s80, s69, s33
	v_lshl_add_u64 v[178:179], v[178:179], 0, v[164:165]
	s_mov_b32 m0, s80
	ds_read_b128 v[192:195], v188 offset:16384
	ds_read_b128 v[196:199], v188 offset:17408
	ds_read_b128 v[200:203], v188 offset:18432
	ds_read_b128 v[204:207], v188 offset:19456
	ds_read_b128 v[208:211], v188 offset:20480
	ds_read_b128 v[212:215], v188 offset:21504
	ds_read_b128 v[220:223], v188 offset:22528
	ds_read_b128 v[224:227], v188 offset:23552
	global_load_lds_dwordx4 v[178:179], off
	v_lshl_add_u64 v[180:181], v[178:179], 0, s[10:11]
	s_add_i32 m0, s80, 0x2000
	s_add_i32 s80, s70, s33
	global_load_lds_dwordx4 v[180:181], off
	v_lshl_add_u64 v[180:181], v[178:179], 0, s[12:13]
	s_mov_b32 m0, s80
	v_lshl_add_u64 v[182:183], s[58:59], 0, v[168:169]
	global_load_lds_dwordx4 v[180:181], off
	v_lshl_add_u64 v[180:181], v[178:179], 0, s[14:15]
	s_add_i32 m0, s80, 0x2000
	s_nop 0
	global_load_lds_dwordx4 v[180:181], off
	v_lshl_add_u64 v[180:181], s[58:59], 0, v[166:167]
	s_mov_b32 m0, s61
	s_nop 0
	global_load_lds_dwordx4 v[180:181], off
	s_mov_b32 m0, s62
	s_nop 0
	global_load_lds_dwordx4 v[182:183], off
	s_waitcnt vmcnt(8)
	s_waitcnt lgkmcnt(0)
	s_barrier
	s_waitcnt lgkmcnt(0)
	v_mfma_scale_f32_16x16x128_f8f6f4 v[94:97], v[26:33], v[192:199], 0, v189, v190 op_sel_hi:[0,0,0]
	v_mfma_scale_f32_16x16x128_f8f6f4 v[90:93], v[18:25], v[192:199], 0, v189, v190 op_sel_hi:[0,0,0]
	v_mfma_scale_f32_16x16x128_f8f6f4 v[86:89], v[26:33], v[200:207], 0, v189, v190 op_sel_hi:[0,0,0]
	v_mfma_scale_f32_16x16x128_f8f6f4 v[78:81], v[18:25], v[200:207], 0, v189, v190 op_sel_hi:[0,0,0]
	v_mfma_scale_f32_16x16x128_f8f6f4 v[70:73], v[26:33], v[208:215], 0, v189, v190 op_sel_hi:[0,0,0]
	v_mfma_scale_f32_16x16x128_f8f6f4 v[62:65], v[18:25], v[208:215], 0, v189, v190 op_sel_hi:[0,0,0]
	v_mfma_scale_f32_16x16x128_f8f6f4 v[54:57], v[26:33], v[220:227], 0, v189, v190 op_sel_hi:[0,0,0]
	v_mfma_scale_f32_16x16x128_f8f6f4 v[46:49], v[18:25], v[220:227], 0, v189, v190 op_sel_hi:[0,0,0]
	v_mfma_scale_f32_16x16x128_f8f6f4 v[82:85], v[10:17], v[192:199], 0, v189, v190 op_sel_hi:[0,0,0]
	v_mfma_scale_f32_16x16x128_f8f6f4 v[74:77], v[2:9], v[192:199], 0, v189, v190 op_sel_hi:[0,0,0]
	v_mfma_scale_f32_16x16x128_f8f6f4 v[66:69], v[10:17], v[200:207], 0, v189, v190 op_sel_hi:[0,0,0]
	v_mfma_scale_f32_16x16x128_f8f6f4 v[58:61], v[2:9], v[200:207], 0, v189, v190 op_sel_hi:[0,0,0]
	v_mfma_scale_f32_16x16x128_f8f6f4 v[50:53], v[10:17], v[208:215], 0, v189, v190 op_sel_hi:[0,0,0]
	v_mfma_scale_f32_16x16x128_f8f6f4 v[42:45], v[2:9], v[208:215], 0, v189, v190 op_sel_hi:[0,0,0]
	v_mfma_scale_f32_16x16x128_f8f6f4 v[38:41], v[10:17], v[220:227], 0, v189, v190 op_sel_hi:[0,0,0]
	v_mfma_scale_f32_16x16x128_f8f6f4 v[34:37], v[2:9], v[220:227], 0, v189, v190 op_sel_hi:[0,0,0]
	s_barrier
	s_add_i32 s80, 0, 0x18000
	s_add_i32 s81, 0, 0x1c000
	v_add_u32_e32 v14, s80, v184
	v_add_u32_e32 v30, s81, v184
	ds_read_b128 v[2:5], v14
	ds_read_b128 v[6:9], v14 offset:1024
	ds_read_b128 v[10:13], v14 offset:2048
	ds_read_b128 v[14:17], v14 offset:3072
	ds_read_b128 v[18:21], v30
	ds_read_b128 v[22:25], v30 offset:1024
	ds_read_b128 v[26:29], v30 offset:2048
	ds_read_b128 v[30:33], v30 offset:3072
	s_add_u32 s58, s58, 0xb0000
	s_addc_u32 s59, s59, 0
	s_mov_b32 m0, s63
	v_lshl_add_u64 v[216:217], s[58:59], 0, v[166:167]
	ds_read_b128 v[192:195], v188 offset:32768
	ds_read_b128 v[196:199], v188 offset:33792
	ds_read_b128 v[200:203], v188 offset:34816
	ds_read_b128 v[204:207], v188 offset:35840
	ds_read_b128 v[208:211], v188 offset:36864
	ds_read_b128 v[212:215], v188 offset:37888
	ds_read_b128 v[220:223], v188 offset:38912
	ds_read_b128 v[224:227], v188 offset:39936
	global_load_lds_dwordx4 v[216:217], off
	v_lshl_add_u64 v[216:217], s[58:59], 0, v[168:169]
	s_mov_b32 m0, s64
	s_nop 0
	global_load_lds_dwordx4 v[216:217], off
	s_waitcnt vmcnt(8)
	s_waitcnt lgkmcnt(0)
	s_barrier
	s_waitcnt lgkmcnt(0)
	v_mfma_scale_f32_16x16x128_f8f6f4 v[158:161], v[2:9], v[192:199], v[158:161], v189, v190 op_sel_hi:[0,0,0]
	v_mfma_scale_f32_16x16x128_f8f6f4 v[154:157], v[10:17], v[192:199], v[154:157], v189, v190 op_sel_hi:[0,0,0]
	v_mfma_scale_f32_16x16x128_f8f6f4 v[150:153], v[2:9], v[200:207], v[150:153], v189, v190 op_sel_hi:[0,0,0]
	v_mfma_scale_f32_16x16x128_f8f6f4 v[142:145], v[10:17], v[200:207], v[142:145], v189, v190 op_sel_hi:[0,0,0]
	v_mfma_scale_f32_16x16x128_f8f6f4 v[134:137], v[2:9], v[208:215], v[134:137], v189, v190 op_sel_hi:[0,0,0]
	v_mfma_scale_f32_16x16x128_f8f6f4 v[126:129], v[10:17], v[208:215], v[126:129], v189, v190 op_sel_hi:[0,0,0]
	v_mfma_scale_f32_16x16x128_f8f6f4 v[118:121], v[2:9], v[220:227], v[118:121], v189, v190 op_sel_hi:[0,0,0]
	v_mfma_scale_f32_16x16x128_f8f6f4 v[110:113], v[10:17], v[220:227], v[110:113], v189, v190 op_sel_hi:[0,0,0]
	v_mfma_scale_f32_16x16x128_f8f6f4 v[146:149], v[18:25], v[192:199], v[146:149], v189, v190 op_sel_hi:[0,0,0]
	v_mfma_scale_f32_16x16x128_f8f6f4 v[138:141], v[26:33], v[192:199], v[138:141], v189, v190 op_sel_hi:[0,0,0]
	v_mfma_scale_f32_16x16x128_f8f6f4 v[130:133], v[18:25], v[200:207], v[130:133], v189, v190 op_sel_hi:[0,0,0]
	v_mfma_scale_f32_16x16x128_f8f6f4 v[122:125], v[26:33], v[200:207], v[122:125], v189, v190 op_sel_hi:[0,0,0]
	v_mfma_scale_f32_16x16x128_f8f6f4 v[114:117], v[18:25], v[208:215], v[114:117], v189, v190 op_sel_hi:[0,0,0]
	v_mfma_scale_f32_16x16x128_f8f6f4 v[106:109], v[26:33], v[208:215], v[106:109], v189, v190 op_sel_hi:[0,0,0]
	v_mfma_scale_f32_16x16x128_f8f6f4 v[102:105], v[18:25], v[220:227], v[102:105], v189, v190 op_sel_hi:[0,0,0]
	v_mfma_scale_f32_16x16x128_f8f6f4 v[98:101], v[26:33], v[220:227], v[98:101], v189, v190 op_sel_hi:[0,0,0]
	s_barrier
	s_add_i32 s58, s80, s33
	v_lshl_add_u64 v[216:217], v[178:179], 0, s[24:25]
	s_mov_b32 m0, s58
	ds_read_b128 v[192:195], v188 offset:49152
	ds_read_b128 v[196:199], v188 offset:50176
	ds_read_b128 v[200:203], v188 offset:51200
	ds_read_b128 v[204:207], v188 offset:52224
	ds_read_b128 v[208:211], v188 offset:53248
	ds_read_b128 v[212:215], v188 offset:54272
	ds_read_b128 v[220:223], v188 offset:55296
	ds_read_b128 v[224:227], v188 offset:56320
	global_load_lds_dwordx4 v[216:217], off
	v_lshl_add_u64 v[216:217], v[178:179], 0, s[26:27]
	s_add_i32 m0, s58, 0x2000
	s_add_i32 s58, s81, s33
	global_load_lds_dwordx4 v[216:217], off
	v_lshl_add_u64 v[216:217], v[178:179], 0, s[38:39]
	s_mov_b32 m0, s58
	v_lshl_add_u64 v[178:179], v[178:179], 0, s[40:41]
	global_load_lds_dwordx4 v[216:217], off
	s_add_i32 m0, s58, 0x2000
	s_nop 0
	global_load_lds_dwordx4 v[178:179], off
	v_lshl_add_u64 v[178:179], v[180:181], 0, s[36:37]
	s_mov_b32 m0, s66
	s_nop 0
	global_load_lds_dwordx4 v[178:179], off
	v_lshl_add_u64 v[178:179], v[182:183], 0, s[36:37]
	s_mov_b32 m0, s67
	s_nop 0
	global_load_lds_dwordx4 v[178:179], off
	s_waitcnt vmcnt(8)
	s_waitcnt lgkmcnt(0)
	s_barrier
	s_waitcnt lgkmcnt(0)
	v_mfma_scale_f32_16x16x128_f8f6f4 v[94:97], v[2:9], v[192:199], v[94:97], v189, v190 op_sel_hi:[0,0,0]
	v_mfma_scale_f32_16x16x128_f8f6f4 v[90:93], v[10:17], v[192:199], v[90:93], v189, v190 op_sel_hi:[0,0,0]
	v_mfma_scale_f32_16x16x128_f8f6f4 v[86:89], v[2:9], v[200:207], v[86:89], v189, v190 op_sel_hi:[0,0,0]
	v_mfma_scale_f32_16x16x128_f8f6f4 v[78:81], v[10:17], v[200:207], v[78:81], v189, v190 op_sel_hi:[0,0,0]
	v_mfma_scale_f32_16x16x128_f8f6f4 v[70:73], v[2:9], v[208:215], v[70:73], v189, v190 op_sel_hi:[0,0,0]
	v_mfma_scale_f32_16x16x128_f8f6f4 v[62:65], v[10:17], v[208:215], v[62:65], v189, v190 op_sel_hi:[0,0,0]
	v_mfma_scale_f32_16x16x128_f8f6f4 v[54:57], v[2:9], v[220:227], v[54:57], v189, v190 op_sel_hi:[0,0,0]
	v_mfma_scale_f32_16x16x128_f8f6f4 v[46:49], v[10:17], v[220:227], v[46:49], v189, v190 op_sel_hi:[0,0,0]
	v_mfma_scale_f32_16x16x128_f8f6f4 v[82:85], v[18:25], v[192:199], v[82:85], v189, v190 op_sel_hi:[0,0,0]
	v_mfma_scale_f32_16x16x128_f8f6f4 v[74:77], v[26:33], v[192:199], v[74:77], v189, v190 op_sel_hi:[0,0,0]
	v_mfma_scale_f32_16x16x128_f8f6f4 v[66:69], v[18:25], v[200:207], v[66:69], v189, v190 op_sel_hi:[0,0,0]
	v_mfma_scale_f32_16x16x128_f8f6f4 v[58:61], v[26:33], v[200:207], v[58:61], v189, v190 op_sel_hi:[0,0,0]
	v_mfma_scale_f32_16x16x128_f8f6f4 v[50:53], v[18:25], v[208:215], v[50:53], v189, v190 op_sel_hi:[0,0,0]
	v_mfma_scale_f32_16x16x128_f8f6f4 v[42:45], v[26:33], v[208:215], v[42:45], v189, v190 op_sel_hi:[0,0,0]
	v_mfma_scale_f32_16x16x128_f8f6f4 v[38:41], v[18:25], v[220:227], v[38:41], v189, v190 op_sel_hi:[0,0,0]
	v_mfma_scale_f32_16x16x128_f8f6f4 v[34:37], v[26:33], v[220:227], v[34:37], v189, v190 op_sel_hi:[0,0,0]
	s_barrier
	s_add_i32 s53, s53, 2
	s_add_u32 s56, s56, 0x100
	s_addc_u32 s57, s57, 0
	s_cmp_gt_u32 s53, 41
	v_lshl_add_u64 v[176:177], v[176:177], 0, s[44:45]
